# all GEMM K-loops: the scalar pointer selects and 64-bit per-lane address adds that sat between a barrier's release and the first MFMA of phases 1-3 now execute before that barrier (start-of-segment le
# speedup vs baseline: 1.0026x; 1.0026x over previous
; #define G_STAGE2(bufoff, gbase, v0, v1) do { \
;         __builtin_amdgcn_global_load_lds((const unsigned*)((const char*)(gbase) + (v0)), (LAS unsigned*)(lds + (bufoff) + ldsw), 16, 0, 0); \
;         __builtin_amdgcn_global_load_lds((const unsigned*)((const char*)(gbase) + (v1)), (LAS unsigned*)(lds + (bufoff) + ldsw + 8192), 16, 0, 0); } while (0)
; #define G_LDA(dst, b, h) do { _Pragma("unroll") for (int m = 0; m < 4; ++m) _Pragma("unroll") for (int k = 0; k < 2; ++k) dst[m][k] = *(const LAS bf16x8*)(lds + G_SA(b, h) + aoff + m * 2048 + k * 1024); } while (0)
; #define G_LDB(dst, b, h) do { _Pragma("unroll") for (int n = 0; n < 2; ++n) _Pragma("unroll") for (int k = 0; k < 2; ++k) dst[n][k] = *(const LAS bf16x8*)(lds + G_SB(b, h) + boff + n * 2048 + k * 1024); } while (0)
; #define G_MMA(ai, bj, At, Bt) do { __builtin_amdgcn_s_setprio(1); _Pragma("unroll") for (int m = 0; m < 4; ++m) _Pragma("unroll") for (int n = 0; n < 2; ++n) _Pragma("unroll") for (int k = 0; k < 2; ++k) \
;         acc[ai][bj][m][n] = __builtin_amdgcn_mfma_f32_16x16x32_bf16(Bt[n][k], At[m][k], acc[ai][bj][m][n], 0, 0, 0); __builtin_amdgcn_s_setprio(0); } while (0)
; #define G_BAR __builtin_amdgcn_s_barrier()
; template <bool PERM, class Epi, class Sched>
; __device__ __forceinline__ void gemm_phase(LAS unsigned char* lds, const Sched& S, const Epi& E) {
;     ...
;             const char* a1 = cA + (size_t)(t + 1) * kstep;
;             G_LDB(B0, 0, 0); G_SCHED; G_LDA(At, 0, 0); G_STAGE2(G_SA(1, 1), a1, va10, va11);
;             const char* a2 = last ? nA : cA + (size_t)(t + 2) * kstep; const char* b2 = last ? nB : cB + (size_t)(t + 2) * kstep;
;             if (last) {
;                 if (Sched::GATHER_A) { va00 = na00; va01 = na01; va10 = na10; va11 = na11; vb0 = nb0; vb1 = nb1; hsB = nhsB; }
;                 else if (has_next) G_OFFS(nxt, va00, va01, va10, va11, vb0, vb1, hsB);
;             }
;             const char* a3 = a2 + kstep; const char* b3 = b2 + kstep;
;             G_WAIT_L(8); G_BAR; G_WAIT_L(0); G_MMA(0, 0, At, B0); G_BAR; G_SCHED;
;             G_LDB(B1, 0, 1); G_STAGE2(G_SB(0, 0), b2, vb0, vb1);
;             G_BAR; G_WAIT_L(0); G_MMA(0, 1, At, B1); G_BAR;
;             G_LDA(At, 0, 1); G_STAGE2(G_SA(0, 0), a2, va00, va01);
;             G_BAR; G_WAIT_L(0); G_MMA(1, 0, At, B0); G_BAR; G_SCHED;
;             G_STAGE2(G_SB(0, 1), b2 + hsB, vb0, vb1);
.LBB0_253:
	s_add_u32 s18, s28, 0x80
	s_addc_u32 s19, s29, 0
	s_and_b64 s[8:9], s[8:9], exec
	v_mov_b32_e32 v205, v147
	v_mov_b32_e32 v207, v147
	s_cselect_b32 s19, s69, s19
	s_cselect_b32 s18, s68, s18
	s_cselect_b32 s9, s71, s2
	s_cselect_b32 s8, s70, s1
	s_waitcnt lgkmcnt(8)
	s_barrier
	s_waitcnt lgkmcnt(0)
	s_setprio 1
	s_waitcnt lgkmcnt(0)
	v_mfma_f32_16x16x32_bf16 v[126:129], v[130:133], v[172:175], v[126:129]
	v_mfma_f32_16x16x32_bf16 v[122:125], v[138:141], v[172:175], v[122:125]
	v_mfma_f32_16x16x32_bf16 v[118:121], v[130:133], v[164:167], v[118:121]
	v_mfma_f32_16x16x32_bf16 v[114:117], v[138:141], v[164:167], v[114:117]
	v_mfma_f32_16x16x32_bf16 v[110:113], v[130:133], v[156:159], v[110:113]
	v_mfma_f32_16x16x32_bf16 v[106:109], v[138:141], v[156:159], v[106:109]
	v_mfma_f32_16x16x32_bf16 v[102:105], v[130:133], v[148:151], v[102:105]
	v_mfma_f32_16x16x32_bf16 v[98:101], v[138:141], v[148:151], v[98:101]
	v_mfma_f32_16x16x32_bf16 v[126:129], v[134:137], v[176:179], v[126:129]
	v_mfma_f32_16x16x32_bf16 v[122:125], v[142:145], v[176:179], v[122:125]
	v_mfma_f32_16x16x32_bf16 v[118:121], v[134:137], v[168:171], v[118:121]
	v_mfma_f32_16x16x32_bf16 v[114:117], v[142:145], v[168:171], v[114:117]
	v_mfma_f32_16x16x32_bf16 v[110:113], v[134:137], v[160:163], v[110:113]
	v_mfma_f32_16x16x32_bf16 v[106:109], v[142:145], v[160:163], v[106:109]
	v_mfma_f32_16x16x32_bf16 v[102:105], v[134:137], v[152:155], v[102:105]
	v_mfma_f32_16x16x32_bf16 v[98:101], v[142:145], v[152:155], v[98:101]
	s_setprio 0
	s_barrier
	s_add_i32 s24, 0, 0x14000
	s_mov_b32 m0, s65
	v_add_u32_e32 v192, s24, v1
	ds_read_b128 v[180:183], v192
	ds_read_b128 v[184:187], v192 offset:1024
	ds_read_b128 v[188:191], v192 offset:2048
	ds_read_b128 v[192:195], v192 offset:3072
	global_load_lds_dwordx4 v146, s[8:9]
	s_mov_b32 m0, s73
	v_mov_b32_e32 v209, v147
	global_load_lds_dwordx4 v208, s[8:9]
	v_lshl_add_u64 v[210:211], s[8:9], 0, v[146:147]
	v_lshl_add_u64 v[212:213], s[8:9], 0, v[208:209]
	s_barrier
	s_waitcnt lgkmcnt(0)
	s_setprio 1
	s_waitcnt lgkmcnt(0)
	v_mfma_f32_16x16x32_bf16 v[62:65], v[180:183], v[172:175], v[62:65]
	v_mfma_f32_16x16x32_bf16 v[58:61], v[188:191], v[172:175], v[58:61]
	v_mfma_f32_16x16x32_bf16 v[54:57], v[180:183], v[164:167], v[54:57]
	v_mfma_f32_16x16x32_bf16 v[50:53], v[188:191], v[164:167], v[50:53]
	v_mfma_f32_16x16x32_bf16 v[46:49], v[180:183], v[156:159], v[46:49]
	v_mfma_f32_16x16x32_bf16 v[42:45], v[188:191], v[156:159], v[42:45]
	v_mfma_f32_16x16x32_bf16 v[38:41], v[180:183], v[148:151], v[38:41]
	v_mfma_f32_16x16x32_bf16 v[34:37], v[188:191], v[148:151], v[34:37]
	v_mfma_f32_16x16x32_bf16 v[62:65], v[184:187], v[176:179], v[62:65]
	v_mfma_f32_16x16x32_bf16 v[58:61], v[192:195], v[176:179], v[58:61]
	v_mfma_f32_16x16x32_bf16 v[54:57], v[184:187], v[168:171], v[54:57]
	v_mfma_f32_16x16x32_bf16 v[50:53], v[192:195], v[168:171], v[50:53]
	v_mfma_f32_16x16x32_bf16 v[46:49], v[184:187], v[160:163], v[46:49]
	v_mfma_f32_16x16x32_bf16 v[42:45], v[192:195], v[160:163], v[42:45]
	v_mfma_f32_16x16x32_bf16 v[38:41], v[184:187], v[152:155], v[38:41]
	v_mfma_f32_16x16x32_bf16 v[34:37], v[192:195], v[152:155], v[34:37]
	s_setprio 0
	s_mov_b32 m0, s64
	s_barrier
	ds_read_b128 v[148:151], v199 offset:16384
	ds_read_b128 v[152:155], v199 offset:17408
	ds_read_b128 v[156:159], v199 offset:18432
	ds_read_b128 v[160:163], v199 offset:19456
	ds_read_b128 v[164:167], v199 offset:20480
	ds_read_b128 v[168:171], v199 offset:21504
	ds_read_b128 v[172:175], v199 offset:22528
	ds_read_b128 v[176:179], v199 offset:23552
	global_load_lds_dwordx4 v200, s[18:19]
	s_mov_b32 m0, s75
	v_mov_b32_e32 v201, v147
	global_load_lds_dwordx4 v202, s[18:19]
	v_mov_b32_e32 v203, v147
	v_lshl_add_u64 v[214:215], s[18:19], 0, v[200:201]
	v_lshl_add_u64 v[216:217], s[18:19], 0, v[202:203]
	s_barrier
	s_waitcnt lgkmcnt(0)
	s_setprio 1
	s_waitcnt lgkmcnt(0)
	v_mfma_f32_16x16x32_bf16 v[94:97], v[130:133], v[148:151], v[94:97]
	v_mfma_f32_16x16x32_bf16 v[90:93], v[138:141], v[148:151], v[90:93]
	v_mfma_f32_16x16x32_bf16 v[86:89], v[130:133], v[156:159], v[86:89]
	v_mfma_f32_16x16x32_bf16 v[82:85], v[138:141], v[156:159], v[82:85]
	v_mfma_f32_16x16x32_bf16 v[78:81], v[130:133], v[164:167], v[78:81]
	v_mfma_f32_16x16x32_bf16 v[74:77], v[138:141], v[164:167], v[74:77]
	v_mfma_f32_16x16x32_bf16 v[70:73], v[130:133], v[172:175], v[70:73]
	v_mfma_f32_16x16x32_bf16 v[66:69], v[138:141], v[172:175], v[66:69]
	v_mfma_f32_16x16x32_bf16 v[94:97], v[134:137], v[152:155], v[94:97]
	v_mfma_f32_16x16x32_bf16 v[90:93], v[142:145], v[152:155], v[90:93]
	v_mfma_f32_16x16x32_bf16 v[86:89], v[134:137], v[160:163], v[86:89]
	v_mfma_f32_16x16x32_bf16 v[82:85], v[142:145], v[160:163], v[82:85]
	v_mfma_f32_16x16x32_bf16 v[78:81], v[134:137], v[168:171], v[78:81]
	v_mfma_f32_16x16x32_bf16 v[74:77], v[142:145], v[168:171], v[74:77]
	v_mfma_f32_16x16x32_bf16 v[70:73], v[134:137], v[176:179], v[70:73]
	v_mfma_f32_16x16x32_bf16 v[66:69], v[142:145], v[176:179], v[66:69]
	s_setprio 0
	s_barrier
	s_add_u32 s22, s8, 0x40000
	s_addc_u32 s23, s9, 0
	s_add_i32 s24, s24, s63
	s_mov_b32 m0, s24
	s_nop 0
	global_load_lds_dwordx4 v146, s[22:23]
	s_add_i32 m0, s24, 0x2000
	s_nop 0
	global_load_lds_dwordx4 v208, s[22:23]
	s_cmp_lg_u32 s100, 0
	s_cbranch_scc1 .Lpj_p4s
	s_waitcnt vmcnt(6)
	s_branch .Lpj_p4j

; #define G_STAGE2(bufoff, gbase, v0, v1) do { \
;         __builtin_amdgcn_global_load_lds((const unsigned*)((const char*)(gbase) + (v0)), (LAS unsigned*)(lds + (bufoff) + ldsw), 16, 0, 0); \
;         __builtin_amdgcn_global_load_lds((const unsigned*)((const char*)(gbase) + (v1)), (LAS unsigned*)(lds + (bufoff) + ldsw + 8192), 16, 0, 0); } while (0)
; #define G_LDA(dst, b, h) do { _Pragma("unroll") for (int m = 0; m < 4; ++m) _Pragma("unroll") for (int k = 0; k < 2; ++k) dst[m][k] = *(const LAS bf16x8*)(lds + G_SA(b, h) + aoff + m * 2048 + k * 1024); } while (0)
; #define G_LDB(dst, b, h) do { _Pragma("unroll") for (int n = 0; n < 2; ++n) _Pragma("unroll") for (int k = 0; k < 2; ++k) dst[n][k] = *(const LAS bf16x8*)(lds + G_SB(b, h) + boff + n * 2048 + k * 1024); } while (0)
; #define G_MMA(ai, bj, At, Bt) do { __builtin_amdgcn_s_setprio(1); _Pragma("unroll") for (int m = 0; m < 4; ++m) _Pragma("unroll") for (int n = 0; n < 2; ++n) _Pragma("unroll") for (int k = 0; k < 2; ++k) \
;         acc[ai][bj][m][n] = __builtin_amdgcn_mfma_f32_16x16x32_bf16(Bt[n][k], At[m][k], acc[ai][bj][m][n], 0, 0, 0); __builtin_amdgcn_s_setprio(0); } while (0)
; template <bool PERM, class Epi, class Sched>
; __device__ __forceinline__ void gemm_phase(LAS unsigned char* lds, const Sched& S, const Epi& E) {
;     ...
;             const char* a1 = cA + (size_t)(t + 1) * kstep;
;             G_LDB(B0, 0, 0); G_SCHED; G_LDA(At, 0, 0); G_STAGE2(G_SA(1, 1), a1, va10, va11);
;             const char* a2 = last ? nA : cA + (size_t)(t + 2) * kstep; const char* b2 = last ? nB : cB + (size_t)(t + 2) * kstep;
;             if (last) {
;                 if (Sched::GATHER_A) { va00 = na00; va01 = na01; va10 = na10; va11 = na11; vb0 = nb0; vb1 = nb1; hsB = nhsB; }
;                 else if (has_next) G_OFFS(nxt, va00, va01, va10, va11, vb0, vb1, hsB);
;             }
;             const char* a3 = a2 + kstep; const char* b3 = b2 + kstep;
;             G_WAIT_L(8); G_BAR; G_WAIT_L(0); G_MMA(0, 0, At, B0); G_BAR; G_SCHED;
;             G_LDB(B1, 0, 1); G_STAGE2(G_SB(0, 0), b2, vb0, vb1);
;             G_BAR; G_WAIT_L(0); G_MMA(0, 1, At, B1); G_BAR;
;             G_LDA(At, 0, 1); G_STAGE2(G_SA(0, 0), a2, va00, va01);
;             G_BAR; G_WAIT_L(0); G_MMA(1, 0, At, B0); G_BAR; G_SCHED;
;             G_STAGE2(G_SB(0, 1), b2 + hsB, vb0, vb1);
;             G_WAIT_V(6); G_BAR; G_MMA(1, 1, At, B1); G_BAR;
.LBB0_599:
	s_add_i32 s74, s74, 2
	s_add_u32 s40, s30, 0x80
	s_addc_u32 s41, s31, 0
	s_and_b64 s[22:23], s[22:23], exec
	s_cselect_b32 s23, s9, s41
	s_cselect_b32 s22, s8, s40
	s_cselect_b32 s41, s25, s72
	s_cselect_b32 s40, s24, s70
	s_waitcnt lgkmcnt(8)
	s_barrier
	s_waitcnt lgkmcnt(0)
	s_setprio 1
	s_waitcnt lgkmcnt(0)
	v_mfma_f32_16x16x32_bf16 v[122:125], v[130:133], v[172:175], v[122:125]
	v_mfma_f32_16x16x32_bf16 v[126:129], v[138:141], v[172:175], v[126:129]
	v_mfma_f32_16x16x32_bf16 v[106:109], v[130:133], v[164:167], v[106:109]
	v_mfma_f32_16x16x32_bf16 v[110:113], v[138:141], v[164:167], v[110:113]
	v_mfma_f32_16x16x32_bf16 v[90:93], v[130:133], v[156:159], v[90:93]
	v_mfma_f32_16x16x32_bf16 v[94:97], v[138:141], v[156:159], v[94:97]
	v_mfma_f32_16x16x32_bf16 v[74:77], v[130:133], v[148:151], v[74:77]
	v_mfma_f32_16x16x32_bf16 v[78:81], v[138:141], v[148:151], v[78:81]
	v_mfma_f32_16x16x32_bf16 v[122:125], v[134:137], v[176:179], v[122:125]
	v_mfma_f32_16x16x32_bf16 v[126:129], v[142:145], v[176:179], v[126:129]
	v_mfma_f32_16x16x32_bf16 v[106:109], v[134:137], v[168:171], v[106:109]
	v_mfma_f32_16x16x32_bf16 v[110:113], v[142:145], v[168:171], v[110:113]
	v_mfma_f32_16x16x32_bf16 v[90:93], v[134:137], v[160:163], v[90:93]
	v_mfma_f32_16x16x32_bf16 v[94:97], v[142:145], v[160:163], v[94:97]
	v_mfma_f32_16x16x32_bf16 v[74:77], v[134:137], v[152:155], v[74:77]
	v_mfma_f32_16x16x32_bf16 v[78:81], v[142:145], v[152:155], v[78:81]
	s_setprio 0
	s_barrier
	s_add_i32 s75, 0, 0x14000
	s_mov_b32 m0, s79
	v_add_u32_e32 v181, s75, v1
	ds_read_b128 v[192:195], v181
	ds_read_b128 v[200:203], v181 offset:1024
	ds_read_b128 v[204:207], v181 offset:2048
	ds_read_b128 v[208:211], v181 offset:3072
	global_load_lds_dwordx4 v146, s[40:41]
	s_mov_b32 m0, s81
	v_mov_b32_e32 v189, v147
	global_load_lds_dwordx4 v188, s[40:41]
	v_lshl_add_u64 v[212:213], s[40:41], 0, v[146:147]
	v_lshl_add_u64 v[214:215], s[40:41], 0, v[188:189]
	s_barrier
	s_waitcnt lgkmcnt(0)
	s_setprio 1
	s_waitcnt lgkmcnt(0)
	v_mfma_f32_16x16x32_bf16 v[118:121], v[192:195], v[172:175], v[118:121]
	v_mfma_f32_16x16x32_bf16 v[114:117], v[204:207], v[172:175], v[114:117]
	v_mfma_f32_16x16x32_bf16 v[102:105], v[192:195], v[164:167], v[102:105]
	v_mfma_f32_16x16x32_bf16 v[98:101], v[204:207], v[164:167], v[98:101]
	v_mfma_f32_16x16x32_bf16 v[86:89], v[192:195], v[156:159], v[86:89]
	v_mfma_f32_16x16x32_bf16 v[82:85], v[204:207], v[156:159], v[82:85]
	v_mfma_f32_16x16x32_bf16 v[70:73], v[192:195], v[148:151], v[70:73]
	v_mfma_f32_16x16x32_bf16 v[66:69], v[204:207], v[148:151], v[66:69]
	v_mfma_f32_16x16x32_bf16 v[118:121], v[200:203], v[176:179], v[118:121]
	v_mfma_f32_16x16x32_bf16 v[114:117], v[208:211], v[176:179], v[114:117]
	v_mfma_f32_16x16x32_bf16 v[102:105], v[200:203], v[168:171], v[102:105]
	v_mfma_f32_16x16x32_bf16 v[98:101], v[208:211], v[168:171], v[98:101]
	v_mfma_f32_16x16x32_bf16 v[86:89], v[200:203], v[160:163], v[86:89]
	v_mfma_f32_16x16x32_bf16 v[82:85], v[208:211], v[160:163], v[82:85]
	v_mfma_f32_16x16x32_bf16 v[70:73], v[200:203], v[152:155], v[70:73]
	v_mfma_f32_16x16x32_bf16 v[66:69], v[208:211], v[152:155], v[66:69]
	s_setprio 0
	s_mov_b32 m0, s73
	s_barrier
	ds_read_b128 v[148:151], v190 offset:16384
	ds_read_b128 v[152:155], v190 offset:17408
	ds_read_b128 v[156:159], v190 offset:18432
	ds_read_b128 v[160:163], v190 offset:19456
	ds_read_b128 v[164:167], v190 offset:20480
	ds_read_b128 v[168:171], v190 offset:21504
	ds_read_b128 v[172:175], v190 offset:22528
	ds_read_b128 v[176:179], v190 offset:23552
	global_load_lds_dwordx4 v180, s[22:23]
	s_mov_b32 m0, s83
	v_mov_b32_e32 v181, v147
	global_load_lds_dwordx4 v182, s[22:23]
	v_mov_b32_e32 v183, v147
	v_lshl_add_u64 v[216:217], s[22:23], 0, v[180:181]
	v_lshl_add_u64 v[218:219], s[22:23], 0, v[182:183]
	s_barrier
	s_waitcnt lgkmcnt(0)
	s_setprio 1
	s_waitcnt lgkmcnt(0)
	v_mfma_f32_16x16x32_bf16 v[58:61], v[130:133], v[148:151], v[58:61]
	v_mfma_f32_16x16x32_bf16 v[62:65], v[138:141], v[148:151], v[62:65]
	v_mfma_f32_16x16x32_bf16 v[42:45], v[130:133], v[156:159], v[42:45]
	v_mfma_f32_16x16x32_bf16 v[46:49], v[138:141], v[156:159], v[46:49]
	v_mfma_f32_16x16x32_bf16 v[26:29], v[130:133], v[164:167], v[26:29]
	v_mfma_f32_16x16x32_bf16 v[30:33], v[138:141], v[164:167], v[30:33]
	v_mfma_f32_16x16x32_bf16 v[2:5], v[130:133], v[172:175], v[2:5]
	v_mfma_f32_16x16x32_bf16 v[6:9], v[138:141], v[172:175], v[6:9]
	v_mfma_f32_16x16x32_bf16 v[58:61], v[134:137], v[152:155], v[58:61]
	v_mfma_f32_16x16x32_bf16 v[62:65], v[142:145], v[152:155], v[62:65]
	v_mfma_f32_16x16x32_bf16 v[42:45], v[134:137], v[160:163], v[42:45]
	v_mfma_f32_16x16x32_bf16 v[46:49], v[142:145], v[160:163], v[46:49]
	v_mfma_f32_16x16x32_bf16 v[26:29], v[134:137], v[168:171], v[26:29]
	v_mfma_f32_16x16x32_bf16 v[30:33], v[142:145], v[168:171], v[30:33]
	v_mfma_f32_16x16x32_bf16 v[2:5], v[134:137], v[176:179], v[2:5]
	v_mfma_f32_16x16x32_bf16 v[6:9], v[142:145], v[176:179], v[6:9]
	s_setprio 0
	s_barrier
	s_add_u32 s40, s40, s44
	s_addc_u32 s41, s41, s45
	s_add_i32 s75, s75, s29
	s_mov_b32 m0, s75
	v_lshl_add_u64 v[220:221], s[40:41], 0, v[146:147]
	global_load_lds_dwordx4 v146, s[40:41]
	s_add_i32 m0, s75, 0x2000
	v_lshl_add_u64 v[222:223], s[40:41], 0, v[188:189]
	global_load_lds_dwordx4 v188, s[40:41]
	s_waitcnt vmcnt(6)
	s_barrier
; #define G_STAGE2(bufoff, gbase, v0, v1) do { \
;         __builtin_amdgcn_global_load_lds((const unsigned*)((const char*)(gbase) + (v0)), (LAS unsigned*)(lds + (bufoff) + ldsw), 16, 0, 0); \
;         __builtin_amdgcn_global_load_lds((const unsigned*)((const char*)(gbase) + (v1)), (LAS unsigned*)(lds + (bufoff) + ldsw + 8192), 16, 0, 0); } while (0)
; #define G_LDA(dst, b, h) do { _Pragma("unroll") for (int m = 0; m < 4; ++m) _Pragma("unroll") for (int k = 0; k < 2; ++k) dst[m][k] = *(const LAS bf16x8*)(lds + G_SA(b, h) + aoff + m * 2048 + k * 1024); } while (0)
; #define G_LDB(dst, b, h) do { _Pragma("unroll") for (int n = 0; n < 2; ++n) _Pragma("unroll") for (int k = 0; k < 2; ++k) dst[n][k] = *(const LAS bf16x8*)(lds + G_SB(b, h) + boff + n * 2048 + k * 1024); } while (0)
; #define G_MMA(ai, bj, At, Bt) do { __builtin_amdgcn_s_setprio(1); _Pragma("unroll") for (int m = 0; m < 4; ++m) _Pragma("unroll") for (int n = 0; n < 2; ++n) _Pragma("unroll") for (int k = 0; k < 2; ++k) \
;         acc[ai][bj][m][n] = __builtin_amdgcn_mfma_f32_16x16x32_bf16(Bt[n][k], At[m][k], acc[ai][bj][m][n], 0, 0, 0); __builtin_amdgcn_s_setprio(0); } while (0)
; #define G_WAIT_V(n) asm volatile("s_waitcnt vmcnt(" #n ")" ::: "memory")
; #define G_WAIT_L(n) asm volatile("s_waitcnt lgkmcnt(" #n ")" ::: "memory")
; #define G_BAR __builtin_amdgcn_s_barrier()
; #define G_SCHED __builtin_amdgcn_sched_barrier(0)
; template <bool PERM, class Epi, class Sched>
; __device__ __forceinline__ void gemm_phase(LAS unsigned char* lds, const Sched& S, const Epi& E) {
;     ...
;             G_WAIT_V(6); G_BAR; G_MMA(1, 1, At, B1); G_BAR;
;             G_LDB(B0, 1, 0); G_SCHED; G_LDA(At, 1, 0); G_STAGE2(G_SA(0, 1), a2, va10, va11);
;             G_WAIT_L(8); G_BAR; G_WAIT_L(0); G_MMA(0, 0, At, B0); G_BAR; G_SCHED;
;             G_LDB(B1, 1, 1); G_STAGE2(G_SB(1, 0), b3, vb0, vb1);
;             G_BAR; G_WAIT_L(0); G_MMA(0, 1, At, B1); G_BAR;
	s_setprio 1
	v_mfma_f32_16x16x32_bf16 v[54:57], v[192:195], v[148:151], v[54:57]
	v_mfma_f32_16x16x32_bf16 v[50:53], v[204:207], v[148:151], v[50:53]
	v_mfma_f32_16x16x32_bf16 v[38:41], v[192:195], v[156:159], v[38:41]
	v_mfma_f32_16x16x32_bf16 v[34:37], v[204:207], v[156:159], v[34:37]
	v_mfma_f32_16x16x32_bf16 v[14:17], v[192:195], v[164:167], v[14:17]
	v_mfma_f32_16x16x32_bf16 v[10:13], v[204:207], v[164:167], v[10:13]
	v_mfma_f32_16x16x32_bf16 v[22:25], v[192:195], v[172:175], v[22:25]
	v_mfma_f32_16x16x32_bf16 v[18:21], v[204:207], v[172:175], v[18:21]
	v_mfma_f32_16x16x32_bf16 v[54:57], v[200:203], v[152:155], v[54:57]
	v_mfma_f32_16x16x32_bf16 v[50:53], v[208:211], v[152:155], v[50:53]
	v_mfma_f32_16x16x32_bf16 v[38:41], v[200:203], v[160:163], v[38:41]
	v_mfma_f32_16x16x32_bf16 v[34:37], v[208:211], v[160:163], v[34:37]
	v_mfma_f32_16x16x32_bf16 v[14:17], v[200:203], v[168:171], v[14:17]
	v_mfma_f32_16x16x32_bf16 v[10:13], v[208:211], v[168:171], v[10:13]
	v_mfma_f32_16x16x32_bf16 v[22:25], v[200:203], v[176:179], v[22:25]
	v_mfma_f32_16x16x32_bf16 v[18:21], v[208:211], v[176:179], v[18:21]
	s_setprio 0
	s_add_i32 s40, 0, 0x18000
	v_add_u32_e32 v142, s40, v1
	s_barrier
	ds_read_b128 v[130:133], v142
	ds_read_b128 v[134:137], v142 offset:1024
	ds_read_b128 v[138:141], v142 offset:2048
	ds_read_b128 v[142:145], v142 offset:3072
	s_mov_b32 m0, s85
	v_lshl_add_u64 v[192:193], s[22:23], 0, v[184:185]
	ds_read_b128 v[148:151], v190 offset:32768
	ds_read_b128 v[152:155], v190 offset:33792
	ds_read_b128 v[156:159], v190 offset:34816
	ds_read_b128 v[160:163], v190 offset:35840
	ds_read_b128 v[164:167], v190 offset:36864
	ds_read_b128 v[168:171], v190 offset:37888
	ds_read_b128 v[172:175], v190 offset:38912
	ds_read_b128 v[176:179], v190 offset:39936
	global_load_lds_dwordx4 v[192:193], off
	v_lshl_add_u64 v[192:193], s[22:23], 0, v[186:187]
	s_mov_b32 m0, s87
	s_nop 0
	global_load_lds_dwordx4 v[192:193], off
	s_waitcnt lgkmcnt(8)
	s_barrier
	s_waitcnt lgkmcnt(0)
	s_setprio 1
	s_waitcnt lgkmcnt(0)
	v_mfma_f32_16x16x32_bf16 v[122:125], v[130:133], v[148:151], v[122:125]
	v_mfma_f32_16x16x32_bf16 v[126:129], v[138:141], v[148:151], v[126:129]
	v_mfma_f32_16x16x32_bf16 v[106:109], v[130:133], v[156:159], v[106:109]
	v_mfma_f32_16x16x32_bf16 v[110:113], v[138:141], v[156:159], v[110:113]
	v_mfma_f32_16x16x32_bf16 v[90:93], v[130:133], v[164:167], v[90:93]
	v_mfma_f32_16x16x32_bf16 v[94:97], v[138:141], v[164:167], v[94:97]
	v_mfma_f32_16x16x32_bf16 v[74:77], v[130:133], v[172:175], v[74:77]
	v_mfma_f32_16x16x32_bf16 v[78:81], v[138:141], v[172:175], v[78:81]
	v_mfma_f32_16x16x32_bf16 v[122:125], v[134:137], v[152:155], v[122:125]
	v_mfma_f32_16x16x32_bf16 v[126:129], v[142:145], v[152:155], v[126:129]
	v_mfma_f32_16x16x32_bf16 v[106:109], v[134:137], v[160:163], v[106:109]
	v_mfma_f32_16x16x32_bf16 v[110:113], v[142:145], v[160:163], v[110:113]
	v_mfma_f32_16x16x32_bf16 v[90:93], v[134:137], v[168:171], v[90:93]
	v_mfma_f32_16x16x32_bf16 v[94:97], v[142:145], v[168:171], v[94:97]
	v_mfma_f32_16x16x32_bf16 v[74:77], v[134:137], v[176:179], v[74:77]
	v_mfma_f32_16x16x32_bf16 v[78:81], v[142:145], v[176:179], v[78:81]
	s_setprio 0
	s_barrier
	s_add_i32 s22, 0, 0x1c000
	s_add_i32 s23, s40, s29
	v_add_u32_e32 v181, s22, v1
	v_lshl_add_u64 v[212:213], v[212:213], 0, s[34:35]
	s_mov_b32 m0, s23
	ds_read_b128 v[192:195], v181
	ds_read_b128 v[200:203], v181 offset:1024
	ds_read_b128 v[204:207], v181 offset:2048
	ds_read_b128 v[208:211], v181 offset:3072
	global_load_lds_dwordx4 v[212:213], off
	v_lshl_add_u64 v[212:213], v[214:215], 0, s[34:35]
	s_add_i32 m0, s23, 0x2000
	s_nop 0
	global_load_lds_dwordx4 v[212:213], off
	s_barrier
; #define G_STAGE2(bufoff, gbase, v0, v1) do { \
;         __builtin_amdgcn_global_load_lds((const unsigned*)((const char*)(gbase) + (v0)), (LAS unsigned*)(lds + (bufoff) + ldsw), 16, 0, 0); \
;         __builtin_amdgcn_global_load_lds((const unsigned*)((const char*)(gbase) + (v1)), (LAS unsigned*)(lds + (bufoff) + ldsw + 8192), 16, 0, 0); } while (0)
; #define G_LDA(dst, b, h) do { _Pragma("unroll") for (int m = 0; m < 4; ++m) _Pragma("unroll") for (int k = 0; k < 2; ++k) dst[m][k] = *(const LAS bf16x8*)(lds + G_SA(b, h) + aoff + m * 2048 + k * 1024); } while (0)
; #define G_MMA(ai, bj, At, Bt) do { __builtin_amdgcn_s_setprio(1); _Pragma("unroll") for (int m = 0; m < 4; ++m) _Pragma("unroll") for (int n = 0; n < 2; ++n) _Pragma("unroll") for (int k = 0; k < 2; ++k) \
;         acc[ai][bj][m][n] = __builtin_amdgcn_mfma_f32_16x16x32_bf16(Bt[n][k], At[m][k], acc[ai][bj][m][n], 0, 0, 0); __builtin_amdgcn_s_setprio(0); } while (0)
; #define G_WAIT_V(n) asm volatile("s_waitcnt vmcnt(" #n ")" ::: "memory")
; #define G_WAIT_L(n) asm volatile("s_waitcnt lgkmcnt(" #n ")" ::: "memory")
; #define G_BAR __builtin_amdgcn_s_barrier()
; #define G_SCHED __builtin_amdgcn_sched_barrier(0)
; template <bool PERM, class Epi, class Sched>
; __device__ __forceinline__ void gemm_phase(LAS unsigned char* lds, const Sched& S, const Epi& E) {
;     ...
;             G_BAR; G_WAIT_L(0); G_MMA(0, 1, At, B1); G_BAR;
;             G_LDA(At, 1, 1); G_STAGE2(G_SA(1, 0), a3, va00, va01);
;             G_BAR; G_WAIT_L(0); G_MMA(1, 0, At, B0); G_BAR; G_SCHED;
;             G_STAGE2(G_SB(1, 1), b3 + hsB, vb0, vb1);
;             G_WAIT_V(6); G_BAR; G_MMA(1, 1, At, B1); G_BAR;
	s_waitcnt lgkmcnt(0)
	s_setprio 1
	s_waitcnt lgkmcnt(0)
	v_mfma_f32_16x16x32_bf16 v[118:121], v[192:195], v[148:151], v[118:121]
	v_mfma_f32_16x16x32_bf16 v[114:117], v[204:207], v[148:151], v[114:117]
	v_mfma_f32_16x16x32_bf16 v[102:105], v[192:195], v[156:159], v[102:105]
	v_mfma_f32_16x16x32_bf16 v[98:101], v[204:207], v[156:159], v[98:101]
	v_mfma_f32_16x16x32_bf16 v[86:89], v[192:195], v[164:167], v[86:89]
	v_mfma_f32_16x16x32_bf16 v[82:85], v[204:207], v[164:167], v[82:85]
	v_mfma_f32_16x16x32_bf16 v[70:73], v[192:195], v[172:175], v[70:73]
	v_mfma_f32_16x16x32_bf16 v[66:69], v[204:207], v[172:175], v[66:69]
	v_mfma_f32_16x16x32_bf16 v[118:121], v[200:203], v[152:155], v[118:121]
	v_mfma_f32_16x16x32_bf16 v[114:117], v[208:211], v[152:155], v[114:117]
	v_mfma_f32_16x16x32_bf16 v[102:105], v[200:203], v[160:163], v[102:105]
	v_mfma_f32_16x16x32_bf16 v[98:101], v[208:211], v[160:163], v[98:101]
	v_mfma_f32_16x16x32_bf16 v[86:89], v[200:203], v[168:171], v[86:89]
	v_mfma_f32_16x16x32_bf16 v[82:85], v[208:211], v[168:171], v[82:85]
	v_mfma_f32_16x16x32_bf16 v[70:73], v[200:203], v[176:179], v[70:73]
	v_mfma_f32_16x16x32_bf16 v[66:69], v[208:211], v[176:179], v[66:69]
	s_setprio 0
	s_mov_b32 m0, s89
	v_lshl_add_u64 v[212:213], v[216:217], 0, s[34:35]
	s_barrier
	ds_read_b128 v[148:151], v190 offset:49152
	ds_read_b128 v[152:155], v190 offset:50176
	ds_read_b128 v[156:159], v190 offset:51200
	ds_read_b128 v[160:163], v190 offset:52224
	ds_read_b128 v[164:167], v190 offset:53248
	ds_read_b128 v[168:171], v190 offset:54272
	ds_read_b128 v[172:175], v190 offset:55296
	ds_read_b128 v[176:179], v190 offset:56320
	global_load_lds_dwordx4 v[212:213], off
	v_lshl_add_u64 v[212:213], v[218:219], 0, s[34:35]
	s_mov_b32 m0, s90
	s_nop 0
	global_load_lds_dwordx4 v[212:213], off
	s_barrier
	s_waitcnt lgkmcnt(0)
	s_setprio 1
	s_waitcnt lgkmcnt(0)
	v_mfma_f32_16x16x32_bf16 v[58:61], v[130:133], v[148:151], v[58:61]
	v_mfma_f32_16x16x32_bf16 v[62:65], v[138:141], v[148:151], v[62:65]
	v_mfma_f32_16x16x32_bf16 v[42:45], v[130:133], v[156:159], v[42:45]
	v_mfma_f32_16x16x32_bf16 v[46:49], v[138:141], v[156:159], v[46:49]
	v_mfma_f32_16x16x32_bf16 v[26:29], v[130:133], v[164:167], v[26:29]
	v_mfma_f32_16x16x32_bf16 v[30:33], v[138:141], v[164:167], v[30:33]
	v_mfma_f32_16x16x32_bf16 v[2:5], v[130:133], v[172:175], v[2:5]
	v_mfma_f32_16x16x32_bf16 v[6:9], v[138:141], v[172:175], v[6:9]
	v_mfma_f32_16x16x32_bf16 v[58:61], v[134:137], v[152:155], v[58:61]
	v_mfma_f32_16x16x32_bf16 v[62:65], v[142:145], v[152:155], v[62:65]
	v_mfma_f32_16x16x32_bf16 v[42:45], v[134:137], v[160:163], v[42:45]
	v_mfma_f32_16x16x32_bf16 v[46:49], v[142:145], v[160:163], v[46:49]
	v_mfma_f32_16x16x32_bf16 v[26:29], v[134:137], v[168:171], v[26:29]
	v_mfma_f32_16x16x32_bf16 v[30:33], v[142:145], v[168:171], v[30:33]
	v_mfma_f32_16x16x32_bf16 v[2:5], v[134:137], v[176:179], v[2:5]
	v_mfma_f32_16x16x32_bf16 v[6:9], v[142:145], v[176:179], v[6:9]
	s_setprio 0
	s_barrier
	s_add_i32 s22, s22, s29
	v_lshl_add_u64 v[130:131], v[220:221], 0, s[34:35]
	s_mov_b32 m0, s22
	s_nop 0
	global_load_lds_dwordx4 v[130:131], off
	v_lshl_add_u64 v[130:131], v[222:223], 0, s[34:35]
	s_add_i32 m0, s22, 0x2000
	s_nop 0
	global_load_lds_dwordx4 v[130:131], off
	s_waitcnt vmcnt(6)
	s_barrier
	s_setprio 1
	v_mfma_f32_16x16x32_bf16 v[54:57], v[192:195], v[148:151], v[54:57]
	v_mfma_f32_16x16x32_bf16 v[50:53], v[204:207], v[148:151], v[50:53]
	v_mfma_f32_16x16x32_bf16 v[38:41], v[192:195], v[156:159], v[38:41]
	v_mfma_f32_16x16x32_bf16 v[34:37], v[204:207], v[156:159], v[34:37]
	v_mfma_f32_16x16x32_bf16 v[14:17], v[192:195], v[164:167], v[14:17]
	v_mfma_f32_16x16x32_bf16 v[10:13], v[204:207], v[164:167], v[10:13]
	v_mfma_f32_16x16x32_bf16 v[22:25], v[192:195], v[172:175], v[22:25]
	v_mfma_f32_16x16x32_bf16 v[18:21], v[204:207], v[172:175], v[18:21]
	v_mfma_f32_16x16x32_bf16 v[54:57], v[200:203], v[152:155], v[54:57]
	v_mfma_f32_16x16x32_bf16 v[50:53], v[208:211], v[152:155], v[50:53]
	v_mfma_f32_16x16x32_bf16 v[38:41], v[200:203], v[160:163], v[38:41]
	v_mfma_f32_16x16x32_bf16 v[34:37], v[208:211], v[160:163], v[34:37]
	v_mfma_f32_16x16x32_bf16 v[14:17], v[200:203], v[168:171], v[14:17]
	v_mfma_f32_16x16x32_bf16 v[10:13], v[208:211], v[168:171], v[10:13]
	v_mfma_f32_16x16x32_bf16 v[22:25], v[200:203], v[176:179], v[22:25]
	v_mfma_f32_16x16x32_bf16 v[18:21], v[208:211], v[176:179], v[18:21]
	s_setprio 0
	s_add_u32 s30, s30, 0x100
	s_addc_u32 s31, s31, 0
	s_add_u32 s70, s70, 0x100
	s_addc_u32 s72, s72, 0
	s_cmp_ge_i32 s74, s43
	s_barrier
	s_cbranch_scc1 .LBB0_602

; #define G_STAGE2(bufoff, gbase, v0, v1) do { \
;         __builtin_amdgcn_global_load_lds((const unsigned*)((const char*)(gbase) + (v0)), (LAS unsigned*)(lds + (bufoff) + ldsw), 16, 0, 0); \
;         __builtin_amdgcn_global_load_lds((const unsigned*)((const char*)(gbase) + (v1)), (LAS unsigned*)(lds + (bufoff) + ldsw + 8192), 16, 0, 0); } while (0)
; #define G_LDA(dst, b, h) do { _Pragma("unroll") for (int m = 0; m < 4; ++m) _Pragma("unroll") for (int k = 0; k < 2; ++k) dst[m][k] = *(const LAS bf16x8*)(lds + G_SA(b, h) + aoff + m * 2048 + k * 1024); } while (0)
; #define G_LDB(dst, b, h) do { _Pragma("unroll") for (int n = 0; n < 2; ++n) _Pragma("unroll") for (int k = 0; k < 2; ++k) dst[n][k] = *(const LAS bf16x8*)(lds + G_SB(b, h) + boff + n * 2048 + k * 1024); } while (0)
; #define G_MMA(ai, bj, At, Bt) do { __builtin_amdgcn_s_setprio(1); _Pragma("unroll") for (int m = 0; m < 4; ++m) _Pragma("unroll") for (int n = 0; n < 2; ++n) _Pragma("unroll") for (int k = 0; k < 2; ++k) \
;         acc[ai][bj][m][n] = __builtin_amdgcn_mfma_f32_16x16x32_bf16(Bt[n][k], At[m][k], acc[ai][bj][m][n], 0, 0, 0); __builtin_amdgcn_s_setprio(0); } while (0)
; template <bool PERM, class Epi, class Sched>
; __device__ __forceinline__ void gemm_phase(LAS unsigned char* lds, const Sched& S, const Epi& E) {
;     ...
;             const char* a1 = cA + (size_t)(t + 1) * kstep;
;             G_LDB(B0, 0, 0); G_SCHED; G_LDA(At, 0, 0); G_STAGE2(G_SA(1, 1), a1, va10, va11);
;             const char* a2 = last ? nA : cA + (size_t)(t + 2) * kstep; const char* b2 = last ? nB : cB + (size_t)(t + 2) * kstep;
;             if (last) {
;                 if (Sched::GATHER_A) { va00 = na00; va01 = na01; va10 = na10; va11 = na11; vb0 = nb0; vb1 = nb1; hsB = nhsB; }
;                 else if (has_next) G_OFFS(nxt, va00, va01, va10, va11, vb0, vb1, hsB);
;             }
;             const char* a3 = a2 + kstep; const char* b3 = b2 + kstep;
;             G_WAIT_L(8); G_BAR; G_WAIT_L(0); G_MMA(0, 0, At, B0); G_BAR; G_SCHED;
;             G_LDB(B1, 0, 1); G_STAGE2(G_SB(0, 0), b2, vb0, vb1);
;             G_BAR; G_WAIT_L(0); G_MMA(0, 1, At, B1); G_BAR;
;             G_LDA(At, 0, 1); G_STAGE2(G_SA(0, 0), a2, va00, va01);
;             G_BAR; G_WAIT_L(0); G_MMA(1, 0, At, B0); G_BAR; G_SCHED;
;             G_STAGE2(G_SB(0, 1), b2 + hsB, vb0, vb1);
;             G_WAIT_V(6); G_BAR; G_MMA(1, 1, At, B1); G_BAR;
.LBB0_733:
	s_add_i32 s74, s74, 2
	s_add_u32 s30, s28, 0x80
	s_addc_u32 s31, s29, 0
	s_and_b64 s[22:23], s[22:23], exec
	s_cselect_b32 s23, s19, s31
	s_cselect_b32 s22, s18, s30
	s_cselect_b32 s31, s25, s64
	s_cselect_b32 s30, s24, s43
	s_waitcnt lgkmcnt(8)
	s_barrier
	s_waitcnt lgkmcnt(0)
	s_setprio 1
	s_waitcnt lgkmcnt(0)
	v_mfma_f32_16x16x32_bf16 v[122:125], v[130:133], v[172:175], v[122:125]
	v_mfma_f32_16x16x32_bf16 v[126:129], v[138:141], v[172:175], v[126:129]
	v_mfma_f32_16x16x32_bf16 v[106:109], v[130:133], v[164:167], v[106:109]
	v_mfma_f32_16x16x32_bf16 v[110:113], v[138:141], v[164:167], v[110:113]
	v_mfma_f32_16x16x32_bf16 v[90:93], v[130:133], v[156:159], v[90:93]
	v_mfma_f32_16x16x32_bf16 v[94:97], v[138:141], v[156:159], v[94:97]
	v_mfma_f32_16x16x32_bf16 v[74:77], v[130:133], v[148:151], v[74:77]
	v_mfma_f32_16x16x32_bf16 v[78:81], v[138:141], v[148:151], v[78:81]
	v_mfma_f32_16x16x32_bf16 v[122:125], v[134:137], v[176:179], v[122:125]
	v_mfma_f32_16x16x32_bf16 v[126:129], v[142:145], v[176:179], v[126:129]
	v_mfma_f32_16x16x32_bf16 v[106:109], v[134:137], v[168:171], v[106:109]
	v_mfma_f32_16x16x32_bf16 v[110:113], v[142:145], v[168:171], v[110:113]
	v_mfma_f32_16x16x32_bf16 v[90:93], v[134:137], v[160:163], v[90:93]
	v_mfma_f32_16x16x32_bf16 v[94:97], v[142:145], v[160:163], v[94:97]
	v_mfma_f32_16x16x32_bf16 v[74:77], v[134:137], v[152:155], v[74:77]
	v_mfma_f32_16x16x32_bf16 v[78:81], v[142:145], v[152:155], v[78:81]
	s_setprio 0
	s_barrier
	s_add_i32 s76, 0, 0x14000
	s_mov_b32 m0, s63
	v_add_u32_e32 v181, s76, v1
	ds_read_b128 v[192:195], v181
	ds_read_b128 v[200:203], v181 offset:1024
	ds_read_b128 v[204:207], v181 offset:2048
	ds_read_b128 v[208:211], v181 offset:3072
	global_load_lds_dwordx4 v146, s[30:31]
	s_mov_b32 m0, s65
	v_mov_b32_e32 v189, v147
	global_load_lds_dwordx4 v188, s[30:31]
	v_lshl_add_u64 v[212:213], s[30:31], 0, v[146:147]
	v_lshl_add_u64 v[214:215], s[30:31], 0, v[188:189]
	s_barrier
	s_waitcnt lgkmcnt(0)
	s_setprio 1
	s_waitcnt lgkmcnt(0)
	v_mfma_f32_16x16x32_bf16 v[118:121], v[192:195], v[172:175], v[118:121]
	v_mfma_f32_16x16x32_bf16 v[114:117], v[204:207], v[172:175], v[114:117]
	v_mfma_f32_16x16x32_bf16 v[102:105], v[192:195], v[164:167], v[102:105]
	v_mfma_f32_16x16x32_bf16 v[98:101], v[204:207], v[164:167], v[98:101]
	v_mfma_f32_16x16x32_bf16 v[86:89], v[192:195], v[156:159], v[86:89]
	v_mfma_f32_16x16x32_bf16 v[82:85], v[204:207], v[156:159], v[82:85]
	v_mfma_f32_16x16x32_bf16 v[70:73], v[192:195], v[148:151], v[70:73]
	v_mfma_f32_16x16x32_bf16 v[66:69], v[204:207], v[148:151], v[66:69]
	v_mfma_f32_16x16x32_bf16 v[118:121], v[200:203], v[176:179], v[118:121]
	v_mfma_f32_16x16x32_bf16 v[114:117], v[208:211], v[176:179], v[114:117]
	v_mfma_f32_16x16x32_bf16 v[102:105], v[200:203], v[168:171], v[102:105]
	v_mfma_f32_16x16x32_bf16 v[98:101], v[208:211], v[168:171], v[98:101]
	v_mfma_f32_16x16x32_bf16 v[86:89], v[200:203], v[160:163], v[86:89]
	v_mfma_f32_16x16x32_bf16 v[82:85], v[208:211], v[160:163], v[82:85]
	v_mfma_f32_16x16x32_bf16 v[70:73], v[200:203], v[152:155], v[70:73]
	v_mfma_f32_16x16x32_bf16 v[66:69], v[208:211], v[152:155], v[66:69]
	s_setprio 0
	s_mov_b32 m0, s62
	s_barrier
	ds_read_b128 v[148:151], v190 offset:16384
	ds_read_b128 v[152:155], v190 offset:17408
	ds_read_b128 v[156:159], v190 offset:18432
	ds_read_b128 v[160:163], v190 offset:19456
	ds_read_b128 v[164:167], v190 offset:20480
	ds_read_b128 v[168:171], v190 offset:21504
	ds_read_b128 v[172:175], v190 offset:22528
	ds_read_b128 v[176:179], v190 offset:23552
	global_load_lds_dwordx4 v180, s[22:23]
	s_mov_b32 m0, s0
	v_mov_b32_e32 v181, v147
	global_load_lds_dwordx4 v182, s[22:23]
	v_mov_b32_e32 v183, v147
	v_lshl_add_u64 v[216:217], s[22:23], 0, v[180:181]
	v_lshl_add_u64 v[218:219], s[22:23], 0, v[182:183]
	s_barrier
	s_waitcnt lgkmcnt(0)
	s_setprio 1
	s_waitcnt lgkmcnt(0)
	v_mfma_f32_16x16x32_bf16 v[58:61], v[130:133], v[148:151], v[58:61]
	v_mfma_f32_16x16x32_bf16 v[62:65], v[138:141], v[148:151], v[62:65]
	v_mfma_f32_16x16x32_bf16 v[42:45], v[130:133], v[156:159], v[42:45]
	v_mfma_f32_16x16x32_bf16 v[46:49], v[138:141], v[156:159], v[46:49]
	v_mfma_f32_16x16x32_bf16 v[26:29], v[130:133], v[164:167], v[26:29]
	v_mfma_f32_16x16x32_bf16 v[30:33], v[138:141], v[164:167], v[30:33]
	v_mfma_f32_16x16x32_bf16 v[2:5], v[130:133], v[172:175], v[2:5]
	v_mfma_f32_16x16x32_bf16 v[6:9], v[138:141], v[172:175], v[6:9]
	v_mfma_f32_16x16x32_bf16 v[58:61], v[134:137], v[152:155], v[58:61]
	v_mfma_f32_16x16x32_bf16 v[62:65], v[142:145], v[152:155], v[62:65]
	v_mfma_f32_16x16x32_bf16 v[42:45], v[134:137], v[160:163], v[42:45]
	v_mfma_f32_16x16x32_bf16 v[46:49], v[142:145], v[160:163], v[46:49]
	v_mfma_f32_16x16x32_bf16 v[26:29], v[134:137], v[168:171], v[26:29]
	v_mfma_f32_16x16x32_bf16 v[30:33], v[142:145], v[168:171], v[30:33]
	v_mfma_f32_16x16x32_bf16 v[2:5], v[134:137], v[176:179], v[2:5]
	v_mfma_f32_16x16x32_bf16 v[6:9], v[142:145], v[176:179], v[6:9]
	s_setprio 0
	s_barrier
	s_add_u32 s30, s30, s66
	s_addc_u32 s31, s31, s67
	s_add_i32 s76, s76, s59
	s_mov_b32 m0, s76
	v_lshl_add_u64 v[220:221], s[30:31], 0, v[146:147]
	global_load_lds_dwordx4 v146, s[30:31]
	s_add_i32 m0, s76, 0x2000
	v_lshl_add_u64 v[222:223], s[30:31], 0, v[188:189]
	global_load_lds_dwordx4 v188, s[30:31]
	s_waitcnt vmcnt(6)
	s_barrier
; #define G_STAGE2(bufoff, gbase, v0, v1) do { \
;         __builtin_amdgcn_global_load_lds((const unsigned*)((const char*)(gbase) + (v0)), (LAS unsigned*)(lds + (bufoff) + ldsw), 16, 0, 0); \
;         __builtin_amdgcn_global_load_lds((const unsigned*)((const char*)(gbase) + (v1)), (LAS unsigned*)(lds + (bufoff) + ldsw + 8192), 16, 0, 0); } while (0)
; #define G_LDA(dst, b, h) do { _Pragma("unroll") for (int m = 0; m < 4; ++m) _Pragma("unroll") for (int k = 0; k < 2; ++k) dst[m][k] = *(const LAS bf16x8*)(lds + G_SA(b, h) + aoff + m * 2048 + k * 1024); } while (0)
; #define G_LDB(dst, b, h) do { _Pragma("unroll") for (int n = 0; n < 2; ++n) _Pragma("unroll") for (int k = 0; k < 2; ++k) dst[n][k] = *(const LAS bf16x8*)(lds + G_SB(b, h) + boff + n * 2048 + k * 1024); } while (0)
; #define G_MMA(ai, bj, At, Bt) do { __builtin_amdgcn_s_setprio(1); _Pragma("unroll") for (int m = 0; m < 4; ++m) _Pragma("unroll") for (int n = 0; n < 2; ++n) _Pragma("unroll") for (int k = 0; k < 2; ++k) \
;         acc[ai][bj][m][n] = __builtin_amdgcn_mfma_f32_16x16x32_bf16(Bt[n][k], At[m][k], acc[ai][bj][m][n], 0, 0, 0); __builtin_amdgcn_s_setprio(0); } while (0)
; #define G_WAIT_V(n) asm volatile("s_waitcnt vmcnt(" #n ")" ::: "memory")
; #define G_WAIT_L(n) asm volatile("s_waitcnt lgkmcnt(" #n ")" ::: "memory")
; #define G_BAR __builtin_amdgcn_s_barrier()
; #define G_SCHED __builtin_amdgcn_sched_barrier(0)
; template <bool PERM, class Epi, class Sched>
; __device__ __forceinline__ void gemm_phase(LAS unsigned char* lds, const Sched& S, const Epi& E) {
;     ...
;             G_WAIT_V(6); G_BAR; G_MMA(1, 1, At, B1); G_BAR;
;             G_LDB(B0, 1, 0); G_SCHED; G_LDA(At, 1, 0); G_STAGE2(G_SA(0, 1), a2, va10, va11);
;             G_WAIT_L(8); G_BAR; G_WAIT_L(0); G_MMA(0, 0, At, B0); G_BAR; G_SCHED;
;             G_LDB(B1, 1, 1); G_STAGE2(G_SB(1, 0), b3, vb0, vb1);
;             G_BAR; G_WAIT_L(0); G_MMA(0, 1, At, B1); G_BAR;
	s_setprio 1
	v_mfma_f32_16x16x32_bf16 v[54:57], v[192:195], v[148:151], v[54:57]
	v_mfma_f32_16x16x32_bf16 v[50:53], v[204:207], v[148:151], v[50:53]
	v_mfma_f32_16x16x32_bf16 v[38:41], v[192:195], v[156:159], v[38:41]
	v_mfma_f32_16x16x32_bf16 v[34:37], v[204:207], v[156:159], v[34:37]
	v_mfma_f32_16x16x32_bf16 v[14:17], v[192:195], v[164:167], v[14:17]
	v_mfma_f32_16x16x32_bf16 v[10:13], v[204:207], v[164:167], v[10:13]
	v_mfma_f32_16x16x32_bf16 v[22:25], v[192:195], v[172:175], v[22:25]
	v_mfma_f32_16x16x32_bf16 v[18:21], v[204:207], v[172:175], v[18:21]
	v_mfma_f32_16x16x32_bf16 v[54:57], v[200:203], v[152:155], v[54:57]
	v_mfma_f32_16x16x32_bf16 v[50:53], v[208:211], v[152:155], v[50:53]
	v_mfma_f32_16x16x32_bf16 v[38:41], v[200:203], v[160:163], v[38:41]
	v_mfma_f32_16x16x32_bf16 v[34:37], v[208:211], v[160:163], v[34:37]
	v_mfma_f32_16x16x32_bf16 v[14:17], v[200:203], v[168:171], v[14:17]
	v_mfma_f32_16x16x32_bf16 v[10:13], v[208:211], v[168:171], v[10:13]
	v_mfma_f32_16x16x32_bf16 v[22:25], v[200:203], v[176:179], v[22:25]
	v_mfma_f32_16x16x32_bf16 v[18:21], v[208:211], v[176:179], v[18:21]
	s_setprio 0
	s_add_i32 s30, 0, 0x18000
	v_add_u32_e32 v142, s30, v1
	s_barrier
	ds_read_b128 v[130:133], v142
	ds_read_b128 v[134:137], v142 offset:1024
	ds_read_b128 v[138:141], v142 offset:2048
	ds_read_b128 v[142:145], v142 offset:3072
	s_mov_b32 m0, s1
	v_lshl_add_u64 v[192:193], s[22:23], 0, v[184:185]
	ds_read_b128 v[148:151], v190 offset:32768
	ds_read_b128 v[152:155], v190 offset:33792
	ds_read_b128 v[156:159], v190 offset:34816
	ds_read_b128 v[160:163], v190 offset:35840
	ds_read_b128 v[164:167], v190 offset:36864
	ds_read_b128 v[168:171], v190 offset:37888
	ds_read_b128 v[172:175], v190 offset:38912
	ds_read_b128 v[176:179], v190 offset:39936
	global_load_lds_dwordx4 v[192:193], off
	v_lshl_add_u64 v[192:193], s[22:23], 0, v[186:187]
	s_mov_b32 m0, s75
	s_nop 0
	global_load_lds_dwordx4 v[192:193], off
	s_waitcnt lgkmcnt(8)
	s_barrier
	s_waitcnt lgkmcnt(0)
	s_setprio 1
	s_waitcnt lgkmcnt(0)
	v_mfma_f32_16x16x32_bf16 v[122:125], v[130:133], v[148:151], v[122:125]
	v_mfma_f32_16x16x32_bf16 v[126:129], v[138:141], v[148:151], v[126:129]
	v_mfma_f32_16x16x32_bf16 v[106:109], v[130:133], v[156:159], v[106:109]
	v_mfma_f32_16x16x32_bf16 v[110:113], v[138:141], v[156:159], v[110:113]
	v_mfma_f32_16x16x32_bf16 v[90:93], v[130:133], v[164:167], v[90:93]
	v_mfma_f32_16x16x32_bf16 v[94:97], v[138:141], v[164:167], v[94:97]
	v_mfma_f32_16x16x32_bf16 v[74:77], v[130:133], v[172:175], v[74:77]
	v_mfma_f32_16x16x32_bf16 v[78:81], v[138:141], v[172:175], v[78:81]
	v_mfma_f32_16x16x32_bf16 v[122:125], v[134:137], v[152:155], v[122:125]
	v_mfma_f32_16x16x32_bf16 v[126:129], v[142:145], v[152:155], v[126:129]
	v_mfma_f32_16x16x32_bf16 v[106:109], v[134:137], v[160:163], v[106:109]
	v_mfma_f32_16x16x32_bf16 v[110:113], v[142:145], v[160:163], v[110:113]
	v_mfma_f32_16x16x32_bf16 v[90:93], v[134:137], v[168:171], v[90:93]
	v_mfma_f32_16x16x32_bf16 v[94:97], v[142:145], v[168:171], v[94:97]
	v_mfma_f32_16x16x32_bf16 v[74:77], v[134:137], v[176:179], v[74:77]
	v_mfma_f32_16x16x32_bf16 v[78:81], v[142:145], v[176:179], v[78:81]
	s_setprio 0
	s_barrier
	s_add_i32 s22, 0, 0x1c000
	s_add_i32 s23, s30, s59
	v_add_u32_e32 v181, s22, v1
	v_lshl_add_u64 v[212:213], v[212:213], 0, s[34:35]
	s_mov_b32 m0, s23
	ds_read_b128 v[192:195], v181
	ds_read_b128 v[200:203], v181 offset:1024
	ds_read_b128 v[204:207], v181 offset:2048
	ds_read_b128 v[208:211], v181 offset:3072
	global_load_lds_dwordx4 v[212:213], off
	v_lshl_add_u64 v[212:213], v[214:215], 0, s[34:35]
	s_add_i32 m0, s23, 0x2000
	s_nop 0
	global_load_lds_dwordx4 v[212:213], off
	s_barrier
; #define G_STAGE2(bufoff, gbase, v0, v1) do { \
;         __builtin_amdgcn_global_load_lds((const unsigned*)((const char*)(gbase) + (v0)), (LAS unsigned*)(lds + (bufoff) + ldsw), 16, 0, 0); \
;         __builtin_amdgcn_global_load_lds((const unsigned*)((const char*)(gbase) + (v1)), (LAS unsigned*)(lds + (bufoff) + ldsw + 8192), 16, 0, 0); } while (0)
; #define G_LDA(dst, b, h) do { _Pragma("unroll") for (int m = 0; m < 4; ++m) _Pragma("unroll") for (int k = 0; k < 2; ++k) dst[m][k] = *(const LAS bf16x8*)(lds + G_SA(b, h) + aoff + m * 2048 + k * 1024); } while (0)
; #define G_MMA(ai, bj, At, Bt) do { __builtin_amdgcn_s_setprio(1); _Pragma("unroll") for (int m = 0; m < 4; ++m) _Pragma("unroll") for (int n = 0; n < 2; ++n) _Pragma("unroll") for (int k = 0; k < 2; ++k) \
;         acc[ai][bj][m][n] = __builtin_amdgcn_mfma_f32_16x16x32_bf16(Bt[n][k], At[m][k], acc[ai][bj][m][n], 0, 0, 0); __builtin_amdgcn_s_setprio(0); } while (0)
; #define G_WAIT_V(n) asm volatile("s_waitcnt vmcnt(" #n ")" ::: "memory")
; #define G_WAIT_L(n) asm volatile("s_waitcnt lgkmcnt(" #n ")" ::: "memory")
; #define G_BAR __builtin_amdgcn_s_barrier()
; #define G_SCHED __builtin_amdgcn_sched_barrier(0)
; template <bool PERM, class Epi, class Sched>
; __device__ __forceinline__ void gemm_phase(LAS unsigned char* lds, const Sched& S, const Epi& E) {
;     ...
;             G_BAR; G_WAIT_L(0); G_MMA(0, 1, At, B1); G_BAR;
;             G_LDA(At, 1, 1); G_STAGE2(G_SA(1, 0), a3, va00, va01);
;             G_BAR; G_WAIT_L(0); G_MMA(1, 0, At, B0); G_BAR; G_SCHED;
;             G_STAGE2(G_SB(1, 1), b3 + hsB, vb0, vb1);
;             G_WAIT_V(6); G_BAR; G_MMA(1, 1, At, B1); G_BAR;
	s_waitcnt lgkmcnt(0)
	s_setprio 1
	s_waitcnt lgkmcnt(0)
	v_mfma_f32_16x16x32_bf16 v[118:121], v[192:195], v[148:151], v[118:121]
	v_mfma_f32_16x16x32_bf16 v[114:117], v[204:207], v[148:151], v[114:117]
	v_mfma_f32_16x16x32_bf16 v[102:105], v[192:195], v[156:159], v[102:105]
	v_mfma_f32_16x16x32_bf16 v[98:101], v[204:207], v[156:159], v[98:101]
	v_mfma_f32_16x16x32_bf16 v[86:89], v[192:195], v[164:167], v[86:89]
	v_mfma_f32_16x16x32_bf16 v[82:85], v[204:207], v[164:167], v[82:85]
	v_mfma_f32_16x16x32_bf16 v[70:73], v[192:195], v[172:175], v[70:73]
	v_mfma_f32_16x16x32_bf16 v[66:69], v[204:207], v[172:175], v[66:69]
	v_mfma_f32_16x16x32_bf16 v[118:121], v[200:203], v[152:155], v[118:121]
	v_mfma_f32_16x16x32_bf16 v[114:117], v[208:211], v[152:155], v[114:117]
	v_mfma_f32_16x16x32_bf16 v[102:105], v[200:203], v[160:163], v[102:105]
	v_mfma_f32_16x16x32_bf16 v[98:101], v[208:211], v[160:163], v[98:101]
	v_mfma_f32_16x16x32_bf16 v[86:89], v[200:203], v[168:171], v[86:89]
	v_mfma_f32_16x16x32_bf16 v[82:85], v[208:211], v[168:171], v[82:85]
	v_mfma_f32_16x16x32_bf16 v[70:73], v[200:203], v[176:179], v[70:73]
	v_mfma_f32_16x16x32_bf16 v[66:69], v[208:211], v[176:179], v[66:69]
	s_setprio 0
	s_mov_b32 m0, s7
	v_lshl_add_u64 v[212:213], v[216:217], 0, s[34:35]
	s_barrier
	ds_read_b128 v[148:151], v190 offset:49152
	ds_read_b128 v[152:155], v190 offset:50176
	ds_read_b128 v[156:159], v190 offset:51200
	ds_read_b128 v[160:163], v190 offset:52224
	ds_read_b128 v[164:167], v190 offset:53248
	ds_read_b128 v[168:171], v190 offset:54272
	ds_read_b128 v[172:175], v190 offset:55296
	ds_read_b128 v[176:179], v190 offset:56320
	global_load_lds_dwordx4 v[212:213], off
	v_lshl_add_u64 v[212:213], v[218:219], 0, s[34:35]
	s_mov_b32 m0, s79
	s_nop 0
	global_load_lds_dwordx4 v[212:213], off
	s_barrier
	s_waitcnt lgkmcnt(0)
	s_setprio 1
	s_waitcnt lgkmcnt(0)
	v_mfma_f32_16x16x32_bf16 v[58:61], v[130:133], v[148:151], v[58:61]
	v_mfma_f32_16x16x32_bf16 v[62:65], v[138:141], v[148:151], v[62:65]
	v_mfma_f32_16x16x32_bf16 v[42:45], v[130:133], v[156:159], v[42:45]
	v_mfma_f32_16x16x32_bf16 v[46:49], v[138:141], v[156:159], v[46:49]
	v_mfma_f32_16x16x32_bf16 v[26:29], v[130:133], v[164:167], v[26:29]
	v_mfma_f32_16x16x32_bf16 v[30:33], v[138:141], v[164:167], v[30:33]
	v_mfma_f32_16x16x32_bf16 v[2:5], v[130:133], v[172:175], v[2:5]
	v_mfma_f32_16x16x32_bf16 v[6:9], v[138:141], v[172:175], v[6:9]
	v_mfma_f32_16x16x32_bf16 v[58:61], v[134:137], v[152:155], v[58:61]
	v_mfma_f32_16x16x32_bf16 v[62:65], v[142:145], v[152:155], v[62:65]
	v_mfma_f32_16x16x32_bf16 v[42:45], v[134:137], v[160:163], v[42:45]
	v_mfma_f32_16x16x32_bf16 v[46:49], v[142:145], v[160:163], v[46:49]
	v_mfma_f32_16x16x32_bf16 v[26:29], v[134:137], v[168:171], v[26:29]
	v_mfma_f32_16x16x32_bf16 v[30:33], v[142:145], v[168:171], v[30:33]
	v_mfma_f32_16x16x32_bf16 v[2:5], v[134:137], v[176:179], v[2:5]
	v_mfma_f32_16x16x32_bf16 v[6:9], v[142:145], v[176:179], v[6:9]
	s_setprio 0
	s_barrier
	s_add_i32 s22, s22, s59
	v_lshl_add_u64 v[130:131], v[220:221], 0, s[34:35]
	s_mov_b32 m0, s22
	s_nop 0
	global_load_lds_dwordx4 v[130:131], off
	v_lshl_add_u64 v[130:131], v[222:223], 0, s[34:35]
	s_add_i32 m0, s22, 0x2000
	s_nop 0
	global_load_lds_dwordx4 v[130:131], off
	s_waitcnt vmcnt(6)
	s_barrier
	s_setprio 1
	v_mfma_f32_16x16x32_bf16 v[54:57], v[192:195], v[148:151], v[54:57]
	v_mfma_f32_16x16x32_bf16 v[50:53], v[204:207], v[148:151], v[50:53]
	v_mfma_f32_16x16x32_bf16 v[38:41], v[192:195], v[156:159], v[38:41]
	v_mfma_f32_16x16x32_bf16 v[34:37], v[204:207], v[156:159], v[34:37]
	v_mfma_f32_16x16x32_bf16 v[14:17], v[192:195], v[164:167], v[14:17]
	v_mfma_f32_16x16x32_bf16 v[10:13], v[204:207], v[164:167], v[10:13]
	v_mfma_f32_16x16x32_bf16 v[22:25], v[192:195], v[172:175], v[22:25]
	v_mfma_f32_16x16x32_bf16 v[18:21], v[204:207], v[172:175], v[18:21]
	v_mfma_f32_16x16x32_bf16 v[54:57], v[200:203], v[152:155], v[54:57]
	v_mfma_f32_16x16x32_bf16 v[50:53], v[208:211], v[152:155], v[50:53]
	v_mfma_f32_16x16x32_bf16 v[38:41], v[200:203], v[160:163], v[38:41]
	v_mfma_f32_16x16x32_bf16 v[34:37], v[208:211], v[160:163], v[34:37]
	v_mfma_f32_16x16x32_bf16 v[14:17], v[200:203], v[168:171], v[14:17]
	v_mfma_f32_16x16x32_bf16 v[10:13], v[208:211], v[168:171], v[10:13]
	v_mfma_f32_16x16x32_bf16 v[22:25], v[200:203], v[176:179], v[22:25]
	v_mfma_f32_16x16x32_bf16 v[18:21], v[208:211], v[176:179], v[18:21]
	s_setprio 0
	s_add_u32 s28, s28, 0x100
	s_addc_u32 s29, s29, 0
	s_add_u32 s43, s43, 0x100
	s_addc_u32 s64, s64, 0
	s_cmp_ge_i32 s74, s41
	s_barrier
	s_cbranch_scc1 .LBB0_736

; #define G_STAGE2(bufoff, gbase, v0, v1) do { \
;         __builtin_amdgcn_global_load_lds((const unsigned*)((const char*)(gbase) + (v0)), (LAS unsigned*)(lds + (bufoff) + ldsw), 16, 0, 0); \
;         __builtin_amdgcn_global_load_lds((const unsigned*)((const char*)(gbase) + (v1)), (LAS unsigned*)(lds + (bufoff) + ldsw + 8192), 16, 0, 0); } while (0)
; #define G_LDA(dst, b, h) do { _Pragma("unroll") for (int m = 0; m < 4; ++m) _Pragma("unroll") for (int k = 0; k < 2; ++k) dst[m][k] = *(const LAS bf16x8*)(lds + G_SA(b, h) + aoff + m * 2048 + k * 1024); } while (0)
; #define G_LDB(dst, b, h) do { _Pragma("unroll") for (int n = 0; n < 2; ++n) _Pragma("unroll") for (int k = 0; k < 2; ++k) dst[n][k] = *(const LAS bf16x8*)(lds + G_SB(b, h) + boff + n * 2048 + k * 1024); } while (0)
; #define G_MMA(ai, bj, At, Bt) do { __builtin_amdgcn_s_setprio(1); _Pragma("unroll") for (int m = 0; m < 4; ++m) _Pragma("unroll") for (int n = 0; n < 2; ++n) _Pragma("unroll") for (int k = 0; k < 2; ++k) \
;         acc[ai][bj][m][n] = __builtin_amdgcn_mfma_f32_16x16x32_bf16(Bt[n][k], At[m][k], acc[ai][bj][m][n], 0, 0, 0); __builtin_amdgcn_s_setprio(0); } while (0)
; template <bool PERM, class Epi, class Sched>
; __device__ __forceinline__ void gemm_phase(LAS unsigned char* lds, const Sched& S, const Epi& E) {
;     ...
;             const char* a1 = cA + (size_t)(t + 1) * kstep;
;             G_LDB(B0, 0, 0); G_SCHED; G_LDA(At, 0, 0); G_STAGE2(G_SA(1, 1), a1, va10, va11);
;             const char* a2 = last ? nA : cA + (size_t)(t + 2) * kstep; const char* b2 = last ? nB : cB + (size_t)(t + 2) * kstep;
;             if (last) {
;                 if (Sched::GATHER_A) { va00 = na00; va01 = na01; va10 = na10; va11 = na11; vb0 = nb0; vb1 = nb1; hsB = nhsB; }
;                 else if (has_next) G_OFFS(nxt, va00, va01, va10, va11, vb0, vb1, hsB);
;             }
;             const char* a3 = a2 + kstep; const char* b3 = b2 + kstep;
;             G_WAIT_L(8); G_BAR; G_WAIT_L(0); G_MMA(0, 0, At, B0); G_BAR; G_SCHED;
;             G_LDB(B1, 0, 1); G_STAGE2(G_SB(0, 0), b2, vb0, vb1);
;             G_BAR; G_WAIT_L(0); G_MMA(0, 1, At, B1); G_BAR;
;             G_LDA(At, 0, 1); G_STAGE2(G_SA(0, 0), a2, va00, va01);
;             G_BAR; G_WAIT_L(0); G_MMA(1, 0, At, B0); G_BAR; G_SCHED;
;             G_STAGE2(G_SB(0, 1), b2 + hsB, vb0, vb1);
;             G_WAIT_V(6); G_BAR; G_MMA(1, 1, At, B1); G_BAR;
.LBB0_835:
	s_add_u32 s18, s64, 0x80
	s_addc_u32 s19, s65, 0
	s_and_b64 s[8:9], s[8:9], exec
	v_mov_b32_e32 v183, v147
	v_mov_b32_e32 v185, v147
	s_cselect_b32 s19, s22, s19
	s_cselect_b32 s18, s23, s18
	s_cselect_b32 s9, s24, s47
	s_cselect_b32 s8, s25, s43
	s_waitcnt lgkmcnt(8)
	s_barrier
	s_waitcnt lgkmcnt(0)
	s_setprio 1
	s_waitcnt lgkmcnt(0)
	v_mfma_f32_16x16x32_bf16 v[126:129], v[130:133], v[172:175], v[126:129]
	v_mfma_f32_16x16x32_bf16 v[122:125], v[138:141], v[172:175], v[122:125]
	v_mfma_f32_16x16x32_bf16 v[118:121], v[130:133], v[164:167], v[118:121]
	v_mfma_f32_16x16x32_bf16 v[110:113], v[138:141], v[164:167], v[110:113]
	v_mfma_f32_16x16x32_bf16 v[94:97], v[130:133], v[156:159], v[94:97]
	v_mfma_f32_16x16x32_bf16 v[90:93], v[138:141], v[156:159], v[90:93]
	v_mfma_f32_16x16x32_bf16 v[86:89], v[130:133], v[148:151], v[86:89]
	v_mfma_f32_16x16x32_bf16 v[78:81], v[138:141], v[148:151], v[78:81]
	v_mfma_f32_16x16x32_bf16 v[126:129], v[134:137], v[176:179], v[126:129]
	v_mfma_f32_16x16x32_bf16 v[122:125], v[142:145], v[176:179], v[122:125]
	v_mfma_f32_16x16x32_bf16 v[118:121], v[134:137], v[168:171], v[118:121]
	v_mfma_f32_16x16x32_bf16 v[110:113], v[142:145], v[168:171], v[110:113]
	v_mfma_f32_16x16x32_bf16 v[94:97], v[134:137], v[160:163], v[94:97]
	v_mfma_f32_16x16x32_bf16 v[90:93], v[142:145], v[160:163], v[90:93]
	v_mfma_f32_16x16x32_bf16 v[86:89], v[134:137], v[152:155], v[86:89]
	v_mfma_f32_16x16x32_bf16 v[78:81], v[142:145], v[152:155], v[78:81]
	s_setprio 0
	s_barrier
	s_add_i32 s84, 0, 0x14000
	s_mov_b32 m0, s55
	v_add_u32_e32 v181, s84, v1
	ds_read_b128 v[188:191], v181
	ds_read_b128 v[192:195], v181 offset:1024
	ds_read_b128 v[200:203], v181 offset:2048
	ds_read_b128 v[204:207], v181 offset:3072
	global_load_lds_dwordx4 v146, s[8:9]
	s_mov_b32 m0, s67
	v_mov_b32_e32 v181, v147
	global_load_lds_dwordx4 v180, s[8:9]
	v_lshl_add_u64 v[208:209], s[8:9], 0, v[146:147]
	v_lshl_add_u64 v[210:211], s[8:9], 0, v[180:181]
	s_barrier
	s_waitcnt lgkmcnt(0)
	s_setprio 1
	s_waitcnt lgkmcnt(0)
	v_mfma_f32_16x16x32_bf16 v[114:117], v[188:191], v[172:175], v[114:117]
	v_mfma_f32_16x16x32_bf16 v[106:109], v[200:203], v[172:175], v[106:109]
	v_mfma_f32_16x16x32_bf16 v[102:105], v[188:191], v[164:167], v[102:105]
	v_mfma_f32_16x16x32_bf16 v[98:101], v[200:203], v[164:167], v[98:101]
	v_mfma_f32_16x16x32_bf16 v[82:85], v[188:191], v[156:159], v[82:85]
	v_mfma_f32_16x16x32_bf16 v[74:77], v[200:203], v[156:159], v[74:77]
	v_mfma_f32_16x16x32_bf16 v[70:73], v[188:191], v[148:151], v[70:73]
	v_mfma_f32_16x16x32_bf16 v[66:69], v[200:203], v[148:151], v[66:69]
	v_mfma_f32_16x16x32_bf16 v[114:117], v[192:195], v[176:179], v[114:117]
	v_mfma_f32_16x16x32_bf16 v[106:109], v[204:207], v[176:179], v[106:109]
	v_mfma_f32_16x16x32_bf16 v[102:105], v[192:195], v[168:171], v[102:105]
	v_mfma_f32_16x16x32_bf16 v[98:101], v[204:207], v[168:171], v[98:101]
	v_mfma_f32_16x16x32_bf16 v[82:85], v[192:195], v[160:163], v[82:85]
	v_mfma_f32_16x16x32_bf16 v[74:77], v[204:207], v[160:163], v[74:77]
	v_mfma_f32_16x16x32_bf16 v[70:73], v[192:195], v[152:155], v[70:73]
	v_mfma_f32_16x16x32_bf16 v[66:69], v[204:207], v[152:155], v[66:69]
	s_setprio 0
	s_mov_b32 m0, s53
	s_barrier
	ds_read_b128 v[148:151], v186 offset:16384
	ds_read_b128 v[152:155], v186 offset:17408
	ds_read_b128 v[156:159], v186 offset:18432
	ds_read_b128 v[160:163], v186 offset:19456
	ds_read_b128 v[164:167], v186 offset:20480
	ds_read_b128 v[168:171], v186 offset:21504
	ds_read_b128 v[172:175], v186 offset:22528
	ds_read_b128 v[176:179], v186 offset:23552
	global_load_lds_dwordx4 v146, s[18:19]
	s_mov_b32 m0, s68
	v_lshl_add_u64 v[212:213], s[18:19], 0, v[146:147]
	global_load_lds_dwordx4 v180, s[18:19]
	v_lshl_add_u64 v[214:215], s[18:19], 0, v[180:181]
	s_barrier
	s_waitcnt lgkmcnt(0)
	s_setprio 1
	s_waitcnt lgkmcnt(0)
	v_mfma_f32_16x16x32_bf16 v[62:65], v[130:133], v[148:151], v[62:65]
	v_mfma_f32_16x16x32_bf16 v[58:61], v[138:141], v[148:151], v[58:61]
	v_mfma_f32_16x16x32_bf16 v[50:53], v[130:133], v[156:159], v[50:53]
	v_mfma_f32_16x16x32_bf16 v[42:45], v[138:141], v[156:159], v[42:45]
	v_mfma_f32_16x16x32_bf16 v[30:33], v[130:133], v[164:167], v[30:33]
	v_mfma_f32_16x16x32_bf16 v[26:29], v[138:141], v[164:167], v[26:29]
	v_mfma_f32_16x16x32_bf16 v[18:21], v[130:133], v[172:175], v[18:21]
	v_mfma_f32_16x16x32_bf16 v[10:13], v[138:141], v[172:175], v[10:13]
	v_mfma_f32_16x16x32_bf16 v[62:65], v[134:137], v[152:155], v[62:65]
	v_mfma_f32_16x16x32_bf16 v[58:61], v[142:145], v[152:155], v[58:61]
	v_mfma_f32_16x16x32_bf16 v[50:53], v[134:137], v[160:163], v[50:53]
	v_mfma_f32_16x16x32_bf16 v[42:45], v[142:145], v[160:163], v[42:45]
	v_mfma_f32_16x16x32_bf16 v[30:33], v[134:137], v[168:171], v[30:33]
	v_mfma_f32_16x16x32_bf16 v[26:29], v[142:145], v[168:171], v[26:29]
	v_mfma_f32_16x16x32_bf16 v[18:21], v[134:137], v[176:179], v[18:21]
	v_mfma_f32_16x16x32_bf16 v[10:13], v[142:145], v[176:179], v[10:13]
	s_setprio 0
	s_barrier
	s_add_u32 s82, s8, 0x40000
	s_addc_u32 s83, s9, 0
	s_add_i32 s84, s84, s66
	s_mov_b32 m0, s84
	s_nop 0
	global_load_lds_dwordx4 v146, s[82:83]
	s_add_i32 m0, s84, 0x2000
	s_nop 0
	global_load_lds_dwordx4 v180, s[82:83]
	s_waitcnt vmcnt(6)
	s_barrier
; #define G_STAGE2(bufoff, gbase, v0, v1) do { \
;         __builtin_amdgcn_global_load_lds((const unsigned*)((const char*)(gbase) + (v0)), (LAS unsigned*)(lds + (bufoff) + ldsw), 16, 0, 0); \
;         __builtin_amdgcn_global_load_lds((const unsigned*)((const char*)(gbase) + (v1)), (LAS unsigned*)(lds + (bufoff) + ldsw + 8192), 16, 0, 0); } while (0)
; #define G_LDA(dst, b, h) do { _Pragma("unroll") for (int m = 0; m < 4; ++m) _Pragma("unroll") for (int k = 0; k < 2; ++k) dst[m][k] = *(const LAS bf16x8*)(lds + G_SA(b, h) + aoff + m * 2048 + k * 1024); } while (0)
; #define G_LDB(dst, b, h) do { _Pragma("unroll") for (int n = 0; n < 2; ++n) _Pragma("unroll") for (int k = 0; k < 2; ++k) dst[n][k] = *(const LAS bf16x8*)(lds + G_SB(b, h) + boff + n * 2048 + k * 1024); } while (0)
; #define G_MMA(ai, bj, At, Bt) do { __builtin_amdgcn_s_setprio(1); _Pragma("unroll") for (int m = 0; m < 4; ++m) _Pragma("unroll") for (int n = 0; n < 2; ++n) _Pragma("unroll") for (int k = 0; k < 2; ++k) \
;         acc[ai][bj][m][n] = __builtin_amdgcn_mfma_f32_16x16x32_bf16(Bt[n][k], At[m][k], acc[ai][bj][m][n], 0, 0, 0); __builtin_amdgcn_s_setprio(0); } while (0)
; #define G_WAIT_V(n) asm volatile("s_waitcnt vmcnt(" #n ")" ::: "memory")
; #define G_WAIT_L(n) asm volatile("s_waitcnt lgkmcnt(" #n ")" ::: "memory")
; #define G_BAR __builtin_amdgcn_s_barrier()
; #define G_SCHED __builtin_amdgcn_sched_barrier(0)
; template <bool PERM, class Epi, class Sched>
; __device__ __forceinline__ void gemm_phase(LAS unsigned char* lds, const Sched& S, const Epi& E) {
;     ...
;             G_WAIT_V(6); G_BAR; G_MMA(1, 1, At, B1); G_BAR;
;             G_LDB(B0, 1, 0); G_SCHED; G_LDA(At, 1, 0); G_STAGE2(G_SA(0, 1), a2, va10, va11);
;             G_WAIT_L(8); G_BAR; G_WAIT_L(0); G_MMA(0, 0, At, B0); G_BAR; G_SCHED;
;             G_LDB(B1, 1, 1); G_STAGE2(G_SB(1, 0), b3, vb0, vb1);
;             G_BAR; G_WAIT_L(0); G_MMA(0, 1, At, B1); G_BAR;
	s_setprio 1
	v_mfma_f32_16x16x32_bf16 v[54:57], v[188:191], v[148:151], v[54:57]
	v_mfma_f32_16x16x32_bf16 v[46:49], v[200:203], v[148:151], v[46:49]
	v_mfma_f32_16x16x32_bf16 v[38:41], v[188:191], v[156:159], v[38:41]
	v_mfma_f32_16x16x32_bf16 v[34:37], v[200:203], v[156:159], v[34:37]
	v_mfma_f32_16x16x32_bf16 v[22:25], v[188:191], v[164:167], v[22:25]
	v_mfma_f32_16x16x32_bf16 v[14:17], v[200:203], v[164:167], v[14:17]
	v_mfma_f32_16x16x32_bf16 v[6:9], v[188:191], v[172:175], v[6:9]
	v_mfma_f32_16x16x32_bf16 v[2:5], v[200:203], v[172:175], v[2:5]
	v_mfma_f32_16x16x32_bf16 v[54:57], v[192:195], v[152:155], v[54:57]
	v_mfma_f32_16x16x32_bf16 v[46:49], v[204:207], v[152:155], v[46:49]
	v_mfma_f32_16x16x32_bf16 v[38:41], v[192:195], v[160:163], v[38:41]
	v_mfma_f32_16x16x32_bf16 v[34:37], v[204:207], v[160:163], v[34:37]
	v_mfma_f32_16x16x32_bf16 v[22:25], v[192:195], v[168:171], v[22:25]
	v_mfma_f32_16x16x32_bf16 v[14:17], v[204:207], v[168:171], v[14:17]
	v_mfma_f32_16x16x32_bf16 v[6:9], v[192:195], v[176:179], v[6:9]
	v_mfma_f32_16x16x32_bf16 v[2:5], v[204:207], v[176:179], v[2:5]
	s_setprio 0
	s_add_i32 s82, 0, 0x18000
	v_add_u32_e32 v142, s82, v1
	s_barrier
	ds_read_b128 v[130:133], v142
	ds_read_b128 v[134:137], v142 offset:1024
	ds_read_b128 v[138:141], v142 offset:2048
	ds_read_b128 v[142:145], v142 offset:3072
	s_mov_b32 m0, s69
	v_lshl_add_u64 v[188:189], s[18:19], 0, v[182:183]
	ds_read_b128 v[148:151], v186 offset:32768
	ds_read_b128 v[152:155], v186 offset:33792
	ds_read_b128 v[156:159], v186 offset:34816
	ds_read_b128 v[160:163], v186 offset:35840
	ds_read_b128 v[164:167], v186 offset:36864
	ds_read_b128 v[168:171], v186 offset:37888
	ds_read_b128 v[172:175], v186 offset:38912
	ds_read_b128 v[176:179], v186 offset:39936
	global_load_lds_dwordx4 v[188:189], off
	v_lshl_add_u64 v[188:189], s[18:19], 0, v[184:185]
	s_mov_b32 m0, s70
	s_nop 0
	global_load_lds_dwordx4 v[188:189], off
	s_waitcnt lgkmcnt(8)
	s_barrier
	s_waitcnt lgkmcnt(0)
	s_setprio 1
	s_waitcnt lgkmcnt(0)
	v_mfma_f32_16x16x32_bf16 v[126:129], v[130:133], v[148:151], v[126:129]
	v_mfma_f32_16x16x32_bf16 v[122:125], v[138:141], v[148:151], v[122:125]
	v_mfma_f32_16x16x32_bf16 v[118:121], v[130:133], v[156:159], v[118:121]
	v_mfma_f32_16x16x32_bf16 v[110:113], v[138:141], v[156:159], v[110:113]
	v_mfma_f32_16x16x32_bf16 v[94:97], v[130:133], v[164:167], v[94:97]
	v_mfma_f32_16x16x32_bf16 v[90:93], v[138:141], v[164:167], v[90:93]
	v_mfma_f32_16x16x32_bf16 v[86:89], v[130:133], v[172:175], v[86:89]
	v_mfma_f32_16x16x32_bf16 v[78:81], v[138:141], v[172:175], v[78:81]
	v_mfma_f32_16x16x32_bf16 v[126:129], v[134:137], v[152:155], v[126:129]
	v_mfma_f32_16x16x32_bf16 v[122:125], v[142:145], v[152:155], v[122:125]
	v_mfma_f32_16x16x32_bf16 v[118:121], v[134:137], v[160:163], v[118:121]
	v_mfma_f32_16x16x32_bf16 v[110:113], v[142:145], v[160:163], v[110:113]
	v_mfma_f32_16x16x32_bf16 v[94:97], v[134:137], v[168:171], v[94:97]
	v_mfma_f32_16x16x32_bf16 v[90:93], v[142:145], v[168:171], v[90:93]
	v_mfma_f32_16x16x32_bf16 v[86:89], v[134:137], v[176:179], v[86:89]
	v_mfma_f32_16x16x32_bf16 v[78:81], v[142:145], v[176:179], v[78:81]
	s_setprio 0
	s_barrier
	s_add_i32 s18, 0, 0x1c000
	s_add_i32 s19, s82, s66
	v_add_u32_e32 v181, s18, v1
	v_lshl_add_u64 v[208:209], v[208:209], 0, s[34:35]
	s_mov_b32 m0, s19
	ds_read_b128 v[188:191], v181
	ds_read_b128 v[192:195], v181 offset:1024
	ds_read_b128 v[200:203], v181 offset:2048
	ds_read_b128 v[204:207], v181 offset:3072
	global_load_lds_dwordx4 v[208:209], off
	v_lshl_add_u64 v[208:209], v[210:211], 0, s[34:35]
	s_add_i32 m0, s19, 0x2000
	s_nop 0
	global_load_lds_dwordx4 v[208:209], off
	s_barrier
; #define G_STAGE2(bufoff, gbase, v0, v1) do { \
;         __builtin_amdgcn_global_load_lds((const unsigned*)((const char*)(gbase) + (v0)), (LAS unsigned*)(lds + (bufoff) + ldsw), 16, 0, 0); \
;         __builtin_amdgcn_global_load_lds((const unsigned*)((const char*)(gbase) + (v1)), (LAS unsigned*)(lds + (bufoff) + ldsw + 8192), 16, 0, 0); } while (0)
; #define G_LDA(dst, b, h) do { _Pragma("unroll") for (int m = 0; m < 4; ++m) _Pragma("unroll") for (int k = 0; k < 2; ++k) dst[m][k] = *(const LAS bf16x8*)(lds + G_SA(b, h) + aoff + m * 2048 + k * 1024); } while (0)
; #define G_MMA(ai, bj, At, Bt) do { __builtin_amdgcn_s_setprio(1); _Pragma("unroll") for (int m = 0; m < 4; ++m) _Pragma("unroll") for (int n = 0; n < 2; ++n) _Pragma("unroll") for (int k = 0; k < 2; ++k) \
;         acc[ai][bj][m][n] = __builtin_amdgcn_mfma_f32_16x16x32_bf16(Bt[n][k], At[m][k], acc[ai][bj][m][n], 0, 0, 0); __builtin_amdgcn_s_setprio(0); } while (0)
; #define G_WAIT_V(n) asm volatile("s_waitcnt vmcnt(" #n ")" ::: "memory")
; #define G_WAIT_L(n) asm volatile("s_waitcnt lgkmcnt(" #n ")" ::: "memory")
; #define G_BAR __builtin_amdgcn_s_barrier()
; #define G_SCHED __builtin_amdgcn_sched_barrier(0)
; template <bool PERM, class Epi, class Sched>
; __device__ __forceinline__ void gemm_phase(LAS unsigned char* lds, const Sched& S, const Epi& E) {
;     ...
;             G_BAR; G_WAIT_L(0); G_MMA(0, 1, At, B1); G_BAR;
;             G_LDA(At, 1, 1); G_STAGE2(G_SA(1, 0), a3, va00, va01);
;             G_BAR; G_WAIT_L(0); G_MMA(1, 0, At, B0); G_BAR; G_SCHED;
;             G_STAGE2(G_SB(1, 1), b3 + hsB, vb0, vb1);
;             G_WAIT_V(6); G_BAR; G_MMA(1, 1, At, B1); G_BAR;
	s_waitcnt lgkmcnt(0)
	s_setprio 1
	s_waitcnt lgkmcnt(0)
	v_mfma_f32_16x16x32_bf16 v[114:117], v[188:191], v[148:151], v[114:117]
	v_mfma_f32_16x16x32_bf16 v[106:109], v[200:203], v[148:151], v[106:109]
	v_mfma_f32_16x16x32_bf16 v[102:105], v[188:191], v[156:159], v[102:105]
	v_mfma_f32_16x16x32_bf16 v[98:101], v[200:203], v[156:159], v[98:101]
	v_mfma_f32_16x16x32_bf16 v[82:85], v[188:191], v[164:167], v[82:85]
	v_mfma_f32_16x16x32_bf16 v[74:77], v[200:203], v[164:167], v[74:77]
	v_mfma_f32_16x16x32_bf16 v[70:73], v[188:191], v[172:175], v[70:73]
	v_mfma_f32_16x16x32_bf16 v[66:69], v[200:203], v[172:175], v[66:69]
	v_mfma_f32_16x16x32_bf16 v[114:117], v[192:195], v[152:155], v[114:117]
	v_mfma_f32_16x16x32_bf16 v[106:109], v[204:207], v[152:155], v[106:109]
	v_mfma_f32_16x16x32_bf16 v[102:105], v[192:195], v[160:163], v[102:105]
	v_mfma_f32_16x16x32_bf16 v[98:101], v[204:207], v[160:163], v[98:101]
	v_mfma_f32_16x16x32_bf16 v[82:85], v[192:195], v[168:171], v[82:85]
	v_mfma_f32_16x16x32_bf16 v[74:77], v[204:207], v[168:171], v[74:77]
	v_mfma_f32_16x16x32_bf16 v[70:73], v[192:195], v[176:179], v[70:73]
	v_mfma_f32_16x16x32_bf16 v[66:69], v[204:207], v[176:179], v[66:69]
	s_setprio 0
	s_mov_b32 m0, s72
	v_lshl_add_u64 v[208:209], v[212:213], 0, s[34:35]
	s_barrier
	ds_read_b128 v[148:151], v186 offset:49152
	ds_read_b128 v[152:155], v186 offset:50176
	ds_read_b128 v[156:159], v186 offset:51200
	ds_read_b128 v[160:163], v186 offset:52224
	ds_read_b128 v[164:167], v186 offset:53248
	ds_read_b128 v[168:171], v186 offset:54272
	ds_read_b128 v[172:175], v186 offset:55296
	ds_read_b128 v[176:179], v186 offset:56320
	global_load_lds_dwordx4 v[208:209], off
	v_lshl_add_u64 v[208:209], v[214:215], 0, s[34:35]
	s_mov_b32 m0, s73
	s_nop 0
	global_load_lds_dwordx4 v[208:209], off
	s_barrier
	s_waitcnt lgkmcnt(0)
	s_setprio 1
	s_waitcnt lgkmcnt(0)
	v_mfma_f32_16x16x32_bf16 v[62:65], v[130:133], v[148:151], v[62:65]
	v_mfma_f32_16x16x32_bf16 v[58:61], v[138:141], v[148:151], v[58:61]
	v_mfma_f32_16x16x32_bf16 v[50:53], v[130:133], v[156:159], v[50:53]
	v_mfma_f32_16x16x32_bf16 v[42:45], v[138:141], v[156:159], v[42:45]
	v_mfma_f32_16x16x32_bf16 v[30:33], v[130:133], v[164:167], v[30:33]
	v_mfma_f32_16x16x32_bf16 v[26:29], v[138:141], v[164:167], v[26:29]
	v_mfma_f32_16x16x32_bf16 v[18:21], v[130:133], v[172:175], v[18:21]
	v_mfma_f32_16x16x32_bf16 v[10:13], v[138:141], v[172:175], v[10:13]
	v_mfma_f32_16x16x32_bf16 v[62:65], v[134:137], v[152:155], v[62:65]
	v_mfma_f32_16x16x32_bf16 v[58:61], v[142:145], v[152:155], v[58:61]
	v_mfma_f32_16x16x32_bf16 v[50:53], v[134:137], v[160:163], v[50:53]
	v_mfma_f32_16x16x32_bf16 v[42:45], v[142:145], v[160:163], v[42:45]
	v_mfma_f32_16x16x32_bf16 v[30:33], v[134:137], v[168:171], v[30:33]
	v_mfma_f32_16x16x32_bf16 v[26:29], v[142:145], v[168:171], v[26:29]
	v_mfma_f32_16x16x32_bf16 v[18:21], v[134:137], v[176:179], v[18:21]
	v_mfma_f32_16x16x32_bf16 v[10:13], v[142:145], v[176:179], v[10:13]
	s_setprio 0
	s_barrier
	s_add_u32 s8, s8, 0x40080
	s_addc_u32 s9, s9, 0
	s_add_i32 s18, s18, s66
	s_mov_b32 m0, s18
	s_nop 0
	global_load_lds_dwordx4 v146, s[8:9]
	s_add_i32 m0, s18, 0x2000
	s_nop 0
	global_load_lds_dwordx4 v180, s[8:9]
	s_waitcnt vmcnt(6)
	s_barrier
	s_setprio 1
	v_mfma_f32_16x16x32_bf16 v[54:57], v[188:191], v[148:151], v[54:57]
	v_mfma_f32_16x16x32_bf16 v[46:49], v[200:203], v[148:151], v[46:49]
	v_mfma_f32_16x16x32_bf16 v[38:41], v[188:191], v[156:159], v[38:41]
	v_mfma_f32_16x16x32_bf16 v[34:37], v[200:203], v[156:159], v[34:37]
	v_mfma_f32_16x16x32_bf16 v[22:25], v[188:191], v[164:167], v[22:25]
	v_mfma_f32_16x16x32_bf16 v[14:17], v[200:203], v[164:167], v[14:17]
	v_mfma_f32_16x16x32_bf16 v[6:9], v[188:191], v[172:175], v[6:9]
	v_mfma_f32_16x16x32_bf16 v[2:5], v[200:203], v[172:175], v[2:5]
	v_mfma_f32_16x16x32_bf16 v[54:57], v[192:195], v[152:155], v[54:57]
	v_mfma_f32_16x16x32_bf16 v[46:49], v[204:207], v[152:155], v[46:49]
	v_mfma_f32_16x16x32_bf16 v[38:41], v[192:195], v[160:163], v[38:41]
	v_mfma_f32_16x16x32_bf16 v[34:37], v[204:207], v[160:163], v[34:37]
	v_mfma_f32_16x16x32_bf16 v[22:25], v[192:195], v[168:171], v[22:25]
	v_mfma_f32_16x16x32_bf16 v[14:17], v[204:207], v[168:171], v[14:17]
	v_mfma_f32_16x16x32_bf16 v[6:9], v[192:195], v[176:179], v[6:9]
	v_mfma_f32_16x16x32_bf16 v[2:5], v[204:207], v[176:179], v[2:5]
	s_setprio 0
	s_add_i32 s81, s81, 2
	s_add_u32 s64, s64, 0x100
	s_addc_u32 s65, s65, 0
	s_add_u32 s43, s43, 0x100
	s_addc_u32 s47, s47, 0
	s_cmp_gt_u32 s81, 13
	s_barrier
	s_cbranch_scc1 .LBB0_838

; #define G_STAGE2(bufoff, gbase, v0, v1) do { \
;         __builtin_amdgcn_global_load_lds((const unsigned*)((const char*)(gbase) + (v0)), (LAS unsigned*)(lds + (bufoff) + ldsw), 16, 0, 0); \
;         __builtin_amdgcn_global_load_lds((const unsigned*)((const char*)(gbase) + (v1)), (LAS unsigned*)(lds + (bufoff) + ldsw + 8192), 16, 0, 0); } while (0)
; #define G_LDA(dst, b, h) do { _Pragma("unroll") for (int m = 0; m < 4; ++m) _Pragma("unroll") for (int k = 0; k < 2; ++k) dst[m][k] = *(const LAS bf16x8*)(lds + G_SA(b, h) + aoff + m * 2048 + k * 1024); } while (0)
; #define G_LDB(dst, b, h) do { _Pragma("unroll") for (int n = 0; n < 2; ++n) _Pragma("unroll") for (int k = 0; k < 2; ++k) dst[n][k] = *(const LAS bf16x8*)(lds + G_SB(b, h) + boff + n * 2048 + k * 1024); } while (0)
; #define G_MMA(ai, bj, At, Bt) do { __builtin_amdgcn_s_setprio(1); _Pragma("unroll") for (int m = 0; m < 4; ++m) _Pragma("unroll") for (int n = 0; n < 2; ++n) _Pragma("unroll") for (int k = 0; k < 2; ++k) \
;         acc[ai][bj][m][n] = __builtin_amdgcn_mfma_f32_16x16x32_bf16(Bt[n][k], At[m][k], acc[ai][bj][m][n], 0, 0, 0); __builtin_amdgcn_s_setprio(0); } while (0)
; template <bool PERM, class Epi, class Sched>
; __device__ __forceinline__ void gemm_phase(LAS unsigned char* lds, const Sched& S, const Epi& E) {
;     ...
;             const char* a1 = cA + (size_t)(t + 1) * kstep;
;             G_LDB(B0, 0, 0); G_SCHED; G_LDA(At, 0, 0); G_STAGE2(G_SA(1, 1), a1, va10, va11);
;             const char* a2 = last ? nA : cA + (size_t)(t + 2) * kstep; const char* b2 = last ? nB : cB + (size_t)(t + 2) * kstep;
;             if (last) {
;                 if (Sched::GATHER_A) { va00 = na00; va01 = na01; va10 = na10; va11 = na11; vb0 = nb0; vb1 = nb1; hsB = nhsB; }
;                 else if (has_next) G_OFFS(nxt, va00, va01, va10, va11, vb0, vb1, hsB);
;             }
;             const char* a3 = a2 + kstep; const char* b3 = b2 + kstep;
;             G_WAIT_L(8); G_BAR; G_WAIT_L(0); G_MMA(0, 0, At, B0); G_BAR; G_SCHED;
;             G_LDB(B1, 0, 1); G_STAGE2(G_SB(0, 0), b2, vb0, vb1);
;             G_BAR; G_WAIT_L(0); G_MMA(0, 1, At, B1); G_BAR;
;             G_LDA(At, 0, 1); G_STAGE2(G_SA(0, 0), a2, va00, va01);
;             G_BAR; G_WAIT_L(0); G_MMA(1, 0, At, B0); G_BAR; G_SCHED;
;             G_STAGE2(G_SB(0, 1), b2 + hsB, vb0, vb1);
;             G_WAIT_V(6); G_BAR; G_MMA(1, 1, At, B1); G_BAR;
.LBB0_862:
	s_add_i32 s45, 0, 0x10000
	v_add_u32_e32 v141, s45, v1
	ds_read_b128 v[142:145], v141
	ds_read_b128 v[148:151], v141 offset:1024
	ds_read_b128 v[152:155], v141 offset:2048
	ds_read_b128 v[156:159], v141 offset:3072
	v_lshl_add_u64 v[192:193], v[138:139], 0, s[42:43]
	s_add_i32 m0, s0, 0xc000
	ds_read_b128 v[160:163], v140
	ds_read_b128 v[164:167], v140 offset:1024
	ds_read_b128 v[168:171], v140 offset:2048
	ds_read_b128 v[172:175], v140 offset:3072
	ds_read_b128 v[176:179], v140 offset:4096
	ds_read_b128 v[180:183], v140 offset:5120
	ds_read_b128 v[184:187], v140 offset:6144
	ds_read_b128 v[188:191], v140 offset:7168
	global_load_lds_dwordx4 v[192:193], off
	v_lshl_add_u64 v[192:193], v[136:137], 0, s[42:43]
	s_add_i32 m0, s0, 0xe000
	s_add_i32 s8, s42, 0xc2ce9f80
	global_load_lds_dwordx4 v[192:193], off
	s_cmp_lg_u32 s44, 12
	s_cselect_b32 s8, s8, 0
	s_add_u32 s18, s28, s8
	s_addc_u32 s19, s29, 0
	s_add_u32 s8, s40, s8
	s_addc_u32 s9, s41, 0
	s_waitcnt lgkmcnt(8)
	s_barrier
	s_waitcnt lgkmcnt(0)
	s_setprio 1
	s_waitcnt lgkmcnt(0)
	v_mfma_f32_16x16x32_bf16 v[126:129], v[142:145], v[160:163], v[126:129]
	v_mfma_f32_16x16x32_bf16 v[122:125], v[152:155], v[160:163], v[122:125]
	v_mfma_f32_16x16x32_bf16 v[114:117], v[142:145], v[168:171], v[114:117]
	v_mfma_f32_16x16x32_bf16 v[106:109], v[152:155], v[168:171], v[106:109]
	v_mfma_f32_16x16x32_bf16 v[94:97], v[142:145], v[176:179], v[94:97]
	v_mfma_f32_16x16x32_bf16 v[90:93], v[152:155], v[176:179], v[90:93]
	v_mfma_f32_16x16x32_bf16 v[82:85], v[142:145], v[184:187], v[82:85]
	v_mfma_f32_16x16x32_bf16 v[74:77], v[152:155], v[184:187], v[74:77]
	v_mfma_f32_16x16x32_bf16 v[126:129], v[148:151], v[164:167], v[126:129]
	v_mfma_f32_16x16x32_bf16 v[122:125], v[156:159], v[164:167], v[122:125]
	v_mfma_f32_16x16x32_bf16 v[114:117], v[148:151], v[172:175], v[114:117]
	v_mfma_f32_16x16x32_bf16 v[106:109], v[156:159], v[172:175], v[106:109]
	v_mfma_f32_16x16x32_bf16 v[94:97], v[148:151], v[180:183], v[94:97]
	v_mfma_f32_16x16x32_bf16 v[90:93], v[156:159], v[180:183], v[90:93]
	v_mfma_f32_16x16x32_bf16 v[82:85], v[148:151], v[188:191], v[82:85]
	v_mfma_f32_16x16x32_bf16 v[74:77], v[156:159], v[188:191], v[74:77]
	s_setprio 0
	s_barrier
	s_add_i32 s48, 0, 0x14000
	s_add_i32 s45, s45, s23
	v_add_u32_e32 v141, s48, v1
	v_lshl_add_u64 v[212:213], s[8:9], 0, v[146:147]
	s_mov_b32 m0, s45
	ds_read_b128 v[192:195], v141
	ds_read_b128 v[200:203], v141 offset:1024
	ds_read_b128 v[204:207], v141 offset:2048
	ds_read_b128 v[208:211], v141 offset:3072
	global_load_lds_dwordx4 v[212:213], off
	v_lshl_add_u64 v[214:215], s[8:9], 0, v[130:131]
	s_add_i32 m0, s45, 0x2000
	s_nop 0
	global_load_lds_dwordx4 v[214:215], off
	s_barrier
	s_waitcnt lgkmcnt(0)
	s_setprio 1
	s_waitcnt lgkmcnt(0)
	v_mfma_f32_16x16x32_bf16 v[118:121], v[192:195], v[160:163], v[118:121]
	v_mfma_f32_16x16x32_bf16 v[110:113], v[204:207], v[160:163], v[110:113]
	v_mfma_f32_16x16x32_bf16 v[102:105], v[192:195], v[168:171], v[102:105]
	v_mfma_f32_16x16x32_bf16 v[98:101], v[204:207], v[168:171], v[98:101]
	v_mfma_f32_16x16x32_bf16 v[86:89], v[192:195], v[176:179], v[86:89]
	v_mfma_f32_16x16x32_bf16 v[78:81], v[204:207], v[176:179], v[78:81]
	v_mfma_f32_16x16x32_bf16 v[70:73], v[192:195], v[184:187], v[70:73]
	v_mfma_f32_16x16x32_bf16 v[66:69], v[204:207], v[184:187], v[66:69]
	v_mfma_f32_16x16x32_bf16 v[118:121], v[200:203], v[164:167], v[118:121]
	v_mfma_f32_16x16x32_bf16 v[110:113], v[208:211], v[164:167], v[110:113]
	v_mfma_f32_16x16x32_bf16 v[102:105], v[200:203], v[172:175], v[102:105]
	v_mfma_f32_16x16x32_bf16 v[98:101], v[208:211], v[172:175], v[98:101]
	v_mfma_f32_16x16x32_bf16 v[86:89], v[200:203], v[180:183], v[86:89]
	v_mfma_f32_16x16x32_bf16 v[78:81], v[208:211], v[180:183], v[78:81]
	v_mfma_f32_16x16x32_bf16 v[70:73], v[200:203], v[188:191], v[70:73]
	v_mfma_f32_16x16x32_bf16 v[66:69], v[208:211], v[188:191], v[66:69]
	s_setprio 0
	s_mov_b32 m0, s0
	v_lshl_add_u64 v[216:217], s[18:19], 0, v[146:147]
	s_barrier
	ds_read_b128 v[160:163], v140 offset:16384
	ds_read_b128 v[164:167], v140 offset:17408
	ds_read_b128 v[168:171], v140 offset:18432
	ds_read_b128 v[172:175], v140 offset:19456
	ds_read_b128 v[176:179], v140 offset:20480
	ds_read_b128 v[180:183], v140 offset:21504
	ds_read_b128 v[184:187], v140 offset:22528
	ds_read_b128 v[188:191], v140 offset:23552
	global_load_lds_dwordx4 v[216:217], off
	v_lshl_add_u64 v[218:219], s[18:19], 0, v[130:131]
	s_mov_b32 m0, s2
	s_nop 0
	global_load_lds_dwordx4 v[218:219], off
	s_barrier
	s_waitcnt lgkmcnt(0)
	s_setprio 1
	s_waitcnt lgkmcnt(0)
	v_mfma_f32_16x16x32_bf16 v[62:65], v[142:145], v[160:163], v[62:65]
	v_mfma_f32_16x16x32_bf16 v[58:61], v[152:155], v[160:163], v[58:61]
	v_mfma_f32_16x16x32_bf16 v[50:53], v[142:145], v[168:171], v[50:53]
	v_mfma_f32_16x16x32_bf16 v[42:45], v[152:155], v[168:171], v[42:45]
	v_mfma_f32_16x16x32_bf16 v[30:33], v[142:145], v[176:179], v[30:33]
	v_mfma_f32_16x16x32_bf16 v[26:29], v[152:155], v[176:179], v[26:29]
	v_mfma_f32_16x16x32_bf16 v[18:21], v[142:145], v[184:187], v[18:21]
	v_mfma_f32_16x16x32_bf16 v[10:13], v[152:155], v[184:187], v[10:13]
	v_mfma_f32_16x16x32_bf16 v[62:65], v[148:151], v[164:167], v[62:65]
	v_mfma_f32_16x16x32_bf16 v[58:61], v[156:159], v[164:167], v[58:61]
	v_mfma_f32_16x16x32_bf16 v[50:53], v[148:151], v[172:175], v[50:53]
	v_mfma_f32_16x16x32_bf16 v[42:45], v[156:159], v[172:175], v[42:45]
	v_mfma_f32_16x16x32_bf16 v[30:33], v[148:151], v[180:183], v[30:33]
	v_mfma_f32_16x16x32_bf16 v[26:29], v[156:159], v[180:183], v[26:29]
	v_mfma_f32_16x16x32_bf16 v[18:21], v[148:151], v[188:191], v[18:21]
	v_mfma_f32_16x16x32_bf16 v[10:13], v[156:159], v[188:191], v[10:13]
	s_setprio 0
	s_barrier
; #define G_STAGE2(bufoff, gbase, v0, v1) do { \
;         __builtin_amdgcn_global_load_lds((const unsigned*)((const char*)(gbase) + (v0)), (LAS unsigned*)(lds + (bufoff) + ldsw), 16, 0, 0); \
;         __builtin_amdgcn_global_load_lds((const unsigned*)((const char*)(gbase) + (v1)), (LAS unsigned*)(lds + (bufoff) + ldsw + 8192), 16, 0, 0); } while (0)
; #define G_LDA(dst, b, h) do { _Pragma("unroll") for (int m = 0; m < 4; ++m) _Pragma("unroll") for (int k = 0; k < 2; ++k) dst[m][k] = *(const LAS bf16x8*)(lds + G_SA(b, h) + aoff + m * 2048 + k * 1024); } while (0)
; #define G_LDB(dst, b, h) do { _Pragma("unroll") for (int n = 0; n < 2; ++n) _Pragma("unroll") for (int k = 0; k < 2; ++k) dst[n][k] = *(const LAS bf16x8*)(lds + G_SB(b, h) + boff + n * 2048 + k * 1024); } while (0)
; #define G_MMA(ai, bj, At, Bt) do { __builtin_amdgcn_s_setprio(1); _Pragma("unroll") for (int m = 0; m < 4; ++m) _Pragma("unroll") for (int n = 0; n < 2; ++n) _Pragma("unroll") for (int k = 0; k < 2; ++k) \
;         acc[ai][bj][m][n] = __builtin_amdgcn_mfma_f32_16x16x32_bf16(Bt[n][k], At[m][k], acc[ai][bj][m][n], 0, 0, 0); __builtin_amdgcn_s_setprio(0); } while (0)
; #define G_WAIT_V(n) asm volatile("s_waitcnt vmcnt(" #n ")" ::: "memory")
; #define G_WAIT_L(n) asm volatile("s_waitcnt lgkmcnt(" #n ")" ::: "memory")
; #define G_BAR __builtin_amdgcn_s_barrier()
; #define G_SCHED __builtin_amdgcn_sched_barrier(0)
; template <bool PERM, class Epi, class Sched>
; __device__ __forceinline__ void gemm_phase(LAS unsigned char* lds, const Sched& S, const Epi& E) {
;     ...
;             G_STAGE2(G_SB(0, 1), b2 + hsB, vb0, vb1);
;             G_WAIT_V(6); G_BAR; G_MMA(1, 1, At, B1); G_BAR;
;             G_LDB(B0, 1, 0); G_SCHED; G_LDA(At, 1, 0); G_STAGE2(G_SA(0, 1), a2, va10, va11);
;             G_WAIT_L(8); G_BAR; G_WAIT_L(0); G_MMA(0, 0, At, B0); G_BAR; G_SCHED;
;             G_LDB(B1, 1, 1); G_STAGE2(G_SB(1, 0), b3, vb0, vb1);
;             G_BAR; G_WAIT_L(0); G_MMA(0, 1, At, B1); G_BAR;
	s_add_u32 s46, s8, 0x40000
	s_addc_u32 s47, s9, 0
	s_add_i32 s45, s48, s23
	v_lshl_add_u64 v[142:143], s[46:47], 0, v[146:147]
	s_mov_b32 m0, s45
	s_nop 0
	global_load_lds_dwordx4 v[142:143], off
	v_lshl_add_u64 v[142:143], s[46:47], 0, v[130:131]
	s_add_i32 m0, s45, 0x2000
	s_nop 0
	global_load_lds_dwordx4 v[142:143], off
	s_waitcnt vmcnt(6)
	s_barrier
	s_setprio 1
	v_mfma_f32_16x16x32_bf16 v[54:57], v[192:195], v[160:163], v[54:57]
	v_mfma_f32_16x16x32_bf16 v[46:49], v[204:207], v[160:163], v[46:49]
	v_mfma_f32_16x16x32_bf16 v[38:41], v[192:195], v[168:171], v[38:41]
	v_mfma_f32_16x16x32_bf16 v[34:37], v[204:207], v[168:171], v[34:37]
	v_mfma_f32_16x16x32_bf16 v[22:25], v[192:195], v[176:179], v[22:25]
	v_mfma_f32_16x16x32_bf16 v[14:17], v[204:207], v[176:179], v[14:17]
	v_mfma_f32_16x16x32_bf16 v[6:9], v[192:195], v[184:187], v[6:9]
	v_mfma_f32_16x16x32_bf16 v[2:5], v[204:207], v[184:187], v[2:5]
	v_mfma_f32_16x16x32_bf16 v[54:57], v[200:203], v[164:167], v[54:57]
	v_mfma_f32_16x16x32_bf16 v[46:49], v[208:211], v[164:167], v[46:49]
	v_mfma_f32_16x16x32_bf16 v[38:41], v[200:203], v[172:175], v[38:41]
	v_mfma_f32_16x16x32_bf16 v[34:37], v[208:211], v[172:175], v[34:37]
	v_mfma_f32_16x16x32_bf16 v[22:25], v[200:203], v[180:183], v[22:25]
	v_mfma_f32_16x16x32_bf16 v[14:17], v[208:211], v[180:183], v[14:17]
	v_mfma_f32_16x16x32_bf16 v[6:9], v[200:203], v[188:191], v[6:9]
	v_mfma_f32_16x16x32_bf16 v[2:5], v[208:211], v[188:191], v[2:5]
	s_setprio 0
	s_add_i32 s45, 0, 0x18000
	v_add_u32_e32 v141, s45, v1
	s_barrier
	ds_read_b128 v[142:145], v141
	ds_read_b128 v[148:151], v141 offset:1024
	ds_read_b128 v[152:155], v141 offset:2048
	ds_read_b128 v[156:159], v141 offset:3072
	s_mov_b32 m0, s7
	v_lshl_add_u64 v[192:193], s[18:19], 0, v[132:133]
	ds_read_b128 v[160:163], v140 offset:32768
	ds_read_b128 v[164:167], v140 offset:33792
	ds_read_b128 v[168:171], v140 offset:34816
	ds_read_b128 v[172:175], v140 offset:35840
	ds_read_b128 v[176:179], v140 offset:36864
	ds_read_b128 v[180:183], v140 offset:37888
	ds_read_b128 v[184:187], v140 offset:38912
	ds_read_b128 v[188:191], v140 offset:39936
	global_load_lds_dwordx4 v[192:193], off
	v_lshl_add_u64 v[192:193], s[18:19], 0, v[134:135]
	s_mov_b32 m0, s24
	s_nop 0
	global_load_lds_dwordx4 v[192:193], off
	s_waitcnt lgkmcnt(8)
	s_barrier
	s_waitcnt lgkmcnt(0)
	s_setprio 1
	s_waitcnt lgkmcnt(0)
	v_mfma_f32_16x16x32_bf16 v[126:129], v[142:145], v[160:163], v[126:129]
	v_mfma_f32_16x16x32_bf16 v[122:125], v[152:155], v[160:163], v[122:125]
	v_mfma_f32_16x16x32_bf16 v[114:117], v[142:145], v[168:171], v[114:117]
	v_mfma_f32_16x16x32_bf16 v[106:109], v[152:155], v[168:171], v[106:109]
	v_mfma_f32_16x16x32_bf16 v[94:97], v[142:145], v[176:179], v[94:97]
	v_mfma_f32_16x16x32_bf16 v[90:93], v[152:155], v[176:179], v[90:93]
	v_mfma_f32_16x16x32_bf16 v[82:85], v[142:145], v[184:187], v[82:85]
	v_mfma_f32_16x16x32_bf16 v[74:77], v[152:155], v[184:187], v[74:77]
	v_mfma_f32_16x16x32_bf16 v[126:129], v[148:151], v[164:167], v[126:129]
	v_mfma_f32_16x16x32_bf16 v[122:125], v[156:159], v[164:167], v[122:125]
	v_mfma_f32_16x16x32_bf16 v[114:117], v[148:151], v[172:175], v[114:117]
	v_mfma_f32_16x16x32_bf16 v[106:109], v[156:159], v[172:175], v[106:109]
	v_mfma_f32_16x16x32_bf16 v[94:97], v[148:151], v[180:183], v[94:97]
	v_mfma_f32_16x16x32_bf16 v[90:93], v[156:159], v[180:183], v[90:93]
	v_mfma_f32_16x16x32_bf16 v[82:85], v[148:151], v[188:191], v[82:85]
	v_mfma_f32_16x16x32_bf16 v[74:77], v[156:159], v[188:191], v[74:77]
	s_setprio 0
	s_barrier
	s_add_i32 s18, 0, 0x1c000
	s_add_i32 s19, s45, s23
	v_add_u32_e32 v141, s18, v1
	v_lshl_add_u64 v[212:213], v[212:213], 0, s[34:35]
	s_mov_b32 m0, s19
	ds_read_b128 v[192:195], v141
	ds_read_b128 v[200:203], v141 offset:1024
	ds_read_b128 v[204:207], v141 offset:2048
	ds_read_b128 v[208:211], v141 offset:3072
	global_load_lds_dwordx4 v[212:213], off
	v_lshl_add_u64 v[212:213], v[214:215], 0, s[34:35]
	s_add_i32 m0, s19, 0x2000
	s_nop 0
	global_load_lds_dwordx4 v[212:213], off
	s_barrier
	s_waitcnt lgkmcnt(0)
	s_setprio 1
	s_waitcnt lgkmcnt(0)
	v_mfma_f32_16x16x32_bf16 v[118:121], v[192:195], v[160:163], v[118:121]
	v_mfma_f32_16x16x32_bf16 v[110:113], v[204:207], v[160:163], v[110:113]
	v_mfma_f32_16x16x32_bf16 v[102:105], v[192:195], v[168:171], v[102:105]
	v_mfma_f32_16x16x32_bf16 v[98:101], v[204:207], v[168:171], v[98:101]
	v_mfma_f32_16x16x32_bf16 v[86:89], v[192:195], v[176:179], v[86:89]
	v_mfma_f32_16x16x32_bf16 v[78:81], v[204:207], v[176:179], v[78:81]
	v_mfma_f32_16x16x32_bf16 v[70:73], v[192:195], v[184:187], v[70:73]
	v_mfma_f32_16x16x32_bf16 v[66:69], v[204:207], v[184:187], v[66:69]
	v_mfma_f32_16x16x32_bf16 v[118:121], v[200:203], v[164:167], v[118:121]
	v_mfma_f32_16x16x32_bf16 v[110:113], v[208:211], v[164:167], v[110:113]
	v_mfma_f32_16x16x32_bf16 v[102:105], v[200:203], v[172:175], v[102:105]
	v_mfma_f32_16x16x32_bf16 v[98:101], v[208:211], v[172:175], v[98:101]
	v_mfma_f32_16x16x32_bf16 v[86:89], v[200:203], v[180:183], v[86:89]
	v_mfma_f32_16x16x32_bf16 v[78:81], v[208:211], v[180:183], v[78:81]
	v_mfma_f32_16x16x32_bf16 v[70:73], v[200:203], v[188:191], v[70:73]
	v_mfma_f32_16x16x32_bf16 v[66:69], v[208:211], v[188:191], v[66:69]
	s_setprio 0
	s_mov_b32 m0, s30
	v_lshl_add_u64 v[212:213], v[216:217], 0, s[34:35]
	s_barrier
	ds_read_b128 v[160:163], v140 offset:49152
	ds_read_b128 v[164:167], v140 offset:50176
	ds_read_b128 v[168:171], v140 offset:51200
	ds_read_b128 v[172:175], v140 offset:52224
	ds_read_b128 v[176:179], v140 offset:53248
	ds_read_b128 v[180:183], v140 offset:54272
	ds_read_b128 v[184:187], v140 offset:55296
	ds_read_b128 v[188:191], v140 offset:56320
	global_load_lds_dwordx4 v[212:213], off
	v_lshl_add_u64 v[212:213], v[218:219], 0, s[34:35]
	s_mov_b32 m0, s31
	s_nop 0
	global_load_lds_dwordx4 v[212:213], off
	s_barrier
;     __device__ __forceinline__ float* mods() const { return (float*)(ws + WS_MODS); }
; #define G_STAGE2(bufoff, gbase, v0, v1) do { \
;         __builtin_amdgcn_global_load_lds((const unsigned*)((const char*)(gbase) + (v0)), (LAS unsigned*)(lds + (bufoff) + ldsw), 16, 0, 0); \
;         __builtin_amdgcn_global_load_lds((const unsigned*)((const char*)(gbase) + (v1)), (LAS unsigned*)(lds + (bufoff) + ldsw + 8192), 16, 0, 0); } while (0)
; #define G_LDA(dst, b, h) do { _Pragma("unroll") for (int m = 0; m < 4; ++m) _Pragma("unroll") for (int k = 0; k < 2; ++k) dst[m][k] = *(const LAS bf16x8*)(lds + G_SA(b, h) + aoff + m * 2048 + k * 1024); } while (0)
; #define G_WAIT_V(n) asm volatile("s_waitcnt vmcnt(" #n ")" ::: "memory")
; #define G_BAR __builtin_amdgcn_s_barrier()
; template <bool PERM, class Epi, class Sched>
; __device__ __forceinline__ void gemm_phase(LAS unsigned char* lds, const Sched& S, const Epi& E) {
;     ...
;             G_BAR; G_WAIT_L(0); G_MMA(0, 1, At, B1); G_BAR;
;             G_LDA(At, 1, 1); G_STAGE2(G_SA(1, 0), a3, va00, va01);
;             G_BAR; G_WAIT_L(0); G_MMA(1, 0, At, B0); G_BAR; G_SCHED;
;             G_STAGE2(G_SB(1, 1), b3 + hsB, vb0, vb1);
;             G_WAIT_V(6); G_BAR; G_MMA(1, 1, At, B1); G_BAR;
;     __device__ __forceinline__ void operator()(const AccT& acc, const gm::GUnit& u, int wr, int wc, int fr, int fq) const {
;         asm volatile("" : "+v"(fr), "+v"(fq));
;         const bool lat = u.pm < 256;
;         const int b = lat ? (u.pm >> 5) : 8;
;         const float* gp = mods + (size_t)b * 6144 + 2 * 1024 + u.pn * 256 + wc * 32 + 4 * fq;
;         f32x4 gv[2][2];
; #pragma unroll
;         for (int bj = 0; bj < 2; ++bj)
; #pragma unroll
;             for (int n = 0; n < 2; ++n) gv[bj][n] = *(const f32x4*)(gp + bj * 128 + n * 16);
; #pragma unroll
;         for (int q = 0; q < 4; ++q) {
;             const int ai = q >> 1, m0 = (q & 1) * 2;
;             f32x4 xv[2][2][2];
; #pragma unroll
;             for (int mi = 0; mi < 2; ++mi) {
;                 const int row = u.pm * 256 + ai * 128 + wr * 64 + (m0 + mi) * 16 + fr;
;                 const float* ip = xin + (size_t)row * DM + u.pn * 256 + wc * 32 + 4 * fq + (lat ? 0ll : din);
; #pragma unroll
;                 for (int bj = 0; bj < 2; ++bj)
; #pragma unroll
;                     for (int n = 0; n < 2; ++n) xv[mi][bj][n] = *(const f32x4*)(ip + bj * 128 + n * 16);
	s_waitcnt lgkmcnt(0)
	s_setprio 1
	s_waitcnt lgkmcnt(0)
	v_mfma_f32_16x16x32_bf16 v[62:65], v[142:145], v[160:163], v[62:65]
	v_mfma_f32_16x16x32_bf16 v[58:61], v[152:155], v[160:163], v[58:61]
	v_mfma_f32_16x16x32_bf16 v[50:53], v[142:145], v[168:171], v[50:53]
	v_mfma_f32_16x16x32_bf16 v[42:45], v[152:155], v[168:171], v[42:45]
	v_mfma_f32_16x16x32_bf16 v[30:33], v[142:145], v[176:179], v[30:33]
	v_mfma_f32_16x16x32_bf16 v[26:29], v[152:155], v[176:179], v[26:29]
	v_mfma_f32_16x16x32_bf16 v[18:21], v[142:145], v[184:187], v[18:21]
	v_mfma_f32_16x16x32_bf16 v[10:13], v[152:155], v[184:187], v[10:13]
	v_mfma_f32_16x16x32_bf16 v[62:65], v[148:151], v[164:167], v[62:65]
	v_mfma_f32_16x16x32_bf16 v[58:61], v[156:159], v[164:167], v[58:61]
	v_mfma_f32_16x16x32_bf16 v[50:53], v[148:151], v[172:175], v[50:53]
	v_mfma_f32_16x16x32_bf16 v[42:45], v[156:159], v[172:175], v[42:45]
	v_mfma_f32_16x16x32_bf16 v[30:33], v[148:151], v[180:183], v[30:33]
	v_mfma_f32_16x16x32_bf16 v[26:29], v[156:159], v[180:183], v[26:29]
	v_mfma_f32_16x16x32_bf16 v[18:21], v[148:151], v[188:191], v[18:21]
	v_mfma_f32_16x16x32_bf16 v[10:13], v[156:159], v[188:191], v[10:13]
	s_setprio 0
	s_barrier
	s_add_u32 s8, s8, 0x40080
	s_addc_u32 s9, s9, 0
	s_add_i32 s18, s18, s23
	v_lshl_add_u64 v[142:143], s[8:9], 0, v[146:147]
	s_mov_b32 m0, s18
	s_nop 0
	global_load_lds_dwordx4 v[142:143], off
	v_lshl_add_u64 v[142:143], s[8:9], 0, v[130:131]
	s_add_i32 m0, s18, 0x2000
	s_nop 0
	global_load_lds_dwordx4 v[142:143], off
	s_waitcnt vmcnt(6)
	s_barrier
	s_setprio 1
	v_mfma_f32_16x16x32_bf16 v[54:57], v[192:195], v[160:163], v[54:57]
	v_mfma_f32_16x16x32_bf16 v[46:49], v[204:207], v[160:163], v[46:49]
	v_mfma_f32_16x16x32_bf16 v[38:41], v[192:195], v[168:171], v[38:41]
	v_mfma_f32_16x16x32_bf16 v[34:37], v[204:207], v[168:171], v[34:37]
	v_mfma_f32_16x16x32_bf16 v[22:25], v[192:195], v[176:179], v[22:25]
	v_mfma_f32_16x16x32_bf16 v[14:17], v[204:207], v[176:179], v[14:17]
	v_mfma_f32_16x16x32_bf16 v[6:9], v[192:195], v[184:187], v[6:9]
	v_mfma_f32_16x16x32_bf16 v[2:5], v[204:207], v[184:187], v[2:5]
	v_mfma_f32_16x16x32_bf16 v[54:57], v[200:203], v[164:167], v[54:57]
	v_mfma_f32_16x16x32_bf16 v[46:49], v[208:211], v[164:167], v[46:49]
	v_mfma_f32_16x16x32_bf16 v[38:41], v[200:203], v[172:175], v[38:41]
	v_mfma_f32_16x16x32_bf16 v[34:37], v[208:211], v[172:175], v[34:37]
	v_mfma_f32_16x16x32_bf16 v[22:25], v[200:203], v[180:183], v[22:25]
	v_mfma_f32_16x16x32_bf16 v[14:17], v[208:211], v[180:183], v[14:17]
	v_mfma_f32_16x16x32_bf16 v[6:9], v[200:203], v[188:191], v[6:9]
	v_mfma_f32_16x16x32_bf16 v[2:5], v[208:211], v[188:191], v[2:5]
	s_setprio 0
	s_add_i32 s44, s44, 2
	s_add_u32 s42, s42, 0x100
	s_addc_u32 s43, s43, 0
	s_cmp_gt_u32 s44, 13
	s_barrier
	s_cbranch_scc0 .LBB0_862
	v_readlane_b32 s7, v254, 0
	v_mov_b32_e32 v1, v226
	v_mov_b32_e32 v146, v197
	s_add_u32 s0, s62, s7
	s_addc_u32 s2, s63, 0
	s_lshl_b32 s76, s25, 2
	v_lshlrev_b32_e32 v130, 2, v1
	s_add_u32 s8, s0, s76
	v_ashrrev_i32_e32 v131, 31, v130
	s_addc_u32 s9, s2, 0
	v_lshlrev_b64 v[148:149], 2, v[130:131]
	v_lshl_add_u64 v[130:131], s[8:9], 0, v[148:149]
	s_mov_b64 s[8:9], 0x32000
	s_mov_b32 s0, 0x32000
	v_lshl_add_u64 v[132:133], v[130:131], 0, s[8:9]
	v_add_co_u32_e32 v130, vcc, s0, v130
	v_readlane_b32 s0, v253, 24
	s_add_i32 s1, s1, s0
	v_readlane_b32 s0, v255, 6
	v_add_u32_e32 v150, s1, v146
	s_add_u32 s0, s0, s7
	v_readlane_b32 s1, v255, 7
	s_addc_u32 s1, s1, 0
	s_add_u32 s0, s0, s76
	s_addc_u32 s1, s1, 0
	v_lshl_add_u64 v[152:153], s[0:1], 0, v[148:149]
	v_readlane_b32 s0, v255, 4
	v_add_u32_e32 v170, 16, v150
	v_readlane_b32 s1, v255, 5
	v_ashrrev_i32_e32 v151, 31, v150
	v_ashrrev_i32_e32 v171, 31, v170
	v_lshl_add_u64 v[152:153], s[0:1], 2, v[152:153]
	v_lshlrev_b64 v[186:187], 12, v[150:151]
	v_lshlrev_b64 v[188:189], 12, v[170:171]
	v_addc_co_u32_e32 v131, vcc, 0, v131, vcc
	v_lshl_add_u64 v[166:167], v[152:153], 0, v[186:187]
	v_lshl_add_u64 v[182:183], v[152:153], 0, v[188:189]
	global_load_dwordx4 v[138:141], v[132:133], off offset:64
	global_load_dwordx4 v[134:137], v[132:133], off offset:512
	global_load_dwordx4 v[142:145], v[130:131], off
	s_nop 0
	global_load_dwordx4 v[130:133], v[132:133], off offset:576
	s_nop 0
	global_load_dwordx4 v[154:157], v[166:167], off
	global_load_dwordx4 v[158:161], v[166:167], off offset:64
	global_load_dwordx4 v[162:165], v[166:167], off offset:512
	s_nop 0
	global_load_dwordx4 v[166:169], v[166:167], off offset:576
	s_nop 0
	global_load_dwordx4 v[170:173], v[182:183], off
	global_load_dwordx4 v[174:177], v[182:183], off offset:64
	global_load_dwordx4 v[178:181], v[182:183], off offset:512
	s_nop 0
	global_load_dwordx4 v[182:185], v[182:183], off offset:576
	v_readlane_b32 s0, v253, 28
	v_readlane_b32 s1, v253, 29
	s_lshl_b64 s[8:9], s[60:61], 2
	s_waitcnt vmcnt(0)
;     __device__ __forceinline__ void operator()(const AccT& acc, const gm::GUnit& u, int wr, int wc, int fr, int fq) const {
;     ...
;         for (int q = 0; q < 4; ++q) {
;             const int ai = q >> 1, m0 = (q & 1) * 2;
;             f32x4 xv[2][2][2];
; #pragma unroll
;             for (int mi = 0; mi < 2; ++mi) {
;                 const int row = u.pm * 256 + ai * 128 + wr * 64 + (m0 + mi) * 16 + fr;
;                 const float* ip = xin + (size_t)row * DM + u.pn * 256 + wc * 32 + 4 * fq + (lat ? 0ll : din);
; #pragma unroll
;                 for (int bj = 0; bj < 2; ++bj)
; #pragma unroll
;                     for (int n = 0; n < 2; ++n) xv[mi][bj][n] = *(const f32x4*)(ip + bj * 128 + n * 16);
;             }
;             __builtin_amdgcn_sched_barrier(0);
; #pragma unroll
;             for (int mi = 0; mi < 2; ++mi) {
;                 const int m = m0 + mi, row = u.pm * 256 + ai * 128 + wr * 64 + m * 16 + fr;
;                 float* op = xout + (size_t)row * DM + u.pn * 256 + wc * 32 + 4 * fq + (lat ? 0ll : dout);
; #pragma unroll
;                 for (int bj = 0; bj < 2; ++bj)
; #pragma unroll
;                     for (int n = 0; n < 2; ++n) *(f32x4*)(op + bj * 128 + n * 16) = xv[mi][bj][n] + gv[bj][n] * acc[ai][bj][m][n];
;             }
;             __builtin_amdgcn_sched_barrier(0);
;         }
	v_pk_fma_f32 v[112:113], v[112:113], v[132:133], v[168:169]
	v_lshl_add_u64 v[186:187], s[0:1], 0, v[186:187]
	v_lshl_add_u64 v[186:187], v[186:187], 0, s[76:77]
	v_lshl_add_u64 v[186:187], v[186:187], 0, v[148:149]
	v_lshl_add_u64 v[186:187], v[186:187], 0, s[8:9]
	v_pk_fma_f32 v[110:111], v[110:111], v[130:131], v[166:167]
	global_store_dwordx4 v[186:187], v[110:113], off offset:576
	v_pk_fma_f32 v[120:121], v[120:121], v[136:137], v[164:165]
	v_pk_fma_f32 v[118:119], v[118:119], v[134:135], v[162:163]
	v_lshl_add_u64 v[110:111], s[0:1], 0, v[188:189]
	v_lshl_add_u64 v[110:111], v[110:111], 0, s[76:77]
	v_lshl_add_u64 v[110:111], v[110:111], 0, v[148:149]
	v_pk_fma_f32 v[128:129], v[128:129], v[144:145], v[156:157]
	v_pk_fma_f32 v[126:127], v[126:127], v[142:143], v[154:155]
	v_pk_fma_f32 v[124:125], v[124:125], v[140:141], v[160:161]
	v_pk_fma_f32 v[122:123], v[122:123], v[138:139], v[158:159]
	global_store_dwordx4 v[186:187], v[118:121], off offset:512
	v_pk_fma_f32 v[112:113], v[116:117], v[144:145], v[172:173]
	v_pk_fma_f32 v[108:109], v[108:109], v[140:141], v[176:177]
	v_lshl_add_u64 v[118:119], v[110:111], 0, s[8:9]
	v_pk_fma_f32 v[110:111], v[114:115], v[142:143], v[170:171]
	v_pk_fma_f32 v[106:107], v[106:107], v[138:139], v[174:175]
	v_pk_fma_f32 v[104:105], v[104:105], v[136:137], v[180:181]
	v_pk_fma_f32 v[102:103], v[102:103], v[134:135], v[178:179]
	v_pk_fma_f32 v[100:101], v[100:101], v[132:133], v[184:185]
	v_pk_fma_f32 v[98:99], v[98:99], v[130:131], v[182:183]
	global_store_dwordx4 v[186:187], v[126:129], off
	global_store_dwordx4 v[186:187], v[122:125], off offset:64
	global_store_dwordx4 v[118:119], v[110:113], off
	global_store_dwordx4 v[118:119], v[106:109], off offset:64
	global_store_dwordx4 v[118:119], v[102:105], off offset:512
	global_store_dwordx4 v[118:119], v[98:101], off offset:576
	s_nop 1
	v_add_u32_e32 v98, 32, v150
	v_add_u32_e32 v114, 48, v150
	v_ashrrev_i32_e32 v99, 31, v98
	v_ashrrev_i32_e32 v115, 31, v114
	v_lshlrev_b64 v[154:155], 12, v[98:99]
	v_lshlrev_b64 v[156:157], 12, v[114:115]
	v_lshl_add_u64 v[110:111], v[152:153], 0, v[154:155]
	v_lshl_add_u64 v[126:127], v[152:153], 0, v[156:157]
	global_load_dwordx4 v[98:101], v[110:111], off
	global_load_dwordx4 v[102:105], v[110:111], off offset:64
	global_load_dwordx4 v[106:109], v[110:111], off offset:512
	s_nop 0
	global_load_dwordx4 v[110:113], v[110:111], off offset:576
	s_nop 0
	global_load_dwordx4 v[114:117], v[126:127], off
	global_load_dwordx4 v[118:121], v[126:127], off offset:64
	global_load_dwordx4 v[122:125], v[126:127], off offset:512
	s_nop 0
	global_load_dwordx4 v[126:129], v[126:127], off offset:576
	v_lshl_add_u64 v[154:155], s[0:1], 0, v[154:155]
	v_lshl_add_u64 v[154:155], v[154:155], 0, s[76:77]
	v_lshl_add_u64 v[154:155], v[154:155], 0, v[148:149]
	v_lshl_add_u64 v[154:155], v[154:155], 0, s[8:9]
	s_waitcnt vmcnt(0)
	v_pk_fma_f32 v[80:81], v[80:81], v[132:133], v[112:113]
	v_pk_fma_f32 v[78:79], v[78:79], v[130:131], v[110:111]
	global_store_dwordx4 v[154:155], v[78:81], off offset:576
	v_pk_fma_f32 v[88:89], v[88:89], v[136:137], v[108:109]
	v_pk_fma_f32 v[86:87], v[86:87], v[134:135], v[106:107]
	v_lshl_add_u64 v[78:79], s[0:1], 0, v[156:157]
	v_lshl_add_u64 v[78:79], v[78:79], 0, s[76:77]
	v_lshl_add_u64 v[78:79], v[78:79], 0, v[148:149]
	v_pk_fma_f32 v[96:97], v[96:97], v[144:145], v[100:101]
	v_pk_fma_f32 v[94:95], v[94:95], v[142:143], v[98:99]
	v_pk_fma_f32 v[92:93], v[92:93], v[140:141], v[104:105]
	v_pk_fma_f32 v[90:91], v[90:91], v[138:139], v[102:103]
	global_store_dwordx4 v[154:155], v[86:89], off offset:512
	v_pk_fma_f32 v[80:81], v[84:85], v[144:145], v[116:117]
	v_pk_fma_f32 v[76:77], v[76:77], v[140:141], v[120:121]
	v_lshl_add_u64 v[86:87], v[78:79], 0, s[8:9]
	v_pk_fma_f32 v[78:79], v[82:83], v[142:143], v[114:115]
	v_pk_fma_f32 v[74:75], v[74:75], v[138:139], v[118:119]
	v_pk_fma_f32 v[72:73], v[72:73], v[136:137], v[124:125]
	v_pk_fma_f32 v[70:71], v[70:71], v[134:135], v[122:123]
	v_pk_fma_f32 v[68:69], v[68:69], v[132:133], v[128:129]
	v_pk_fma_f32 v[66:67], v[66:67], v[130:131], v[126:127]
	global_store_dwordx4 v[154:155], v[94:97], off
	global_store_dwordx4 v[154:155], v[90:93], off offset:64
	global_store_dwordx4 v[86:87], v[78:81], off
	global_store_dwordx4 v[86:87], v[74:77], off offset:64
	global_store_dwordx4 v[86:87], v[70:73], off offset:512
	global_store_dwordx4 v[86:87], v[66:69], off offset:576
	s_nop 1
	v_add_u32_e32 v66, 0x80, v150
	v_add_u32_e32 v82, 0x90, v150
	v_ashrrev_i32_e32 v67, 31, v66
	v_ashrrev_i32_e32 v83, 31, v82
	v_lshlrev_b64 v[98:99], 12, v[66:67]
	v_lshlrev_b64 v[100:101], 12, v[82:83]
	v_lshl_add_u64 v[78:79], v[152:153], 0, v[98:99]
	v_lshl_add_u64 v[94:95], v[152:153], 0, v[100:101]
	global_load_dwordx4 v[66:69], v[78:79], off
	global_load_dwordx4 v[70:73], v[78:79], off offset:64
	global_load_dwordx4 v[74:77], v[78:79], off offset:512
	s_nop 0
	global_load_dwordx4 v[78:81], v[78:79], off offset:576
	s_nop 0
	global_load_dwordx4 v[82:85], v[94:95], off
	global_load_dwordx4 v[86:89], v[94:95], off offset:64
	global_load_dwordx4 v[90:93], v[94:95], off offset:512
	s_nop 0
	global_load_dwordx4 v[94:97], v[94:95], off offset:576
	v_lshl_add_u64 v[98:99], s[0:1], 0, v[98:99]
	v_lshl_add_u64 v[98:99], v[98:99], 0, s[76:77]
	v_lshl_add_u64 v[98:99], v[98:99], 0, v[148:149]
	v_lshl_add_u64 v[98:99], v[98:99], 0, s[8:9]
	s_waitcnt vmcnt(0)
;     __device__ __forceinline__ void operator()(const AccT& acc, const gm::GUnit& u, int wr, int wc, int fr, int fq) const {
;     ...
;         for (int q = 0; q < 4; ++q) {
;             const int ai = q >> 1, m0 = (q & 1) * 2;
;             f32x4 xv[2][2][2];
; #pragma unroll
;             for (int mi = 0; mi < 2; ++mi) {
;                 const int row = u.pm * 256 + ai * 128 + wr * 64 + (m0 + mi) * 16 + fr;
;                 const float* ip = xin + (size_t)row * DM + u.pn * 256 + wc * 32 + 4 * fq + (lat ? 0ll : din);
; #pragma unroll
;                 for (int bj = 0; bj < 2; ++bj)
; #pragma unroll
;                     for (int n = 0; n < 2; ++n) xv[mi][bj][n] = *(const f32x4*)(ip + bj * 128 + n * 16);
;             }
;             __builtin_amdgcn_sched_barrier(0);
; #pragma unroll
;             for (int mi = 0; mi < 2; ++mi) {
;                 const int m = m0 + mi, row = u.pm * 256 + ai * 128 + wr * 64 + m * 16 + fr;
;                 float* op = xout + (size_t)row * DM + u.pn * 256 + wc * 32 + 4 * fq + (lat ? 0ll : dout);
; #pragma unroll
;                 for (int bj = 0; bj < 2; ++bj)
; #pragma unroll
;                     for (int n = 0; n < 2; ++n) *(f32x4*)(op + bj * 128 + n * 16) = xv[mi][bj][n] + gv[bj][n] * acc[ai][bj][m][n];
;             }
;             __builtin_amdgcn_sched_barrier(0);
;         }
	v_pk_fma_f32 v[48:49], v[48:49], v[132:133], v[80:81]
	v_pk_fma_f32 v[46:47], v[46:47], v[130:131], v[78:79]
	global_store_dwordx4 v[98:99], v[46:49], off offset:576
	v_pk_fma_f32 v[56:57], v[56:57], v[136:137], v[76:77]
	v_pk_fma_f32 v[54:55], v[54:55], v[134:135], v[74:75]
	v_lshl_add_u64 v[46:47], s[0:1], 0, v[100:101]
	v_lshl_add_u64 v[46:47], v[46:47], 0, s[76:77]
	v_lshl_add_u64 v[46:47], v[46:47], 0, v[148:149]
	v_pk_fma_f32 v[64:65], v[64:65], v[144:145], v[68:69]
	v_pk_fma_f32 v[62:63], v[62:63], v[142:143], v[66:67]
	v_pk_fma_f32 v[60:61], v[60:61], v[140:141], v[72:73]
	v_pk_fma_f32 v[58:59], v[58:59], v[138:139], v[70:71]
	global_store_dwordx4 v[98:99], v[54:57], off offset:512
	v_pk_fma_f32 v[48:49], v[52:53], v[144:145], v[84:85]
	v_pk_fma_f32 v[44:45], v[44:45], v[140:141], v[88:89]
	v_lshl_add_u64 v[54:55], v[46:47], 0, s[8:9]
	v_pk_fma_f32 v[46:47], v[50:51], v[142:143], v[82:83]
	v_pk_fma_f32 v[42:43], v[42:43], v[138:139], v[86:87]
	v_pk_fma_f32 v[40:41], v[40:41], v[136:137], v[92:93]
	v_pk_fma_f32 v[38:39], v[38:39], v[134:135], v[90:91]
	v_pk_fma_f32 v[36:37], v[36:37], v[132:133], v[96:97]
	v_pk_fma_f32 v[34:35], v[34:35], v[130:131], v[94:95]
	global_store_dwordx4 v[98:99], v[62:65], off
	global_store_dwordx4 v[98:99], v[58:61], off offset:64
	global_store_dwordx4 v[54:55], v[46:49], off
	global_store_dwordx4 v[54:55], v[42:45], off offset:64
	global_store_dwordx4 v[54:55], v[38:41], off offset:512
	global_store_dwordx4 v[54:55], v[34:37], off offset:576
	s_nop 1
	v_add_u32_e32 v34, 0xa0, v150
	v_add_u32_e32 v50, 0xb0, v150
	v_ashrrev_i32_e32 v35, 31, v34
	v_ashrrev_i32_e32 v51, 31, v50
	v_lshlrev_b64 v[66:67], 12, v[34:35]
	v_lshlrev_b64 v[68:69], 12, v[50:51]
	v_lshl_add_u64 v[46:47], v[152:153], 0, v[66:67]
	v_lshl_add_u64 v[62:63], v[152:153], 0, v[68:69]
	global_load_dwordx4 v[34:37], v[46:47], off
	global_load_dwordx4 v[38:41], v[46:47], off offset:64
	global_load_dwordx4 v[42:45], v[46:47], off offset:512
	s_nop 0
	global_load_dwordx4 v[46:49], v[46:47], off offset:576
	s_nop 0
	global_load_dwordx4 v[50:53], v[62:63], off
	global_load_dwordx4 v[54:57], v[62:63], off offset:64
	global_load_dwordx4 v[58:61], v[62:63], off offset:512
	s_nop 0
	global_load_dwordx4 v[62:65], v[62:63], off offset:576
	v_lshl_add_u64 v[66:67], s[0:1], 0, v[66:67]
	v_lshl_add_u64 v[66:67], v[66:67], 0, s[76:77]
	v_lshl_add_u64 v[66:67], v[66:67], 0, v[148:149]
	v_lshl_add_u64 v[66:67], v[66:67], 0, s[8:9]
	s_waitcnt vmcnt(0)
	v_pk_fma_f32 v[16:17], v[16:17], v[132:133], v[48:49]
	v_pk_fma_f32 v[14:15], v[14:15], v[130:131], v[46:47]
	global_store_dwordx4 v[66:67], v[14:17], off offset:576
	v_pk_fma_f32 v[24:25], v[24:25], v[136:137], v[44:45]
	v_pk_fma_f32 v[22:23], v[22:23], v[134:135], v[42:43]
	v_lshl_add_u64 v[14:15], s[0:1], 0, v[68:69]
	v_lshl_add_u64 v[14:15], v[14:15], 0, s[76:77]
	v_lshl_add_u64 v[14:15], v[14:15], 0, v[148:149]
	v_pk_fma_f32 v[32:33], v[32:33], v[144:145], v[36:37]
	v_pk_fma_f32 v[30:31], v[30:31], v[142:143], v[34:35]
	v_pk_fma_f32 v[28:29], v[28:29], v[140:141], v[40:41]
	v_pk_fma_f32 v[26:27], v[26:27], v[138:139], v[38:39]
	global_store_dwordx4 v[66:67], v[22:25], off offset:512
	v_pk_fma_f32 v[16:17], v[20:21], v[144:145], v[52:53]
	v_pk_fma_f32 v[12:13], v[12:13], v[140:141], v[56:57]
	v_lshl_add_u64 v[22:23], v[14:15], 0, s[8:9]
	v_pk_fma_f32 v[14:15], v[18:19], v[142:143], v[50:51]
	v_pk_fma_f32 v[10:11], v[10:11], v[138:139], v[54:55]
	v_pk_fma_f32 v[8:9], v[8:9], v[136:137], v[60:61]
	v_pk_fma_f32 v[6:7], v[6:7], v[134:135], v[58:59]
	v_pk_fma_f32 v[4:5], v[4:5], v[132:133], v[64:65]
	v_pk_fma_f32 v[2:3], v[2:3], v[130:131], v[62:63]
	global_store_dwordx4 v[66:67], v[30:33], off
	global_store_dwordx4 v[66:67], v[26:29], off offset:64
	global_store_dwordx4 v[22:23], v[14:17], off
	global_store_dwordx4 v[22:23], v[10:13], off offset:64
	global_store_dwordx4 v[22:23], v[6:9], off offset:512
	global_store_dwordx4 v[22:23], v[2:5], off offset:576
	s_waitcnt vmcnt(0)
	s_cmpk_lt_u32 s22, 0x100
	s_cbranch_scc0 .LBB0_865
	s_barrier

; #define G_STAGE2(bufoff, gbase, v0, v1) do { \
;         __builtin_amdgcn_global_load_lds((const unsigned*)((const char*)(gbase) + (v0)), (LAS unsigned*)(lds + (bufoff) + ldsw), 16, 0, 0); \
;         __builtin_amdgcn_global_load_lds((const unsigned*)((const char*)(gbase) + (v1)), (LAS unsigned*)(lds + (bufoff) + ldsw + 8192), 16, 0, 0); } while (0)
; #define G_LDA(dst, b, h) do { _Pragma("unroll") for (int m = 0; m < 4; ++m) _Pragma("unroll") for (int k = 0; k < 2; ++k) dst[m][k] = *(const LAS bf16x8*)(lds + G_SA(b, h) + aoff + m * 2048 + k * 1024); } while (0)
; #define G_LDB(dst, b, h) do { _Pragma("unroll") for (int n = 0; n < 2; ++n) _Pragma("unroll") for (int k = 0; k < 2; ++k) dst[n][k] = *(const LAS bf16x8*)(lds + G_SB(b, h) + boff + n * 2048 + k * 1024); } while (0)
; #define G_MMA(ai, bj, At, Bt) do { __builtin_amdgcn_s_setprio(1); _Pragma("unroll") for (int m = 0; m < 4; ++m) _Pragma("unroll") for (int n = 0; n < 2; ++n) _Pragma("unroll") for (int k = 0; k < 2; ++k) \
;         acc[ai][bj][m][n] = __builtin_amdgcn_mfma_f32_16x16x32_bf16(Bt[n][k], At[m][k], acc[ai][bj][m][n], 0, 0, 0); __builtin_amdgcn_s_setprio(0); } while (0)
; template <bool PERM, class Epi, class Sched>
; __device__ __forceinline__ void gemm_phase(LAS unsigned char* lds, const Sched& S, const Epi& E) {
;     ...
;             const char* a1 = cA + (size_t)(t + 1) * kstep;
;             G_LDB(B0, 0, 0); G_SCHED; G_LDA(At, 0, 0); G_STAGE2(G_SA(1, 1), a1, va10, va11);
;             const char* a2 = last ? nA : cA + (size_t)(t + 2) * kstep; const char* b2 = last ? nB : cB + (size_t)(t + 2) * kstep;
;             if (last) {
;                 if (Sched::GATHER_A) { va00 = na00; va01 = na01; va10 = na10; va11 = na11; vb0 = nb0; vb1 = nb1; hsB = nhsB; }
;                 else if (has_next) G_OFFS(nxt, va00, va01, va10, va11, vb0, vb1, hsB);
;             }
;             const char* a3 = a2 + kstep; const char* b3 = b2 + kstep;
;             G_WAIT_L(8); G_BAR; G_WAIT_L(0); G_MMA(0, 0, At, B0); G_BAR; G_SCHED;
;             G_LDB(B1, 0, 1); G_STAGE2(G_SB(0, 0), b2, vb0, vb1);
;             G_BAR; G_WAIT_L(0); G_MMA(0, 1, At, B1); G_BAR;
;             G_LDA(At, 0, 1); G_STAGE2(G_SA(0, 0), a2, va00, va01);
;             G_BAR; G_WAIT_L(0); G_MMA(1, 0, At, B0); G_BAR; G_SCHED;
;             G_STAGE2(G_SB(0, 1), b2 + hsB, vb0, vb1);
;             G_WAIT_V(6); G_BAR; G_MMA(1, 1, At, B1); G_BAR;
.LBB0_1756:
	s_add_u32 s18, s8, 0x100
	s_addc_u32 s19, s9, 0
	s_and_b64 s[24:25], s[22:23], exec
	s_cselect_b32 s24, 0, s18
	s_cselect_b32 s25, 0, s19
	s_add_u32 s24, s48, s24
	s_addc_u32 s25, s49, s25
	s_add_u32 s29, s2, s8
	s_addc_u32 s44, s7, s9
	s_and_b64 s[8:9], s[22:23], exec
	s_cselect_b32 s9, s55, s44
	s_cselect_b32 s8, s54, s29
	s_waitcnt lgkmcnt(8)
	s_barrier
	s_waitcnt lgkmcnt(0)
	s_setprio 1
	s_waitcnt lgkmcnt(0)
	v_mfma_f32_16x16x32_bf16 v[134:137], v[74:77], v[172:175], v[134:137]
	v_mfma_f32_16x16x32_bf16 v[130:133], v[138:141], v[172:175], v[130:133]
	v_mfma_f32_16x16x32_bf16 v[126:129], v[74:77], v[164:167], v[126:129]
	v_mfma_f32_16x16x32_bf16 v[122:125], v[138:141], v[164:167], v[122:125]
	v_mfma_f32_16x16x32_bf16 v[118:121], v[74:77], v[156:159], v[118:121]
	v_mfma_f32_16x16x32_bf16 v[114:117], v[138:141], v[156:159], v[114:117]
	v_mfma_f32_16x16x32_bf16 v[110:113], v[74:77], v[148:151], v[110:113]
	v_mfma_f32_16x16x32_bf16 v[106:109], v[138:141], v[148:151], v[106:109]
	v_mfma_f32_16x16x32_bf16 v[134:137], v[78:81], v[176:179], v[134:137]
	v_mfma_f32_16x16x32_bf16 v[130:133], v[142:145], v[176:179], v[130:133]
	v_mfma_f32_16x16x32_bf16 v[126:129], v[78:81], v[168:171], v[126:129]
	v_mfma_f32_16x16x32_bf16 v[122:125], v[142:145], v[168:171], v[122:125]
	v_mfma_f32_16x16x32_bf16 v[118:121], v[78:81], v[160:163], v[118:121]
	v_mfma_f32_16x16x32_bf16 v[114:117], v[142:145], v[160:163], v[114:117]
	v_mfma_f32_16x16x32_bf16 v[110:113], v[78:81], v[152:155], v[110:113]
	v_mfma_f32_16x16x32_bf16 v[106:109], v[142:145], v[152:155], v[106:109]
	s_setprio 0
	s_barrier
	s_add_i32 s29, 0, 0x14000
	s_mov_b32 m0, s57
	v_add_u32_e32 v181, s29, v1
	ds_read_b128 v[206:209], v181
	ds_read_b128 v[210:213], v181 offset:1024
	ds_read_b128 v[214:217], v181 offset:2048
	ds_read_b128 v[218:221], v181 offset:3072
	global_load_lds_dwordx4 v146, s[8:9]
	s_mov_b32 m0, s58
	v_mov_b32_e32 v189, v147
	global_load_lds_dwordx4 v188, s[8:9]
	v_lshl_add_u64 v[222:223], s[8:9], 0, v[146:147]
	v_lshl_add_u64 v[224:225], s[8:9], 0, v[188:189]
	s_barrier
	s_waitcnt lgkmcnt(0)
	s_setprio 1
	s_waitcnt lgkmcnt(0)
	v_mfma_f32_16x16x32_bf16 v[62:65], v[206:209], v[172:175], v[62:65]
	v_mfma_f32_16x16x32_bf16 v[58:61], v[214:217], v[172:175], v[58:61]
	v_mfma_f32_16x16x32_bf16 v[54:57], v[206:209], v[164:167], v[54:57]
	v_mfma_f32_16x16x32_bf16 v[50:53], v[214:217], v[164:167], v[50:53]
	v_mfma_f32_16x16x32_bf16 v[46:49], v[206:209], v[156:159], v[46:49]
	v_mfma_f32_16x16x32_bf16 v[42:45], v[214:217], v[156:159], v[42:45]
	v_mfma_f32_16x16x32_bf16 v[38:41], v[206:209], v[148:151], v[38:41]
	v_mfma_f32_16x16x32_bf16 v[34:37], v[214:217], v[148:151], v[34:37]
	v_mfma_f32_16x16x32_bf16 v[62:65], v[210:213], v[176:179], v[62:65]
	v_mfma_f32_16x16x32_bf16 v[58:61], v[218:221], v[176:179], v[58:61]
	v_mfma_f32_16x16x32_bf16 v[54:57], v[210:213], v[168:171], v[54:57]
	v_mfma_f32_16x16x32_bf16 v[50:53], v[218:221], v[168:171], v[50:53]
	v_mfma_f32_16x16x32_bf16 v[46:49], v[210:213], v[160:163], v[46:49]
	v_mfma_f32_16x16x32_bf16 v[42:45], v[218:221], v[160:163], v[42:45]
	v_mfma_f32_16x16x32_bf16 v[38:41], v[210:213], v[152:155], v[38:41]
	v_mfma_f32_16x16x32_bf16 v[34:37], v[218:221], v[152:155], v[34:37]
	s_setprio 0
	s_mov_b32 m0, s41
	s_barrier
	ds_read_b128 v[148:151], v199 offset:16384
	ds_read_b128 v[152:155], v199 offset:17408
	ds_read_b128 v[156:159], v199 offset:18432
	ds_read_b128 v[160:163], v199 offset:19456
	ds_read_b128 v[164:167], v199 offset:20480
	ds_read_b128 v[168:171], v199 offset:21504
	ds_read_b128 v[172:175], v199 offset:22528
	ds_read_b128 v[176:179], v199 offset:23552
	global_load_lds_dwordx4 v180, s[24:25]
	s_mov_b32 m0, s59
	v_mov_b32_e32 v181, v147
	global_load_lds_dwordx4 v182, s[24:25]
	v_mov_b32_e32 v183, v147
	v_lshl_add_u64 v[234:235], s[24:25], 0, v[180:181]
	v_lshl_add_u64 v[238:239], s[24:25], 0, v[182:183]
	s_barrier
	s_waitcnt lgkmcnt(0)
	s_setprio 1
	s_waitcnt lgkmcnt(0)
	v_mfma_f32_16x16x32_bf16 v[102:105], v[74:77], v[148:151], v[102:105]
	v_mfma_f32_16x16x32_bf16 v[98:101], v[138:141], v[148:151], v[98:101]
	v_mfma_f32_16x16x32_bf16 v[94:97], v[74:77], v[156:159], v[94:97]
	v_mfma_f32_16x16x32_bf16 v[90:93], v[138:141], v[156:159], v[90:93]
	v_mfma_f32_16x16x32_bf16 v[86:89], v[74:77], v[164:167], v[86:89]
	v_mfma_f32_16x16x32_bf16 v[82:85], v[138:141], v[164:167], v[82:85]
	v_mfma_f32_16x16x32_bf16 v[70:73], v[74:77], v[172:175], v[70:73]
	v_mfma_f32_16x16x32_bf16 v[66:69], v[138:141], v[172:175], v[66:69]
	v_mfma_f32_16x16x32_bf16 v[102:105], v[78:81], v[152:155], v[102:105]
	v_mfma_f32_16x16x32_bf16 v[98:101], v[142:145], v[152:155], v[98:101]
	v_mfma_f32_16x16x32_bf16 v[94:97], v[78:81], v[160:163], v[94:97]
	v_mfma_f32_16x16x32_bf16 v[90:93], v[142:145], v[160:163], v[90:93]
	v_mfma_f32_16x16x32_bf16 v[86:89], v[78:81], v[168:171], v[86:89]
	v_mfma_f32_16x16x32_bf16 v[82:85], v[142:145], v[168:171], v[82:85]
	v_mfma_f32_16x16x32_bf16 v[70:73], v[78:81], v[176:179], v[70:73]
	v_mfma_f32_16x16x32_bf16 v[66:69], v[142:145], v[176:179], v[66:69]
	s_setprio 0
	s_barrier
	s_add_u32 s22, s8, 0x40000
	s_addc_u32 s23, s9, 0
	s_add_i32 s29, s29, s40
	s_mov_b32 m0, s29
	s_nop 0
	global_load_lds_dwordx4 v146, s[22:23]
	s_add_i32 m0, s29, 0x2000
	s_nop 0
	global_load_lds_dwordx4 v188, s[22:23]
	s_waitcnt vmcnt(6)
	s_barrier
; #define G_STAGE2(bufoff, gbase, v0, v1) do { \
;         __builtin_amdgcn_global_load_lds((const unsigned*)((const char*)(gbase) + (v0)), (LAS unsigned*)(lds + (bufoff) + ldsw), 16, 0, 0); \
;         __builtin_amdgcn_global_load_lds((const unsigned*)((const char*)(gbase) + (v1)), (LAS unsigned*)(lds + (bufoff) + ldsw + 8192), 16, 0, 0); } while (0)
; #define G_LDA(dst, b, h) do { _Pragma("unroll") for (int m = 0; m < 4; ++m) _Pragma("unroll") for (int k = 0; k < 2; ++k) dst[m][k] = *(const LAS bf16x8*)(lds + G_SA(b, h) + aoff + m * 2048 + k * 1024); } while (0)
; #define G_LDB(dst, b, h) do { _Pragma("unroll") for (int n = 0; n < 2; ++n) _Pragma("unroll") for (int k = 0; k < 2; ++k) dst[n][k] = *(const LAS bf16x8*)(lds + G_SB(b, h) + boff + n * 2048 + k * 1024); } while (0)
; #define G_MMA(ai, bj, At, Bt) do { __builtin_amdgcn_s_setprio(1); _Pragma("unroll") for (int m = 0; m < 4; ++m) _Pragma("unroll") for (int n = 0; n < 2; ++n) _Pragma("unroll") for (int k = 0; k < 2; ++k) \
;         acc[ai][bj][m][n] = __builtin_amdgcn_mfma_f32_16x16x32_bf16(Bt[n][k], At[m][k], acc[ai][bj][m][n], 0, 0, 0); __builtin_amdgcn_s_setprio(0); } while (0)
; #define G_WAIT_V(n) asm volatile("s_waitcnt vmcnt(" #n ")" ::: "memory")
; #define G_WAIT_L(n) asm volatile("s_waitcnt lgkmcnt(" #n ")" ::: "memory")
; #define G_BAR __builtin_amdgcn_s_barrier()
; #define G_SCHED __builtin_amdgcn_sched_barrier(0)
; template <bool PERM, class Epi, class Sched>
; __device__ __forceinline__ void gemm_phase(LAS unsigned char* lds, const Sched& S, const Epi& E) {
;     ...
;             G_WAIT_V(6); G_BAR; G_MMA(1, 1, At, B1); G_BAR;
;             G_LDB(B0, 1, 0); G_SCHED; G_LDA(At, 1, 0); G_STAGE2(G_SA(0, 1), a2, va10, va11);
;             G_WAIT_L(8); G_BAR; G_WAIT_L(0); G_MMA(0, 0, At, B0); G_BAR; G_SCHED;
;             G_LDB(B1, 1, 1); G_STAGE2(G_SB(1, 0), b3, vb0, vb1);
;             G_BAR; G_WAIT_L(0); G_MMA(0, 1, At, B1); G_BAR;
	s_setprio 1
	v_mfma_f32_16x16x32_bf16 v[30:33], v[206:209], v[148:151], v[30:33]
	v_mfma_f32_16x16x32_bf16 v[26:29], v[214:217], v[148:151], v[26:29]
	v_mfma_f32_16x16x32_bf16 v[22:25], v[206:209], v[156:159], v[22:25]
	v_mfma_f32_16x16x32_bf16 v[18:21], v[214:217], v[156:159], v[18:21]
	v_mfma_f32_16x16x32_bf16 v[14:17], v[206:209], v[164:167], v[14:17]
	v_mfma_f32_16x16x32_bf16 v[10:13], v[214:217], v[164:167], v[10:13]
	v_mfma_f32_16x16x32_bf16 v[6:9], v[206:209], v[172:175], v[6:9]
	v_mfma_f32_16x16x32_bf16 v[2:5], v[214:217], v[172:175], v[2:5]
	v_mfma_f32_16x16x32_bf16 v[30:33], v[210:213], v[152:155], v[30:33]
	v_mfma_f32_16x16x32_bf16 v[26:29], v[218:221], v[152:155], v[26:29]
	v_mfma_f32_16x16x32_bf16 v[22:25], v[210:213], v[160:163], v[22:25]
	v_mfma_f32_16x16x32_bf16 v[18:21], v[218:221], v[160:163], v[18:21]
	v_mfma_f32_16x16x32_bf16 v[14:17], v[210:213], v[168:171], v[14:17]
	v_mfma_f32_16x16x32_bf16 v[10:13], v[218:221], v[168:171], v[10:13]
	v_mfma_f32_16x16x32_bf16 v[6:9], v[210:213], v[176:179], v[6:9]
	v_mfma_f32_16x16x32_bf16 v[2:5], v[218:221], v[176:179], v[2:5]
	s_setprio 0
	s_add_i32 s22, 0, 0x18000
	v_add_u32_e32 v142, s22, v1
	s_barrier
	ds_read_b128 v[74:77], v142
	ds_read_b128 v[78:81], v142 offset:1024
	ds_read_b128 v[138:141], v142 offset:2048
	ds_read_b128 v[142:145], v142 offset:3072
	s_mov_b32 m0, s60
	v_lshl_add_u64 v[200:201], s[24:25], 0, v[200:201]
	ds_read_b128 v[148:151], v199 offset:32768
	ds_read_b128 v[152:155], v199 offset:33792
	ds_read_b128 v[156:159], v199 offset:34816
	ds_read_b128 v[160:163], v199 offset:35840
	ds_read_b128 v[164:167], v199 offset:36864
	ds_read_b128 v[168:171], v199 offset:37888
	ds_read_b128 v[172:175], v199 offset:38912
	ds_read_b128 v[176:179], v199 offset:39936
	global_load_lds_dwordx4 v[200:201], off
	v_lshl_add_u64 v[194:195], s[24:25], 0, v[194:195]
	s_mov_b32 m0, s61
	s_nop 0
	global_load_lds_dwordx4 v[194:195], off
	s_waitcnt lgkmcnt(8)
	s_barrier
	s_waitcnt lgkmcnt(0)
	s_setprio 1
	s_waitcnt lgkmcnt(0)
	v_mfma_f32_16x16x32_bf16 v[134:137], v[74:77], v[148:151], v[134:137]
	v_mfma_f32_16x16x32_bf16 v[130:133], v[138:141], v[148:151], v[130:133]
	v_mfma_f32_16x16x32_bf16 v[126:129], v[74:77], v[156:159], v[126:129]
	v_mfma_f32_16x16x32_bf16 v[122:125], v[138:141], v[156:159], v[122:125]
	v_mfma_f32_16x16x32_bf16 v[118:121], v[74:77], v[164:167], v[118:121]
	v_mfma_f32_16x16x32_bf16 v[114:117], v[138:141], v[164:167], v[114:117]
	v_mfma_f32_16x16x32_bf16 v[110:113], v[74:77], v[172:175], v[110:113]
	v_mfma_f32_16x16x32_bf16 v[106:109], v[138:141], v[172:175], v[106:109]
	v_mfma_f32_16x16x32_bf16 v[134:137], v[78:81], v[152:155], v[134:137]
	v_mfma_f32_16x16x32_bf16 v[130:133], v[142:145], v[152:155], v[130:133]
	v_mfma_f32_16x16x32_bf16 v[126:129], v[78:81], v[160:163], v[126:129]
	v_mfma_f32_16x16x32_bf16 v[122:125], v[142:145], v[160:163], v[122:125]
	v_mfma_f32_16x16x32_bf16 v[118:121], v[78:81], v[168:171], v[118:121]
	v_mfma_f32_16x16x32_bf16 v[114:117], v[142:145], v[168:171], v[114:117]
	v_mfma_f32_16x16x32_bf16 v[110:113], v[78:81], v[176:179], v[110:113]
	v_mfma_f32_16x16x32_bf16 v[106:109], v[142:145], v[176:179], v[106:109]
	s_setprio 0
	s_barrier
	s_add_i32 s23, 0, 0x1c000
	s_add_i32 s22, s22, s40
	v_add_u32_e32 v181, s23, v1
	v_lshl_add_u64 v[194:195], v[222:223], 0, s[34:35]
	s_mov_b32 m0, s22
	ds_read_b128 v[206:209], v181
	ds_read_b128 v[210:213], v181 offset:1024
	ds_read_b128 v[214:217], v181 offset:2048
	ds_read_b128 v[218:221], v181 offset:3072
	global_load_lds_dwordx4 v[194:195], off
	v_lshl_add_u64 v[194:195], v[224:225], 0, s[34:35]
	s_add_i32 m0, s22, 0x2000
	s_nop 0
	global_load_lds_dwordx4 v[194:195], off
	s_barrier
; #define G_STAGE2(bufoff, gbase, v0, v1) do { \
;         __builtin_amdgcn_global_load_lds((const unsigned*)((const char*)(gbase) + (v0)), (LAS unsigned*)(lds + (bufoff) + ldsw), 16, 0, 0); \
;         __builtin_amdgcn_global_load_lds((const unsigned*)((const char*)(gbase) + (v1)), (LAS unsigned*)(lds + (bufoff) + ldsw + 8192), 16, 0, 0); } while (0)
; #define G_LDA(dst, b, h) do { _Pragma("unroll") for (int m = 0; m < 4; ++m) _Pragma("unroll") for (int k = 0; k < 2; ++k) dst[m][k] = *(const LAS bf16x8*)(lds + G_SA(b, h) + aoff + m * 2048 + k * 1024); } while (0)
; #define G_MMA(ai, bj, At, Bt) do { __builtin_amdgcn_s_setprio(1); _Pragma("unroll") for (int m = 0; m < 4; ++m) _Pragma("unroll") for (int n = 0; n < 2; ++n) _Pragma("unroll") for (int k = 0; k < 2; ++k) \
;         acc[ai][bj][m][n] = __builtin_amdgcn_mfma_f32_16x16x32_bf16(Bt[n][k], At[m][k], acc[ai][bj][m][n], 0, 0, 0); __builtin_amdgcn_s_setprio(0); } while (0)
; #define G_WAIT_V(n) asm volatile("s_waitcnt vmcnt(" #n ")" ::: "memory")
; #define G_WAIT_L(n) asm volatile("s_waitcnt lgkmcnt(" #n ")" ::: "memory")
; #define G_BAR __builtin_amdgcn_s_barrier()
; #define G_SCHED __builtin_amdgcn_sched_barrier(0)
; template <bool PERM, class Epi, class Sched>
; __device__ __forceinline__ void gemm_phase(LAS unsigned char* lds, const Sched& S, const Epi& E) {
;     ...
;             G_BAR; G_WAIT_L(0); G_MMA(0, 1, At, B1); G_BAR;
;             G_LDA(At, 1, 1); G_STAGE2(G_SA(1, 0), a3, va00, va01);
;             G_BAR; G_WAIT_L(0); G_MMA(1, 0, At, B0); G_BAR; G_SCHED;
;             G_STAGE2(G_SB(1, 1), b3 + hsB, vb0, vb1);
;             G_WAIT_V(6); G_BAR; G_MMA(1, 1, At, B1); G_BAR;
	s_waitcnt lgkmcnt(0)
	s_setprio 1
	s_waitcnt lgkmcnt(0)
	v_mfma_f32_16x16x32_bf16 v[62:65], v[206:209], v[148:151], v[62:65]
	v_mfma_f32_16x16x32_bf16 v[58:61], v[214:217], v[148:151], v[58:61]
	v_mfma_f32_16x16x32_bf16 v[54:57], v[206:209], v[156:159], v[54:57]
	v_mfma_f32_16x16x32_bf16 v[50:53], v[214:217], v[156:159], v[50:53]
	v_mfma_f32_16x16x32_bf16 v[46:49], v[206:209], v[164:167], v[46:49]
	v_mfma_f32_16x16x32_bf16 v[42:45], v[214:217], v[164:167], v[42:45]
	v_mfma_f32_16x16x32_bf16 v[38:41], v[206:209], v[172:175], v[38:41]
	v_mfma_f32_16x16x32_bf16 v[34:37], v[214:217], v[172:175], v[34:37]
	v_mfma_f32_16x16x32_bf16 v[62:65], v[210:213], v[152:155], v[62:65]
	v_mfma_f32_16x16x32_bf16 v[58:61], v[218:221], v[152:155], v[58:61]
	v_mfma_f32_16x16x32_bf16 v[54:57], v[210:213], v[160:163], v[54:57]
	v_mfma_f32_16x16x32_bf16 v[50:53], v[218:221], v[160:163], v[50:53]
	v_mfma_f32_16x16x32_bf16 v[46:49], v[210:213], v[168:171], v[46:49]
	v_mfma_f32_16x16x32_bf16 v[42:45], v[218:221], v[168:171], v[42:45]
	v_mfma_f32_16x16x32_bf16 v[38:41], v[210:213], v[176:179], v[38:41]
	v_mfma_f32_16x16x32_bf16 v[34:37], v[218:221], v[176:179], v[34:37]
	s_setprio 0
	s_mov_b32 m0, s63
	v_lshl_add_u64 v[194:195], v[234:235], 0, s[34:35]
	s_barrier
	ds_read_b128 v[148:151], v199 offset:49152
	ds_read_b128 v[152:155], v199 offset:50176
	ds_read_b128 v[156:159], v199 offset:51200
	ds_read_b128 v[160:163], v199 offset:52224
	ds_read_b128 v[164:167], v199 offset:53248
	ds_read_b128 v[168:171], v199 offset:54272
	ds_read_b128 v[172:175], v199 offset:55296
	ds_read_b128 v[176:179], v199 offset:56320
	global_load_lds_dwordx4 v[194:195], off
	v_lshl_add_u64 v[194:195], v[238:239], 0, s[34:35]
	s_mov_b32 m0, s71
	s_nop 0
	global_load_lds_dwordx4 v[194:195], off
	s_barrier
	s_waitcnt lgkmcnt(0)
	s_setprio 1
	s_waitcnt lgkmcnt(0)
	v_mfma_f32_16x16x32_bf16 v[102:105], v[74:77], v[148:151], v[102:105]
	v_mfma_f32_16x16x32_bf16 v[98:101], v[138:141], v[148:151], v[98:101]
	v_mfma_f32_16x16x32_bf16 v[94:97], v[74:77], v[156:159], v[94:97]
	v_mfma_f32_16x16x32_bf16 v[90:93], v[138:141], v[156:159], v[90:93]
	v_mfma_f32_16x16x32_bf16 v[86:89], v[74:77], v[164:167], v[86:89]
	v_mfma_f32_16x16x32_bf16 v[82:85], v[138:141], v[164:167], v[82:85]
	v_mfma_f32_16x16x32_bf16 v[70:73], v[74:77], v[172:175], v[70:73]
	v_mfma_f32_16x16x32_bf16 v[66:69], v[138:141], v[172:175], v[66:69]
	v_mfma_f32_16x16x32_bf16 v[102:105], v[78:81], v[152:155], v[102:105]
	v_mfma_f32_16x16x32_bf16 v[98:101], v[142:145], v[152:155], v[98:101]
	v_mfma_f32_16x16x32_bf16 v[94:97], v[78:81], v[160:163], v[94:97]
	v_mfma_f32_16x16x32_bf16 v[90:93], v[142:145], v[160:163], v[90:93]
	v_mfma_f32_16x16x32_bf16 v[86:89], v[78:81], v[168:171], v[86:89]
	v_mfma_f32_16x16x32_bf16 v[82:85], v[142:145], v[168:171], v[82:85]
	v_mfma_f32_16x16x32_bf16 v[70:73], v[78:81], v[176:179], v[70:73]
	v_mfma_f32_16x16x32_bf16 v[66:69], v[142:145], v[176:179], v[66:69]
	s_setprio 0
	s_barrier
	s_add_u32 s8, s8, 0x40080
	s_addc_u32 s9, s9, 0
	s_add_i32 s22, s23, s40
	s_mov_b32 m0, s22
	s_nop 0
	global_load_lds_dwordx4 v146, s[8:9]
	s_add_i32 m0, s22, 0x2000
	s_nop 0
	global_load_lds_dwordx4 v188, s[8:9]
	s_waitcnt vmcnt(6)
	s_barrier
	s_setprio 1
	v_mfma_f32_16x16x32_bf16 v[30:33], v[206:209], v[148:151], v[30:33]
	v_mfma_f32_16x16x32_bf16 v[26:29], v[214:217], v[148:151], v[26:29]
	v_mfma_f32_16x16x32_bf16 v[22:25], v[206:209], v[156:159], v[22:25]
	v_mfma_f32_16x16x32_bf16 v[18:21], v[214:217], v[156:159], v[18:21]
	v_mfma_f32_16x16x32_bf16 v[14:17], v[206:209], v[164:167], v[14:17]
	v_mfma_f32_16x16x32_bf16 v[10:13], v[214:217], v[164:167], v[10:13]
	v_mfma_f32_16x16x32_bf16 v[6:9], v[206:209], v[172:175], v[6:9]
	v_mfma_f32_16x16x32_bf16 v[2:5], v[214:217], v[172:175], v[2:5]
	v_mfma_f32_16x16x32_bf16 v[30:33], v[210:213], v[152:155], v[30:33]
	v_mfma_f32_16x16x32_bf16 v[26:29], v[218:221], v[152:155], v[26:29]
	v_mfma_f32_16x16x32_bf16 v[22:25], v[210:213], v[160:163], v[22:25]
	v_mfma_f32_16x16x32_bf16 v[18:21], v[218:221], v[160:163], v[18:21]
	v_mfma_f32_16x16x32_bf16 v[14:17], v[210:213], v[168:171], v[14:17]
	v_mfma_f32_16x16x32_bf16 v[10:13], v[218:221], v[168:171], v[10:13]
	v_mfma_f32_16x16x32_bf16 v[6:9], v[210:213], v[176:179], v[6:9]
	v_mfma_f32_16x16x32_bf16 v[2:5], v[218:221], v[176:179], v[2:5]
	s_setprio 0
	s_add_i32 s28, s28, 2
	s_cmp_gt_u32 s28, 13
	s_barrier
	s_cbranch_scc1 .LBB0_1739
	s_mov_b64 s[8:9], s[18:19]
	s_branch .LBB0_1753

; #define G_STAGE2(bufoff, gbase, v0, v1) do { \
;         __builtin_amdgcn_global_load_lds((const unsigned*)((const char*)(gbase) + (v0)), (LAS unsigned*)(lds + (bufoff) + ldsw), 16, 0, 0); \
;         __builtin_amdgcn_global_load_lds((const unsigned*)((const char*)(gbase) + (v1)), (LAS unsigned*)(lds + (bufoff) + ldsw + 8192), 16, 0, 0); } while (0)
; #define G_LDA(dst, b, h) do { _Pragma("unroll") for (int m = 0; m < 4; ++m) _Pragma("unroll") for (int k = 0; k < 2; ++k) dst[m][k] = *(const LAS bf16x8*)(lds + G_SA(b, h) + aoff + m * 2048 + k * 1024); } while (0)
; #define G_LDB(dst, b, h) do { _Pragma("unroll") for (int n = 0; n < 2; ++n) _Pragma("unroll") for (int k = 0; k < 2; ++k) dst[n][k] = *(const LAS bf16x8*)(lds + G_SB(b, h) + boff + n * 2048 + k * 1024); } while (0)
; #define G_MMA(ai, bj, At, Bt) do { __builtin_amdgcn_s_setprio(1); _Pragma("unroll") for (int m = 0; m < 4; ++m) _Pragma("unroll") for (int n = 0; n < 2; ++n) _Pragma("unroll") for (int k = 0; k < 2; ++k) \
;         acc[ai][bj][m][n] = __builtin_amdgcn_mfma_f32_16x16x32_bf16(Bt[n][k], At[m][k], acc[ai][bj][m][n], 0, 0, 0); __builtin_amdgcn_s_setprio(0); } while (0)
; template <bool PERM, class Epi, class Sched>
; __device__ __forceinline__ void gemm_phase(LAS unsigned char* lds, const Sched& S, const Epi& E) {
;     ...
;             const char* a1 = cA + (size_t)(t + 1) * kstep;
;             G_LDB(B0, 0, 0); G_SCHED; G_LDA(At, 0, 0); G_STAGE2(G_SA(1, 1), a1, va10, va11);
;             const char* a2 = last ? nA : cA + (size_t)(t + 2) * kstep; const char* b2 = last ? nB : cB + (size_t)(t + 2) * kstep;
;             if (last) {
;                 if (Sched::GATHER_A) { va00 = na00; va01 = na01; va10 = na10; va11 = na11; vb0 = nb0; vb1 = nb1; hsB = nhsB; }
;                 else if (has_next) G_OFFS(nxt, va00, va01, va10, va11, vb0, vb1, hsB);
;             }
;             const char* a3 = a2 + kstep; const char* b3 = b2 + kstep;
;             G_WAIT_L(8); G_BAR; G_WAIT_L(0); G_MMA(0, 0, At, B0); G_BAR; G_SCHED;
;             G_LDB(B1, 0, 1); G_STAGE2(G_SB(0, 0), b2, vb0, vb1);
;             G_BAR; G_WAIT_L(0); G_MMA(0, 1, At, B1); G_BAR;
;             G_LDA(At, 0, 1); G_STAGE2(G_SA(0, 0), a2, va00, va01);
;             G_BAR; G_WAIT_L(0); G_MMA(1, 0, At, B0); G_BAR; G_SCHED;
;             G_STAGE2(G_SB(0, 1), b2 + hsB, vb0, vb1);
;             G_WAIT_V(6); G_BAR; G_MMA(1, 1, At, B1); G_BAR;
.LBB0_1797:
	s_add_u32 s18, s28, 0x80
	s_addc_u32 s19, s29, 0
	s_and_b64 s[8:9], s[8:9], exec
	s_cselect_b32 s19, s61, s19
	s_cselect_b32 s18, s60, s18
	s_cselect_b32 s9, s55, s23
	s_cselect_b32 s8, s54, s22
	s_waitcnt lgkmcnt(8)
	s_barrier
	s_waitcnt lgkmcnt(0)
	s_setprio 1
	s_waitcnt lgkmcnt(0)
	v_mfma_f32_16x16x32_bf16 v[134:137], v[122:125], v[172:175], v[134:137]
	v_mfma_f32_16x16x32_bf16 v[130:133], v[138:141], v[172:175], v[130:133]
	v_mfma_f32_16x16x32_bf16 v[118:121], v[122:125], v[164:167], v[118:121]
	v_mfma_f32_16x16x32_bf16 v[114:117], v[138:141], v[164:167], v[114:117]
	v_mfma_f32_16x16x32_bf16 v[110:113], v[122:125], v[156:159], v[110:113]
	v_mfma_f32_16x16x32_bf16 v[106:109], v[138:141], v[156:159], v[106:109]
	v_mfma_f32_16x16x32_bf16 v[102:105], v[122:125], v[148:151], v[102:105]
	v_mfma_f32_16x16x32_bf16 v[98:101], v[138:141], v[148:151], v[98:101]
	v_mfma_f32_16x16x32_bf16 v[134:137], v[126:129], v[176:179], v[134:137]
	v_mfma_f32_16x16x32_bf16 v[130:133], v[142:145], v[176:179], v[130:133]
	v_mfma_f32_16x16x32_bf16 v[118:121], v[126:129], v[168:171], v[118:121]
	v_mfma_f32_16x16x32_bf16 v[114:117], v[142:145], v[168:171], v[114:117]
	v_mfma_f32_16x16x32_bf16 v[110:113], v[126:129], v[160:163], v[110:113]
	v_mfma_f32_16x16x32_bf16 v[106:109], v[142:145], v[160:163], v[106:109]
	v_mfma_f32_16x16x32_bf16 v[102:105], v[126:129], v[152:155], v[102:105]
	v_mfma_f32_16x16x32_bf16 v[98:101], v[142:145], v[152:155], v[98:101]
	s_setprio 0
	s_barrier
	s_add_i32 s25, 0, 0x14000
	s_mov_b32 m0, s82
	v_add_u32_e32 v181, s25, v1
	ds_read_b128 v[206:209], v181
	ds_read_b128 v[210:213], v181 offset:1024
	ds_read_b128 v[214:217], v181 offset:2048
	ds_read_b128 v[218:221], v181 offset:3072
	global_load_lds_dwordx4 v146, s[8:9]
	s_mov_b32 m0, s83
	v_mov_b32_e32 v189, v147
	global_load_lds_dwordx4 v188, s[8:9]
	v_lshl_add_u64 v[222:223], s[8:9], 0, v[146:147]
	v_lshl_add_u64 v[224:225], s[8:9], 0, v[188:189]
	s_barrier
	s_waitcnt lgkmcnt(0)
	s_setprio 1
	s_waitcnt lgkmcnt(0)
	v_mfma_f32_16x16x32_bf16 v[62:65], v[206:209], v[172:175], v[62:65]
	v_mfma_f32_16x16x32_bf16 v[58:61], v[214:217], v[172:175], v[58:61]
	v_mfma_f32_16x16x32_bf16 v[54:57], v[206:209], v[164:167], v[54:57]
	v_mfma_f32_16x16x32_bf16 v[50:53], v[214:217], v[164:167], v[50:53]
	v_mfma_f32_16x16x32_bf16 v[46:49], v[206:209], v[156:159], v[46:49]
	v_mfma_f32_16x16x32_bf16 v[42:45], v[214:217], v[156:159], v[42:45]
	v_mfma_f32_16x16x32_bf16 v[38:41], v[206:209], v[148:151], v[38:41]
	v_mfma_f32_16x16x32_bf16 v[34:37], v[214:217], v[148:151], v[34:37]
	v_mfma_f32_16x16x32_bf16 v[62:65], v[210:213], v[176:179], v[62:65]
	v_mfma_f32_16x16x32_bf16 v[58:61], v[218:221], v[176:179], v[58:61]
	v_mfma_f32_16x16x32_bf16 v[54:57], v[210:213], v[168:171], v[54:57]
	v_mfma_f32_16x16x32_bf16 v[50:53], v[218:221], v[168:171], v[50:53]
	v_mfma_f32_16x16x32_bf16 v[46:49], v[210:213], v[160:163], v[46:49]
	v_mfma_f32_16x16x32_bf16 v[42:45], v[218:221], v[160:163], v[42:45]
	v_mfma_f32_16x16x32_bf16 v[38:41], v[210:213], v[152:155], v[38:41]
	v_mfma_f32_16x16x32_bf16 v[34:37], v[218:221], v[152:155], v[34:37]
	s_setprio 0
	s_mov_b32 m0, s81
	s_barrier
	ds_read_b128 v[148:151], v199 offset:16384
	ds_read_b128 v[152:155], v199 offset:17408
	ds_read_b128 v[156:159], v199 offset:18432
	ds_read_b128 v[160:163], v199 offset:19456
	ds_read_b128 v[164:167], v199 offset:20480
	ds_read_b128 v[168:171], v199 offset:21504
	ds_read_b128 v[172:175], v199 offset:22528
	ds_read_b128 v[176:179], v199 offset:23552
	global_load_lds_dwordx4 v180, s[18:19]
	s_mov_b32 m0, s84
	v_mov_b32_e32 v181, v147
	global_load_lds_dwordx4 v186, s[18:19]
	v_mov_b32_e32 v187, v147
	v_lshl_add_u64 v[234:235], s[18:19], 0, v[180:181]
	v_lshl_add_u64 v[238:239], s[18:19], 0, v[186:187]
	s_barrier
	s_waitcnt lgkmcnt(0)
	s_setprio 1
	s_waitcnt lgkmcnt(0)
	v_mfma_f32_16x16x32_bf16 v[94:97], v[122:125], v[148:151], v[94:97]
	v_mfma_f32_16x16x32_bf16 v[90:93], v[138:141], v[148:151], v[90:93]
	v_mfma_f32_16x16x32_bf16 v[86:89], v[122:125], v[156:159], v[86:89]
	v_mfma_f32_16x16x32_bf16 v[82:85], v[138:141], v[156:159], v[82:85]
	v_mfma_f32_16x16x32_bf16 v[78:81], v[122:125], v[164:167], v[78:81]
	v_mfma_f32_16x16x32_bf16 v[74:77], v[138:141], v[164:167], v[74:77]
	v_mfma_f32_16x16x32_bf16 v[70:73], v[122:125], v[172:175], v[70:73]
	v_mfma_f32_16x16x32_bf16 v[66:69], v[138:141], v[172:175], v[66:69]
	v_mfma_f32_16x16x32_bf16 v[94:97], v[126:129], v[152:155], v[94:97]
	v_mfma_f32_16x16x32_bf16 v[90:93], v[142:145], v[152:155], v[90:93]
	v_mfma_f32_16x16x32_bf16 v[86:89], v[126:129], v[160:163], v[86:89]
	v_mfma_f32_16x16x32_bf16 v[82:85], v[142:145], v[160:163], v[82:85]
	v_mfma_f32_16x16x32_bf16 v[78:81], v[126:129], v[168:171], v[78:81]
	v_mfma_f32_16x16x32_bf16 v[74:77], v[142:145], v[168:171], v[74:77]
	v_mfma_f32_16x16x32_bf16 v[70:73], v[126:129], v[176:179], v[70:73]
	v_mfma_f32_16x16x32_bf16 v[66:69], v[142:145], v[176:179], v[66:69]
	s_setprio 0
	s_barrier
	s_add_u32 vcc_lo, s8, 0x40000
	s_addc_u32 vcc_hi, s9, 0
	s_add_i32 s25, s25, s80
	s_mov_b32 m0, s25
	s_nop 0
	global_load_lds_dwordx4 v146, vcc
	s_add_i32 m0, s25, 0x2000
	s_nop 0
	global_load_lds_dwordx4 v188, vcc
	s_waitcnt vmcnt(6)
	s_barrier
; #define G_STAGE2(bufoff, gbase, v0, v1) do { \
;         __builtin_amdgcn_global_load_lds((const unsigned*)((const char*)(gbase) + (v0)), (LAS unsigned*)(lds + (bufoff) + ldsw), 16, 0, 0); \
;         __builtin_amdgcn_global_load_lds((const unsigned*)((const char*)(gbase) + (v1)), (LAS unsigned*)(lds + (bufoff) + ldsw + 8192), 16, 0, 0); } while (0)
; #define G_LDA(dst, b, h) do { _Pragma("unroll") for (int m = 0; m < 4; ++m) _Pragma("unroll") for (int k = 0; k < 2; ++k) dst[m][k] = *(const LAS bf16x8*)(lds + G_SA(b, h) + aoff + m * 2048 + k * 1024); } while (0)
; #define G_LDB(dst, b, h) do { _Pragma("unroll") for (int n = 0; n < 2; ++n) _Pragma("unroll") for (int k = 0; k < 2; ++k) dst[n][k] = *(const LAS bf16x8*)(lds + G_SB(b, h) + boff + n * 2048 + k * 1024); } while (0)
; #define G_MMA(ai, bj, At, Bt) do { __builtin_amdgcn_s_setprio(1); _Pragma("unroll") for (int m = 0; m < 4; ++m) _Pragma("unroll") for (int n = 0; n < 2; ++n) _Pragma("unroll") for (int k = 0; k < 2; ++k) \
;         acc[ai][bj][m][n] = __builtin_amdgcn_mfma_f32_16x16x32_bf16(Bt[n][k], At[m][k], acc[ai][bj][m][n], 0, 0, 0); __builtin_amdgcn_s_setprio(0); } while (0)
; #define G_WAIT_V(n) asm volatile("s_waitcnt vmcnt(" #n ")" ::: "memory")
; #define G_WAIT_L(n) asm volatile("s_waitcnt lgkmcnt(" #n ")" ::: "memory")
; #define G_BAR __builtin_amdgcn_s_barrier()
; #define G_SCHED __builtin_amdgcn_sched_barrier(0)
; template <bool PERM, class Epi, class Sched>
; __device__ __forceinline__ void gemm_phase(LAS unsigned char* lds, const Sched& S, const Epi& E) {
;     ...
;             G_WAIT_V(6); G_BAR; G_MMA(1, 1, At, B1); G_BAR;
;             G_LDB(B0, 1, 0); G_SCHED; G_LDA(At, 1, 0); G_STAGE2(G_SA(0, 1), a2, va10, va11);
;             G_WAIT_L(8); G_BAR; G_WAIT_L(0); G_MMA(0, 0, At, B0); G_BAR; G_SCHED;
;             G_LDB(B1, 1, 1); G_STAGE2(G_SB(1, 0), b3, vb0, vb1);
;             G_BAR; G_WAIT_L(0); G_MMA(0, 1, At, B1); G_BAR;
	s_setprio 1
	v_mfma_f32_16x16x32_bf16 v[30:33], v[206:209], v[148:151], v[30:33]
	v_mfma_f32_16x16x32_bf16 v[26:29], v[214:217], v[148:151], v[26:29]
	v_mfma_f32_16x16x32_bf16 v[22:25], v[206:209], v[156:159], v[22:25]
	v_mfma_f32_16x16x32_bf16 v[18:21], v[214:217], v[156:159], v[18:21]
	v_mfma_f32_16x16x32_bf16 v[14:17], v[206:209], v[164:167], v[14:17]
	v_mfma_f32_16x16x32_bf16 v[10:13], v[214:217], v[164:167], v[10:13]
	v_mfma_f32_16x16x32_bf16 v[6:9], v[206:209], v[172:175], v[6:9]
	v_mfma_f32_16x16x32_bf16 v[2:5], v[214:217], v[172:175], v[2:5]
	v_mfma_f32_16x16x32_bf16 v[30:33], v[210:213], v[152:155], v[30:33]
	v_mfma_f32_16x16x32_bf16 v[26:29], v[218:221], v[152:155], v[26:29]
	v_mfma_f32_16x16x32_bf16 v[22:25], v[210:213], v[160:163], v[22:25]
	v_mfma_f32_16x16x32_bf16 v[18:21], v[218:221], v[160:163], v[18:21]
	v_mfma_f32_16x16x32_bf16 v[14:17], v[210:213], v[168:171], v[14:17]
	v_mfma_f32_16x16x32_bf16 v[10:13], v[218:221], v[168:171], v[10:13]
	v_mfma_f32_16x16x32_bf16 v[6:9], v[210:213], v[176:179], v[6:9]
	v_mfma_f32_16x16x32_bf16 v[2:5], v[218:221], v[176:179], v[2:5]
	s_setprio 0
	s_add_i32 s25, 0, 0x18000
	v_add_u32_e32 v142, s25, v1
	s_barrier
	ds_read_b128 v[122:125], v142
	ds_read_b128 v[126:129], v142 offset:1024
	ds_read_b128 v[138:141], v142 offset:2048
	ds_read_b128 v[142:145], v142 offset:3072
	s_mov_b32 m0, s85
	v_lshl_add_u64 v[200:201], s[18:19], 0, v[200:201]
	ds_read_b128 v[148:151], v199 offset:32768
	ds_read_b128 v[152:155], v199 offset:33792
	ds_read_b128 v[156:159], v199 offset:34816
	ds_read_b128 v[160:163], v199 offset:35840
	ds_read_b128 v[164:167], v199 offset:36864
	ds_read_b128 v[168:171], v199 offset:37888
	ds_read_b128 v[172:175], v199 offset:38912
	ds_read_b128 v[176:179], v199 offset:39936
	global_load_lds_dwordx4 v[200:201], off
	v_lshl_add_u64 v[194:195], s[18:19], 0, v[194:195]
	s_mov_b32 m0, s86
	s_nop 0
	global_load_lds_dwordx4 v[194:195], off
	s_waitcnt lgkmcnt(8)
	s_barrier
	s_waitcnt lgkmcnt(0)
	s_setprio 1
	s_waitcnt lgkmcnt(0)
	v_mfma_f32_16x16x32_bf16 v[134:137], v[122:125], v[148:151], v[134:137]
	v_mfma_f32_16x16x32_bf16 v[130:133], v[138:141], v[148:151], v[130:133]
	v_mfma_f32_16x16x32_bf16 v[118:121], v[122:125], v[156:159], v[118:121]
	v_mfma_f32_16x16x32_bf16 v[114:117], v[138:141], v[156:159], v[114:117]
	v_mfma_f32_16x16x32_bf16 v[110:113], v[122:125], v[164:167], v[110:113]
	v_mfma_f32_16x16x32_bf16 v[106:109], v[138:141], v[164:167], v[106:109]
	v_mfma_f32_16x16x32_bf16 v[102:105], v[122:125], v[172:175], v[102:105]
	v_mfma_f32_16x16x32_bf16 v[98:101], v[138:141], v[172:175], v[98:101]
	v_mfma_f32_16x16x32_bf16 v[134:137], v[126:129], v[152:155], v[134:137]
	v_mfma_f32_16x16x32_bf16 v[130:133], v[142:145], v[152:155], v[130:133]
	v_mfma_f32_16x16x32_bf16 v[118:121], v[126:129], v[160:163], v[118:121]
	v_mfma_f32_16x16x32_bf16 v[114:117], v[142:145], v[160:163], v[114:117]
	v_mfma_f32_16x16x32_bf16 v[110:113], v[126:129], v[168:171], v[110:113]
	v_mfma_f32_16x16x32_bf16 v[106:109], v[142:145], v[168:171], v[106:109]
	v_mfma_f32_16x16x32_bf16 v[102:105], v[126:129], v[176:179], v[102:105]
	v_mfma_f32_16x16x32_bf16 v[98:101], v[142:145], v[176:179], v[98:101]
	s_setprio 0
	s_barrier
	s_add_i32 s18, 0, 0x1c000
	s_add_i32 s19, s25, s80
	v_add_u32_e32 v181, s18, v1
	v_lshl_add_u64 v[194:195], v[222:223], 0, s[34:35]
	s_mov_b32 m0, s19
	ds_read_b128 v[206:209], v181
	ds_read_b128 v[210:213], v181 offset:1024
	ds_read_b128 v[214:217], v181 offset:2048
	ds_read_b128 v[218:221], v181 offset:3072
	global_load_lds_dwordx4 v[194:195], off
	v_lshl_add_u64 v[194:195], v[224:225], 0, s[34:35]
	s_add_i32 m0, s19, 0x2000
	s_nop 0
	global_load_lds_dwordx4 v[194:195], off
	s_barrier
; #define G_STAGE2(bufoff, gbase, v0, v1) do { \
;         __builtin_amdgcn_global_load_lds((const unsigned*)((const char*)(gbase) + (v0)), (LAS unsigned*)(lds + (bufoff) + ldsw), 16, 0, 0); \
;         __builtin_amdgcn_global_load_lds((const unsigned*)((const char*)(gbase) + (v1)), (LAS unsigned*)(lds + (bufoff) + ldsw + 8192), 16, 0, 0); } while (0)
; #define G_LDA(dst, b, h) do { _Pragma("unroll") for (int m = 0; m < 4; ++m) _Pragma("unroll") for (int k = 0; k < 2; ++k) dst[m][k] = *(const LAS bf16x8*)(lds + G_SA(b, h) + aoff + m * 2048 + k * 1024); } while (0)
; #define G_MMA(ai, bj, At, Bt) do { __builtin_amdgcn_s_setprio(1); _Pragma("unroll") for (int m = 0; m < 4; ++m) _Pragma("unroll") for (int n = 0; n < 2; ++n) _Pragma("unroll") for (int k = 0; k < 2; ++k) \
;         acc[ai][bj][m][n] = __builtin_amdgcn_mfma_f32_16x16x32_bf16(Bt[n][k], At[m][k], acc[ai][bj][m][n], 0, 0, 0); __builtin_amdgcn_s_setprio(0); } while (0)
; #define G_WAIT_V(n) asm volatile("s_waitcnt vmcnt(" #n ")" ::: "memory")
; #define G_WAIT_L(n) asm volatile("s_waitcnt lgkmcnt(" #n ")" ::: "memory")
; #define G_BAR __builtin_amdgcn_s_barrier()
; #define G_SCHED __builtin_amdgcn_sched_barrier(0)
; template <bool PERM, class Epi, class Sched>
; __device__ __forceinline__ void gemm_phase(LAS unsigned char* lds, const Sched& S, const Epi& E) {
;     ...
;             G_BAR; G_WAIT_L(0); G_MMA(0, 1, At, B1); G_BAR;
;             G_LDA(At, 1, 1); G_STAGE2(G_SA(1, 0), a3, va00, va01);
;             G_BAR; G_WAIT_L(0); G_MMA(1, 0, At, B0); G_BAR; G_SCHED;
;             G_STAGE2(G_SB(1, 1), b3 + hsB, vb0, vb1);
;             G_WAIT_V(6); G_BAR; G_MMA(1, 1, At, B1); G_BAR;
	s_waitcnt lgkmcnt(0)
	s_setprio 1
	s_waitcnt lgkmcnt(0)
	v_mfma_f32_16x16x32_bf16 v[62:65], v[206:209], v[148:151], v[62:65]
	v_mfma_f32_16x16x32_bf16 v[58:61], v[214:217], v[148:151], v[58:61]
	v_mfma_f32_16x16x32_bf16 v[54:57], v[206:209], v[156:159], v[54:57]
	v_mfma_f32_16x16x32_bf16 v[50:53], v[214:217], v[156:159], v[50:53]
	v_mfma_f32_16x16x32_bf16 v[46:49], v[206:209], v[164:167], v[46:49]
	v_mfma_f32_16x16x32_bf16 v[42:45], v[214:217], v[164:167], v[42:45]
	v_mfma_f32_16x16x32_bf16 v[38:41], v[206:209], v[172:175], v[38:41]
	v_mfma_f32_16x16x32_bf16 v[34:37], v[214:217], v[172:175], v[34:37]
	v_mfma_f32_16x16x32_bf16 v[62:65], v[210:213], v[152:155], v[62:65]
	v_mfma_f32_16x16x32_bf16 v[58:61], v[218:221], v[152:155], v[58:61]
	v_mfma_f32_16x16x32_bf16 v[54:57], v[210:213], v[160:163], v[54:57]
	v_mfma_f32_16x16x32_bf16 v[50:53], v[218:221], v[160:163], v[50:53]
	v_mfma_f32_16x16x32_bf16 v[46:49], v[210:213], v[168:171], v[46:49]
	v_mfma_f32_16x16x32_bf16 v[42:45], v[218:221], v[168:171], v[42:45]
	v_mfma_f32_16x16x32_bf16 v[38:41], v[210:213], v[176:179], v[38:41]
	v_mfma_f32_16x16x32_bf16 v[34:37], v[218:221], v[176:179], v[34:37]
	s_setprio 0
	s_mov_b32 m0, s89
	v_lshl_add_u64 v[194:195], v[234:235], 0, s[34:35]
	s_barrier
	ds_read_b128 v[148:151], v199 offset:49152
	ds_read_b128 v[152:155], v199 offset:50176
	ds_read_b128 v[156:159], v199 offset:51200
	ds_read_b128 v[160:163], v199 offset:52224
	ds_read_b128 v[164:167], v199 offset:53248
	ds_read_b128 v[168:171], v199 offset:54272
	ds_read_b128 v[172:175], v199 offset:55296
	ds_read_b128 v[176:179], v199 offset:56320
	global_load_lds_dwordx4 v[194:195], off
	v_lshl_add_u64 v[194:195], v[238:239], 0, s[34:35]
	s_mov_b32 m0, s90
	s_nop 0
	global_load_lds_dwordx4 v[194:195], off
	s_barrier
	s_waitcnt lgkmcnt(0)
	s_setprio 1
	s_waitcnt lgkmcnt(0)
	v_mfma_f32_16x16x32_bf16 v[94:97], v[122:125], v[148:151], v[94:97]
	v_mfma_f32_16x16x32_bf16 v[90:93], v[138:141], v[148:151], v[90:93]
	v_mfma_f32_16x16x32_bf16 v[86:89], v[122:125], v[156:159], v[86:89]
	v_mfma_f32_16x16x32_bf16 v[82:85], v[138:141], v[156:159], v[82:85]
	v_mfma_f32_16x16x32_bf16 v[78:81], v[122:125], v[164:167], v[78:81]
	v_mfma_f32_16x16x32_bf16 v[74:77], v[138:141], v[164:167], v[74:77]
	v_mfma_f32_16x16x32_bf16 v[70:73], v[122:125], v[172:175], v[70:73]
	v_mfma_f32_16x16x32_bf16 v[66:69], v[138:141], v[172:175], v[66:69]
	v_mfma_f32_16x16x32_bf16 v[94:97], v[126:129], v[152:155], v[94:97]
	v_mfma_f32_16x16x32_bf16 v[90:93], v[142:145], v[152:155], v[90:93]
	v_mfma_f32_16x16x32_bf16 v[86:89], v[126:129], v[160:163], v[86:89]
	v_mfma_f32_16x16x32_bf16 v[82:85], v[142:145], v[160:163], v[82:85]
	v_mfma_f32_16x16x32_bf16 v[78:81], v[126:129], v[168:171], v[78:81]
	v_mfma_f32_16x16x32_bf16 v[74:77], v[142:145], v[168:171], v[74:77]
	v_mfma_f32_16x16x32_bf16 v[70:73], v[126:129], v[176:179], v[70:73]
	v_mfma_f32_16x16x32_bf16 v[66:69], v[142:145], v[176:179], v[66:69]
	s_setprio 0
	s_barrier
	s_add_u32 s8, s8, 0x40080
	s_addc_u32 s9, s9, 0
	s_add_i32 s18, s18, s80
	s_mov_b32 m0, s18
	s_nop 0
	global_load_lds_dwordx4 v146, s[8:9]
	s_add_i32 m0, s18, 0x2000
	s_nop 0
	global_load_lds_dwordx4 v188, s[8:9]
	s_waitcnt vmcnt(6)
	s_barrier
	s_setprio 1
	v_mfma_f32_16x16x32_bf16 v[30:33], v[206:209], v[148:151], v[30:33]
	v_mfma_f32_16x16x32_bf16 v[26:29], v[214:217], v[148:151], v[26:29]
	v_mfma_f32_16x16x32_bf16 v[22:25], v[206:209], v[156:159], v[22:25]
	v_mfma_f32_16x16x32_bf16 v[18:21], v[214:217], v[156:159], v[18:21]
	v_mfma_f32_16x16x32_bf16 v[14:17], v[206:209], v[164:167], v[14:17]
	v_mfma_f32_16x16x32_bf16 v[10:13], v[214:217], v[164:167], v[10:13]
	v_mfma_f32_16x16x32_bf16 v[6:9], v[206:209], v[172:175], v[6:9]
	v_mfma_f32_16x16x32_bf16 v[2:5], v[214:217], v[172:175], v[2:5]
	v_mfma_f32_16x16x32_bf16 v[30:33], v[210:213], v[152:155], v[30:33]
	v_mfma_f32_16x16x32_bf16 v[26:29], v[218:221], v[152:155], v[26:29]
	v_mfma_f32_16x16x32_bf16 v[22:25], v[210:213], v[160:163], v[22:25]
	v_mfma_f32_16x16x32_bf16 v[18:21], v[218:221], v[160:163], v[18:21]
	v_mfma_f32_16x16x32_bf16 v[14:17], v[210:213], v[168:171], v[14:17]
	v_mfma_f32_16x16x32_bf16 v[10:13], v[218:221], v[168:171], v[10:13]
	v_mfma_f32_16x16x32_bf16 v[6:9], v[210:213], v[176:179], v[6:9]
	v_mfma_f32_16x16x32_bf16 v[2:5], v[218:221], v[176:179], v[2:5]
	s_setprio 0
	s_add_i32 s24, s24, 2
	s_add_u32 s28, s28, 0x100
	s_addc_u32 s29, s29, 0
	s_add_u32 s22, s22, 0x100
	s_addc_u32 s23, s23, 0
	s_cmp_gt_u32 s24, 13
	s_barrier
	s_cbranch_scc1 .LBB0_1800

; #define G_STAGE2(bufoff, gbase, v0, v1) do { \
;         __builtin_amdgcn_global_load_lds((const unsigned*)((const char*)(gbase) + (v0)), (LAS unsigned*)(lds + (bufoff) + ldsw), 16, 0, 0); \
;         __builtin_amdgcn_global_load_lds((const unsigned*)((const char*)(gbase) + (v1)), (LAS unsigned*)(lds + (bufoff) + ldsw + 8192), 16, 0, 0); } while (0)
; #define G_WAIT_V(n) asm volatile("s_waitcnt vmcnt(" #n ")" ::: "memory")
; #define G_BAR __builtin_amdgcn_s_barrier()
; template <bool PERM, class Epi, class Sched>
; __device__ __forceinline__ void gemm_phase(LAS unsigned char* lds, const Sched& S, const Epi& E) {
;     ...
;         for (int t = 0; t < nt; t += 2) {
;             const bool last = (t == nt - 2);
;             const char* a1 = cA + (size_t)(t + 1) * kstep;
;             G_LDB(B0, 0, 0); G_SCHED; G_LDA(At, 0, 0); G_STAGE2(G_SA(1, 1), a1, va10, va11);
;             const char* a2 = last ? nA : cA + (size_t)(t + 2) * kstep; const char* b2 = last ? nB : cB + (size_t)(t + 2) * kstep;
;             if (last) {
;                 if (Sched::GATHER_A) { va00 = na00; va01 = na01; va10 = na10; va11 = na11; vb0 = nb0; vb1 = nb1; hsB = nhsB; }
;                 else if (has_next) G_OFFS(nxt, va00, va01, va10, va11, vb0, vb1, hsB);
;             }
;             const char* a3 = a2 + kstep; const char* b3 = b2 + kstep;
;             G_WAIT_L(8); G_BAR; G_WAIT_L(0); G_MMA(0, 0, At, B0); G_BAR; G_SCHED;
;             G_LDB(B1, 0, 1); G_STAGE2(G_SB(0, 0), b2, vb0, vb1);
;             G_BAR; G_WAIT_L(0); G_MMA(0, 1, At, B1); G_BAR;
;             G_LDA(At, 0, 1); G_STAGE2(G_SA(0, 0), a2, va00, va01);
;             G_BAR; G_WAIT_L(0); G_MMA(1, 0, At, B0); G_BAR; G_SCHED;
;             G_STAGE2(G_SB(0, 1), b2 + hsB, vb0, vb1);
;             G_WAIT_V(6); G_BAR; G_MMA(1, 1, At, B1); G_BAR;
;             G_LDB(B0, 1, 0); G_SCHED; G_LDA(At, 1, 0); G_STAGE2(G_SA(0, 1), a2, va10, va11);
;             G_WAIT_L(8); G_BAR; G_WAIT_L(0); G_MMA(0, 0, At, B0); G_BAR; G_SCHED;
;             G_LDB(B1, 1, 1); G_STAGE2(G_SB(1, 0), b3, vb0, vb1);
;             G_BAR; G_WAIT_L(0); G_MMA(0, 1, At, B1); G_BAR;
;             G_LDA(At, 1, 1); G_STAGE2(G_SA(1, 0), a3, va00, va01);
;             G_BAR; G_WAIT_L(0); G_MMA(1, 0, At, B0); G_BAR; G_SCHED;
;             G_STAGE2(G_SB(1, 1), b3 + hsB, vb0, vb1);
;             G_WAIT_V(6); G_BAR; G_MMA(1, 1, At, B1); G_BAR;
.LBB0_1853:
	s_add_u32 s18, s28, 0x80
	s_addc_u32 s19, s29, 0
	s_and_b64 s[8:9], s[8:9], exec
	v_mov_b32_e32 v185, v147
	v_mov_b32_e32 v187, v147
	s_cselect_b32 s19, s49, s19
	s_cselect_b32 s18, s48, s18
	s_cselect_b32 s9, s51, s83
	s_cselect_b32 s8, s50, s82
	s_waitcnt lgkmcnt(8)
	s_barrier
	s_waitcnt lgkmcnt(0)
	s_setprio 1
	s_waitcnt lgkmcnt(0)
	v_mfma_f32_16x16x32_bf16 v[126:129], v[130:133], v[172:175], v[126:129]
	v_mfma_f32_16x16x32_bf16 v[122:125], v[138:141], v[172:175], v[122:125]
	v_mfma_f32_16x16x32_bf16 v[118:121], v[130:133], v[164:167], v[118:121]
	v_mfma_f32_16x16x32_bf16 v[114:117], v[138:141], v[164:167], v[114:117]
	v_mfma_f32_16x16x32_bf16 v[110:113], v[130:133], v[156:159], v[110:113]
	v_mfma_f32_16x16x32_bf16 v[106:109], v[138:141], v[156:159], v[106:109]
	v_mfma_f32_16x16x32_bf16 v[102:105], v[130:133], v[148:151], v[102:105]
	v_mfma_f32_16x16x32_bf16 v[98:101], v[138:141], v[148:151], v[98:101]
	v_mfma_f32_16x16x32_bf16 v[126:129], v[134:137], v[176:179], v[126:129]
	v_mfma_f32_16x16x32_bf16 v[122:125], v[142:145], v[176:179], v[122:125]
	v_mfma_f32_16x16x32_bf16 v[118:121], v[134:137], v[168:171], v[118:121]
	v_mfma_f32_16x16x32_bf16 v[114:117], v[142:145], v[168:171], v[114:117]
	v_mfma_f32_16x16x32_bf16 v[110:113], v[134:137], v[160:163], v[110:113]
	v_mfma_f32_16x16x32_bf16 v[106:109], v[142:145], v[160:163], v[106:109]
	v_mfma_f32_16x16x32_bf16 v[102:105], v[134:137], v[152:155], v[102:105]
	v_mfma_f32_16x16x32_bf16 v[98:101], v[142:145], v[152:155], v[98:101]
	s_setprio 0
	s_barrier
	s_add_i32 s85, 0, 0x14000
	s_mov_b32 m0, s25
	v_add_u32_e32 v181, s85, v1
	ds_read_b128 v[200:203], v181
	ds_read_b128 v[204:207], v181 offset:1024
	ds_read_b128 v[208:211], v181 offset:2048
	ds_read_b128 v[212:215], v181 offset:3072
	global_load_lds_dwordx4 v146, s[8:9]
	s_mov_b32 m0, s30
	v_mov_b32_e32 v189, v147
	global_load_lds_dwordx4 v188, s[8:9]
	v_lshl_add_u64 v[190:191], s[8:9], 0, v[146:147]
	v_lshl_add_u64 v[194:195], s[8:9], 0, v[188:189]
	s_barrier
	s_waitcnt lgkmcnt(0)
	s_setprio 1
	s_waitcnt lgkmcnt(0)
	v_mfma_f32_16x16x32_bf16 v[62:65], v[200:203], v[172:175], v[62:65]
	v_mfma_f32_16x16x32_bf16 v[58:61], v[208:211], v[172:175], v[58:61]
	v_mfma_f32_16x16x32_bf16 v[54:57], v[200:203], v[164:167], v[54:57]
	v_mfma_f32_16x16x32_bf16 v[50:53], v[208:211], v[164:167], v[50:53]
	v_mfma_f32_16x16x32_bf16 v[46:49], v[200:203], v[156:159], v[46:49]
	v_mfma_f32_16x16x32_bf16 v[42:45], v[208:211], v[156:159], v[42:45]
	v_mfma_f32_16x16x32_bf16 v[38:41], v[200:203], v[148:151], v[38:41]
	v_mfma_f32_16x16x32_bf16 v[34:37], v[208:211], v[148:151], v[34:37]
	v_mfma_f32_16x16x32_bf16 v[62:65], v[204:207], v[176:179], v[62:65]
	v_mfma_f32_16x16x32_bf16 v[58:61], v[212:215], v[176:179], v[58:61]
	v_mfma_f32_16x16x32_bf16 v[54:57], v[204:207], v[168:171], v[54:57]
	v_mfma_f32_16x16x32_bf16 v[50:53], v[212:215], v[168:171], v[50:53]
	v_mfma_f32_16x16x32_bf16 v[46:49], v[204:207], v[160:163], v[46:49]
	v_mfma_f32_16x16x32_bf16 v[42:45], v[212:215], v[160:163], v[42:45]
	v_mfma_f32_16x16x32_bf16 v[38:41], v[204:207], v[152:155], v[38:41]
	v_mfma_f32_16x16x32_bf16 v[34:37], v[212:215], v[152:155], v[34:37]
	s_setprio 0
	s_mov_b32 m0, s24
	s_barrier
	ds_read_b128 v[148:151], v192 offset:16384
	ds_read_b128 v[152:155], v192 offset:17408
	ds_read_b128 v[156:159], v192 offset:18432
	ds_read_b128 v[160:163], v192 offset:19456
	ds_read_b128 v[164:167], v192 offset:20480
	ds_read_b128 v[168:171], v192 offset:21504
	ds_read_b128 v[172:175], v192 offset:22528
	ds_read_b128 v[176:179], v192 offset:23552
	global_load_lds_dwordx4 v180, s[18:19]
	s_mov_b32 m0, s31
	v_mov_b32_e32 v181, v147
	global_load_lds_dwordx4 v182, s[18:19]
	v_mov_b32_e32 v183, v147
	v_lshl_add_u64 v[216:217], s[18:19], 0, v[180:181]
	v_lshl_add_u64 v[218:219], s[18:19], 0, v[182:183]
	s_barrier
	s_waitcnt lgkmcnt(0)
	s_setprio 1
	s_waitcnt lgkmcnt(0)
	v_mfma_f32_16x16x32_bf16 v[94:97], v[130:133], v[148:151], v[94:97]
	v_mfma_f32_16x16x32_bf16 v[90:93], v[138:141], v[148:151], v[90:93]
	v_mfma_f32_16x16x32_bf16 v[86:89], v[130:133], v[156:159], v[86:89]
	v_mfma_f32_16x16x32_bf16 v[82:85], v[138:141], v[156:159], v[82:85]
	v_mfma_f32_16x16x32_bf16 v[78:81], v[130:133], v[164:167], v[78:81]
	v_mfma_f32_16x16x32_bf16 v[74:77], v[138:141], v[164:167], v[74:77]
	v_mfma_f32_16x16x32_bf16 v[70:73], v[130:133], v[172:175], v[70:73]
	v_mfma_f32_16x16x32_bf16 v[66:69], v[138:141], v[172:175], v[66:69]
	v_mfma_f32_16x16x32_bf16 v[94:97], v[134:137], v[152:155], v[94:97]
	v_mfma_f32_16x16x32_bf16 v[90:93], v[142:145], v[152:155], v[90:93]
	v_mfma_f32_16x16x32_bf16 v[86:89], v[134:137], v[160:163], v[86:89]
	v_mfma_f32_16x16x32_bf16 v[82:85], v[142:145], v[160:163], v[82:85]
	v_mfma_f32_16x16x32_bf16 v[78:81], v[134:137], v[168:171], v[78:81]
	v_mfma_f32_16x16x32_bf16 v[74:77], v[142:145], v[168:171], v[74:77]
	v_mfma_f32_16x16x32_bf16 v[70:73], v[134:137], v[176:179], v[70:73]
	v_mfma_f32_16x16x32_bf16 v[66:69], v[142:145], v[176:179], v[66:69]
	s_setprio 0
	s_barrier
	s_add_u32 s86, s8, 0x40000
	s_addc_u32 s87, s9, 0
	s_add_i32 s85, s85, s23
	s_mov_b32 m0, s85
	s_nop 0
	global_load_lds_dwordx4 v146, s[86:87]
	s_add_i32 m0, s85, 0x2000
	s_nop 0
	global_load_lds_dwordx4 v188, s[86:87]
	s_waitcnt vmcnt(6)
	s_barrier
; #define G_STAGE2(bufoff, gbase, v0, v1) do { \
;         __builtin_amdgcn_global_load_lds((const unsigned*)((const char*)(gbase) + (v0)), (LAS unsigned*)(lds + (bufoff) + ldsw), 16, 0, 0); \
;         __builtin_amdgcn_global_load_lds((const unsigned*)((const char*)(gbase) + (v1)), (LAS unsigned*)(lds + (bufoff) + ldsw + 8192), 16, 0, 0); } while (0)
; #define G_LDA(dst, b, h) do { _Pragma("unroll") for (int m = 0; m < 4; ++m) _Pragma("unroll") for (int k = 0; k < 2; ++k) dst[m][k] = *(const LAS bf16x8*)(lds + G_SA(b, h) + aoff + m * 2048 + k * 1024); } while (0)
; #define G_LDB(dst, b, h) do { _Pragma("unroll") for (int n = 0; n < 2; ++n) _Pragma("unroll") for (int k = 0; k < 2; ++k) dst[n][k] = *(const LAS bf16x8*)(lds + G_SB(b, h) + boff + n * 2048 + k * 1024); } while (0)
; #define G_MMA(ai, bj, At, Bt) do { __builtin_amdgcn_s_setprio(1); _Pragma("unroll") for (int m = 0; m < 4; ++m) _Pragma("unroll") for (int n = 0; n < 2; ++n) _Pragma("unroll") for (int k = 0; k < 2; ++k) \
;         acc[ai][bj][m][n] = __builtin_amdgcn_mfma_f32_16x16x32_bf16(Bt[n][k], At[m][k], acc[ai][bj][m][n], 0, 0, 0); __builtin_amdgcn_s_setprio(0); } while (0)
; #define G_WAIT_V(n) asm volatile("s_waitcnt vmcnt(" #n ")" ::: "memory")
; #define G_WAIT_L(n) asm volatile("s_waitcnt lgkmcnt(" #n ")" ::: "memory")
; template <bool PERM, class Epi, class Sched>
; __device__ __forceinline__ void gemm_phase(LAS unsigned char* lds, const Sched& S, const Epi& E) {
;     ...
;             G_WAIT_L(8); G_BAR; G_WAIT_L(0); G_MMA(0, 0, At, B0); G_BAR; G_SCHED;
;             G_LDB(B1, 0, 1); G_STAGE2(G_SB(0, 0), b2, vb0, vb1);
;             G_BAR; G_WAIT_L(0); G_MMA(0, 1, At, B1); G_BAR;
;             G_LDA(At, 0, 1); G_STAGE2(G_SA(0, 0), a2, va00, va01);
;             G_BAR; G_WAIT_L(0); G_MMA(1, 0, At, B0); G_BAR; G_SCHED;
;             G_STAGE2(G_SB(0, 1), b2 + hsB, vb0, vb1);
;             G_WAIT_V(6); G_BAR; G_MMA(1, 1, At, B1); G_BAR;
;             G_LDB(B0, 1, 0); G_SCHED; G_LDA(At, 1, 0); G_STAGE2(G_SA(0, 1), a2, va10, va11);
;             G_WAIT_L(8); G_BAR; G_WAIT_L(0); G_MMA(0, 0, At, B0); G_BAR; G_SCHED;
;             G_LDB(B1, 1, 1); G_STAGE2(G_SB(1, 0), b3, vb0, vb1);
;             G_BAR; G_WAIT_L(0); G_MMA(0, 1, At, B1); G_BAR;
;             G_LDA(At, 1, 1); G_STAGE2(G_SA(1, 0), a3, va00, va01);
;             G_BAR; G_WAIT_L(0); G_MMA(1, 0, At, B0); G_BAR; G_SCHED;
	s_setprio 1
	v_mfma_f32_16x16x32_bf16 v[30:33], v[200:203], v[148:151], v[30:33]
	v_mfma_f32_16x16x32_bf16 v[26:29], v[208:211], v[148:151], v[26:29]
	v_mfma_f32_16x16x32_bf16 v[22:25], v[200:203], v[156:159], v[22:25]
	v_mfma_f32_16x16x32_bf16 v[18:21], v[208:211], v[156:159], v[18:21]
	v_mfma_f32_16x16x32_bf16 v[14:17], v[200:203], v[164:167], v[14:17]
	v_mfma_f32_16x16x32_bf16 v[10:13], v[208:211], v[164:167], v[10:13]
	v_mfma_f32_16x16x32_bf16 v[6:9], v[200:203], v[172:175], v[6:9]
	v_mfma_f32_16x16x32_bf16 v[2:5], v[208:211], v[172:175], v[2:5]
	v_mfma_f32_16x16x32_bf16 v[30:33], v[204:207], v[152:155], v[30:33]
	v_mfma_f32_16x16x32_bf16 v[26:29], v[212:215], v[152:155], v[26:29]
	v_mfma_f32_16x16x32_bf16 v[22:25], v[204:207], v[160:163], v[22:25]
	v_mfma_f32_16x16x32_bf16 v[18:21], v[212:215], v[160:163], v[18:21]
	v_mfma_f32_16x16x32_bf16 v[14:17], v[204:207], v[168:171], v[14:17]
	v_mfma_f32_16x16x32_bf16 v[10:13], v[212:215], v[168:171], v[10:13]
	v_mfma_f32_16x16x32_bf16 v[6:9], v[204:207], v[176:179], v[6:9]
	v_mfma_f32_16x16x32_bf16 v[2:5], v[212:215], v[176:179], v[2:5]
	s_setprio 0
	s_add_i32 s85, 0, 0x18000
	v_add_u32_e32 v142, s85, v1
	s_barrier
	ds_read_b128 v[130:133], v142
	ds_read_b128 v[134:137], v142 offset:1024
	ds_read_b128 v[138:141], v142 offset:2048
	ds_read_b128 v[142:145], v142 offset:3072
	s_mov_b32 m0, s53
	v_lshl_add_u64 v[200:201], s[18:19], 0, v[184:185]
	ds_read_b128 v[148:151], v192 offset:32768
	ds_read_b128 v[152:155], v192 offset:33792
	ds_read_b128 v[156:159], v192 offset:34816
	ds_read_b128 v[160:163], v192 offset:35840
	ds_read_b128 v[164:167], v192 offset:36864
	ds_read_b128 v[168:171], v192 offset:37888
	ds_read_b128 v[172:175], v192 offset:38912
	ds_read_b128 v[176:179], v192 offset:39936
	global_load_lds_dwordx4 v[200:201], off
	v_lshl_add_u64 v[200:201], s[18:19], 0, v[186:187]
	s_mov_b32 m0, s54
	s_nop 0
	global_load_lds_dwordx4 v[200:201], off
	s_waitcnt lgkmcnt(8)
	s_barrier
	s_waitcnt lgkmcnt(0)
	s_setprio 1
	s_waitcnt lgkmcnt(0)
	v_mfma_f32_16x16x32_bf16 v[126:129], v[130:133], v[148:151], v[126:129]
	v_mfma_f32_16x16x32_bf16 v[122:125], v[138:141], v[148:151], v[122:125]
	v_mfma_f32_16x16x32_bf16 v[118:121], v[130:133], v[156:159], v[118:121]
	v_mfma_f32_16x16x32_bf16 v[114:117], v[138:141], v[156:159], v[114:117]
	v_mfma_f32_16x16x32_bf16 v[110:113], v[130:133], v[164:167], v[110:113]
	v_mfma_f32_16x16x32_bf16 v[106:109], v[138:141], v[164:167], v[106:109]
	v_mfma_f32_16x16x32_bf16 v[102:105], v[130:133], v[172:175], v[102:105]
	v_mfma_f32_16x16x32_bf16 v[98:101], v[138:141], v[172:175], v[98:101]
	v_mfma_f32_16x16x32_bf16 v[126:129], v[134:137], v[152:155], v[126:129]
	v_mfma_f32_16x16x32_bf16 v[122:125], v[142:145], v[152:155], v[122:125]
	v_mfma_f32_16x16x32_bf16 v[118:121], v[134:137], v[160:163], v[118:121]
	v_mfma_f32_16x16x32_bf16 v[114:117], v[142:145], v[160:163], v[114:117]
	v_mfma_f32_16x16x32_bf16 v[110:113], v[134:137], v[168:171], v[110:113]
	v_mfma_f32_16x16x32_bf16 v[106:109], v[142:145], v[168:171], v[106:109]
	v_mfma_f32_16x16x32_bf16 v[102:105], v[134:137], v[176:179], v[102:105]
	v_mfma_f32_16x16x32_bf16 v[98:101], v[142:145], v[176:179], v[98:101]
	s_setprio 0
	s_barrier
	s_add_i32 s18, 0, 0x1c000
	s_add_i32 s19, s85, s23
	v_add_u32_e32 v181, s18, v1
	v_lshl_add_u64 v[190:191], v[190:191], 0, s[34:35]
	s_mov_b32 m0, s19
	ds_read_b128 v[200:203], v181
	ds_read_b128 v[204:207], v181 offset:1024
	ds_read_b128 v[208:211], v181 offset:2048
	ds_read_b128 v[212:215], v181 offset:3072
	global_load_lds_dwordx4 v[190:191], off
	v_lshl_add_u64 v[190:191], v[194:195], 0, s[34:35]
	s_add_i32 m0, s19, 0x2000
	s_nop 0
	global_load_lds_dwordx4 v[190:191], off
	s_barrier
; #define G_STAGE2(bufoff, gbase, v0, v1) do { \
;         __builtin_amdgcn_global_load_lds((const unsigned*)((const char*)(gbase) + (v0)), (LAS unsigned*)(lds + (bufoff) + ldsw), 16, 0, 0); \
;         __builtin_amdgcn_global_load_lds((const unsigned*)((const char*)(gbase) + (v1)), (LAS unsigned*)(lds + (bufoff) + ldsw + 8192), 16, 0, 0); } while (0)
; #define G_LDA(dst, b, h) do { _Pragma("unroll") for (int m = 0; m < 4; ++m) _Pragma("unroll") for (int k = 0; k < 2; ++k) dst[m][k] = *(const LAS bf16x8*)(lds + G_SA(b, h) + aoff + m * 2048 + k * 1024); } while (0)
; #define G_LDB(dst, b, h) do { _Pragma("unroll") for (int n = 0; n < 2; ++n) _Pragma("unroll") for (int k = 0; k < 2; ++k) dst[n][k] = *(const LAS bf16x8*)(lds + G_SB(b, h) + boff + n * 2048 + k * 1024); } while (0)
; #define G_MMA(ai, bj, At, Bt) do { __builtin_amdgcn_s_setprio(1); _Pragma("unroll") for (int m = 0; m < 4; ++m) _Pragma("unroll") for (int n = 0; n < 2; ++n) _Pragma("unroll") for (int k = 0; k < 2; ++k) \
;         acc[ai][bj][m][n] = __builtin_amdgcn_mfma_f32_16x16x32_bf16(Bt[n][k], At[m][k], acc[ai][bj][m][n], 0, 0, 0); __builtin_amdgcn_s_setprio(0); } while (0)
; #define G_WAIT_V(n) asm volatile("s_waitcnt vmcnt(" #n ")" ::: "memory")
; #define G_WAIT_L(n) asm volatile("s_waitcnt lgkmcnt(" #n ")" ::: "memory")
; #define G_BAR __builtin_amdgcn_s_barrier()
; #define G_SCHED __builtin_amdgcn_sched_barrier(0)
; template <bool PERM, class Epi, class Sched>
; __device__ __forceinline__ void gemm_phase(LAS unsigned char* lds, const Sched& S, const Epi& E) {
;     ...
;             G_WAIT_L(8); G_BAR; G_WAIT_L(0); G_MMA(0, 0, At, B0); G_BAR; G_SCHED;
;             G_LDB(B1, 1, 1); G_STAGE2(G_SB(1, 0), b3, vb0, vb1);
;             G_BAR; G_WAIT_L(0); G_MMA(0, 1, At, B1); G_BAR;
;             G_LDA(At, 1, 1); G_STAGE2(G_SA(1, 0), a3, va00, va01);
;             G_BAR; G_WAIT_L(0); G_MMA(1, 0, At, B0); G_BAR; G_SCHED;
;             G_STAGE2(G_SB(1, 1), b3 + hsB, vb0, vb1);
;             G_WAIT_V(6); G_BAR; G_MMA(1, 1, At, B1); G_BAR;
;         }
	s_waitcnt lgkmcnt(0)
	s_setprio 1
	s_waitcnt lgkmcnt(0)
	v_mfma_f32_16x16x32_bf16 v[62:65], v[200:203], v[148:151], v[62:65]
	v_mfma_f32_16x16x32_bf16 v[58:61], v[208:211], v[148:151], v[58:61]
	v_mfma_f32_16x16x32_bf16 v[54:57], v[200:203], v[156:159], v[54:57]
	v_mfma_f32_16x16x32_bf16 v[50:53], v[208:211], v[156:159], v[50:53]
	v_mfma_f32_16x16x32_bf16 v[46:49], v[200:203], v[164:167], v[46:49]
	v_mfma_f32_16x16x32_bf16 v[42:45], v[208:211], v[164:167], v[42:45]
	v_mfma_f32_16x16x32_bf16 v[38:41], v[200:203], v[172:175], v[38:41]
	v_mfma_f32_16x16x32_bf16 v[34:37], v[208:211], v[172:175], v[34:37]
	v_mfma_f32_16x16x32_bf16 v[62:65], v[204:207], v[152:155], v[62:65]
	v_mfma_f32_16x16x32_bf16 v[58:61], v[212:215], v[152:155], v[58:61]
	v_mfma_f32_16x16x32_bf16 v[54:57], v[204:207], v[160:163], v[54:57]
	v_mfma_f32_16x16x32_bf16 v[50:53], v[212:215], v[160:163], v[50:53]
	v_mfma_f32_16x16x32_bf16 v[46:49], v[204:207], v[168:171], v[46:49]
	v_mfma_f32_16x16x32_bf16 v[42:45], v[212:215], v[168:171], v[42:45]
	v_mfma_f32_16x16x32_bf16 v[38:41], v[204:207], v[176:179], v[38:41]
	v_mfma_f32_16x16x32_bf16 v[34:37], v[212:215], v[176:179], v[34:37]
	s_setprio 0
	s_mov_b32 m0, s57
	v_lshl_add_u64 v[190:191], v[216:217], 0, s[34:35]
	s_barrier
	ds_read_b128 v[148:151], v192 offset:49152
	ds_read_b128 v[152:155], v192 offset:50176
	ds_read_b128 v[156:159], v192 offset:51200
	ds_read_b128 v[160:163], v192 offset:52224
	ds_read_b128 v[164:167], v192 offset:53248
	ds_read_b128 v[168:171], v192 offset:54272
	ds_read_b128 v[172:175], v192 offset:55296
	ds_read_b128 v[176:179], v192 offset:56320
	global_load_lds_dwordx4 v[190:191], off
	v_lshl_add_u64 v[190:191], v[218:219], 0, s[34:35]
	s_mov_b32 m0, s60
	s_nop 0
	global_load_lds_dwordx4 v[190:191], off
	s_barrier
	s_waitcnt lgkmcnt(0)
	s_setprio 1
	s_waitcnt lgkmcnt(0)
	v_mfma_f32_16x16x32_bf16 v[94:97], v[130:133], v[148:151], v[94:97]
	v_mfma_f32_16x16x32_bf16 v[90:93], v[138:141], v[148:151], v[90:93]
	v_mfma_f32_16x16x32_bf16 v[86:89], v[130:133], v[156:159], v[86:89]
	v_mfma_f32_16x16x32_bf16 v[82:85], v[138:141], v[156:159], v[82:85]
	v_mfma_f32_16x16x32_bf16 v[78:81], v[130:133], v[164:167], v[78:81]
	v_mfma_f32_16x16x32_bf16 v[74:77], v[138:141], v[164:167], v[74:77]
	v_mfma_f32_16x16x32_bf16 v[70:73], v[130:133], v[172:175], v[70:73]
	v_mfma_f32_16x16x32_bf16 v[66:69], v[138:141], v[172:175], v[66:69]
	v_mfma_f32_16x16x32_bf16 v[94:97], v[134:137], v[152:155], v[94:97]
	v_mfma_f32_16x16x32_bf16 v[90:93], v[142:145], v[152:155], v[90:93]
	v_mfma_f32_16x16x32_bf16 v[86:89], v[134:137], v[160:163], v[86:89]
	v_mfma_f32_16x16x32_bf16 v[82:85], v[142:145], v[160:163], v[82:85]
	v_mfma_f32_16x16x32_bf16 v[78:81], v[134:137], v[168:171], v[78:81]
	v_mfma_f32_16x16x32_bf16 v[74:77], v[142:145], v[168:171], v[74:77]
	v_mfma_f32_16x16x32_bf16 v[70:73], v[134:137], v[176:179], v[70:73]
	v_mfma_f32_16x16x32_bf16 v[66:69], v[142:145], v[176:179], v[66:69]
	s_setprio 0
	s_barrier
	s_add_u32 s8, s8, 0x40080
	s_addc_u32 s9, s9, 0
	s_add_i32 s18, s18, s23
	s_mov_b32 m0, s18
	s_nop 0
	global_load_lds_dwordx4 v146, s[8:9]
	s_add_i32 m0, s18, 0x2000
	s_nop 0
	global_load_lds_dwordx4 v188, s[8:9]
	s_waitcnt vmcnt(6)
	s_barrier
	s_setprio 1
	v_mfma_f32_16x16x32_bf16 v[30:33], v[200:203], v[148:151], v[30:33]
	v_mfma_f32_16x16x32_bf16 v[26:29], v[208:211], v[148:151], v[26:29]
	v_mfma_f32_16x16x32_bf16 v[22:25], v[200:203], v[156:159], v[22:25]
	v_mfma_f32_16x16x32_bf16 v[18:21], v[208:211], v[156:159], v[18:21]
	v_mfma_f32_16x16x32_bf16 v[14:17], v[200:203], v[164:167], v[14:17]
	v_mfma_f32_16x16x32_bf16 v[10:13], v[208:211], v[164:167], v[10:13]
	v_mfma_f32_16x16x32_bf16 v[6:9], v[200:203], v[172:175], v[6:9]
	v_mfma_f32_16x16x32_bf16 v[2:5], v[208:211], v[172:175], v[2:5]
	v_mfma_f32_16x16x32_bf16 v[30:33], v[204:207], v[152:155], v[30:33]
	v_mfma_f32_16x16x32_bf16 v[26:29], v[212:215], v[152:155], v[26:29]
	v_mfma_f32_16x16x32_bf16 v[22:25], v[204:207], v[160:163], v[22:25]
	v_mfma_f32_16x16x32_bf16 v[18:21], v[212:215], v[160:163], v[18:21]
	v_mfma_f32_16x16x32_bf16 v[14:17], v[204:207], v[168:171], v[14:17]
	v_mfma_f32_16x16x32_bf16 v[10:13], v[212:215], v[168:171], v[10:13]
	v_mfma_f32_16x16x32_bf16 v[6:9], v[204:207], v[176:179], v[6:9]
	v_mfma_f32_16x16x32_bf16 v[2:5], v[212:215], v[176:179], v[2:5]
	s_setprio 0
	s_add_i32 s84, s84, 2
	s_add_u32 s28, s28, 0x100
	s_addc_u32 s29, s29, 0
	s_add_u32 s82, s82, 0x100
	s_addc_u32 s83, s83, 0
	s_cmp_gt_u32 s84, 13
	s_barrier
	s_cbranch_scc1 .LBB0_1856
